# removed every s_setprio from the GEMM K-loops (plus the earlier wait/m0 trims)
# speedup vs baseline: 1.0063x; 1.0036x over previous
.LBB0_260:
	s_ashr_i32 s41, s40, 31
	s_lshl_b64 s[42:43], s[40:41], 19
	s_add_u32 s42, s54, s42
	s_addc_u32 s43, s55, s43
	s_and_b64 s[44:45], s[4:5], exec
	ds_read_b128 v[0:3], v219
	ds_read_b128 v[4:7], v219 offset:1024
	ds_read_b128 v[8:11], v219 offset:2048
	s_waitcnt vmcnt(2)
	ds_read_b128 v[12:15], v219 offset:3072
	s_waitcnt vmcnt(1)
	ds_read_b128 v[16:19], v220
	s_waitcnt vmcnt(0)
	ds_read_b128 v[20:23], v220 offset:1024
	ds_read_b128 v[24:27], v220 offset:2048
	ds_read_b128 v[28:31], v220 offset:3072
	s_cselect_b32 s7, s43, s13
	s_cselect_b32 s11, s42, s12
	s_ashr_i32 s39, s38, 31
	s_lshl_b64 s[44:45], s[38:39], 19
	s_add_u32 s44, s56, s44
	s_addc_u32 s45, s57, s45
	s_and_b64 s[46:47], s[4:5], exec
	s_cselect_b32 s39, s45, s9
	s_cselect_b32 s41, s44, s8
	s_add_u32 s46, s12, 0x100
	s_addc_u32 s47, s13, 0
	s_add_u32 s52, s8, 0x100
	s_addc_u32 s53, s9, 0
	s_add_u32 s48, s12, 0x180
	s_addc_u32 s49, s13, 0
	ds_read_b128 v[32:35], v221
	ds_read_b128 v[36:39], v221 offset:1024
	ds_read_b128 v[40:43], v221 offset:2048
	ds_read_b128 v[44:47], v221 offset:3072
	ds_read_b128 v[48:51], v221 offset:4096
	ds_read_b128 v[52:55], v221 offset:5120
	ds_read_b128 v[56:59], v221 offset:6144
	ds_read_b128 v[60:63], v221 offset:7168
	s_add_u32 s50, s8, 0x180
	s_addc_u32 s51, s9, 0
	s_add_u32 s76, s12, 0x40080
	s_addc_u32 s77, s13, 0
	s_add_i32 m0, s59, 0xc000
	s_nop 0
	global_load_lds_dwordx4 v215, s[76:77]
	s_nop 0
	s_add_i32 m0, s59, 0xe000
	s_nop 0
	global_load_lds_dwordx4 v217, s[76:77]
	s_waitcnt vmcnt(8)
	s_waitcnt lgkmcnt(0)
	s_barrier
	s_waitcnt lgkmcnt(7)
	v_mfma_i32_16x16x64_i8 v[64:67], v[0:3], v[32:35], 0
	s_mov_b32 s76, 0
	v_mfma_i32_16x16x64_i8 v[68:71], v[8:11], v[32:35], 0
	s_waitcnt lgkmcnt(5)
	v_mfma_i32_16x16x64_i8 v[72:75], v[0:3], v[40:43], 0
	v_mfma_i32_16x16x64_i8 v[76:79], v[8:11], v[40:43], 0
	s_waitcnt lgkmcnt(3)
	v_mfma_i32_16x16x64_i8 v[84:87], v[8:11], v[48:51], 0
	s_waitcnt lgkmcnt(1)
	v_mfma_i32_16x16x64_i8 v[88:91], v[0:3], v[56:59], 0
	v_mfma_i32_16x16x64_i8 v[140:143], v[4:7], v[36:39], v[64:67]
	v_mfma_i32_16x16x64_i8 v[144:147], v[12:15], v[36:39], v[68:71]
	v_mfma_i32_16x16x64_i8 v[152:155], v[4:7], v[44:47], v[72:75]
	v_mfma_i32_16x16x64_i8 v[156:159], v[12:15], v[44:47], v[76:79]
	v_mfma_i32_16x16x64_i8 v[80:83], v[0:3], v[48:51], 0
	v_mfma_i32_16x16x64_i8 v[84:87], v[12:15], v[52:55], v[84:87]
	s_waitcnt lgkmcnt(0)
	v_mfma_i32_16x16x64_i8 v[88:91], v[4:7], v[60:63], v[88:91]
	v_mfma_i32_16x16x64_i8 v[92:95], v[8:11], v[56:59], 0
	v_mfma_i32_16x16x64_i8 v[80:83], v[4:7], v[52:55], v[80:83]
	v_mfma_i32_16x16x64_i8 v[92:95], v[12:15], v[60:63], v[92:95]
	v_mfma_i32_16x16x64_i8 v[96:99], v[16:19], v[32:35], 0
	v_mfma_i32_16x16x64_i8 v[32:35], v[24:27], v[32:35], 0
	v_mfma_i32_16x16x64_i8 v[96:99], v[20:23], v[36:39], v[96:99]
	v_mfma_i32_16x16x64_i8 v[32:35], v[28:31], v[36:39], v[32:35]
	v_mfma_i32_16x16x64_i8 v[36:39], v[16:19], v[40:43], 0
	v_mfma_i32_16x16x64_i8 v[40:43], v[24:27], v[40:43], 0
	v_mfma_i32_16x16x64_i8 v[36:39], v[20:23], v[44:47], v[36:39]
	v_mfma_i32_16x16x64_i8 v[40:43], v[28:31], v[44:47], v[40:43]
	v_mfma_i32_16x16x64_i8 v[44:47], v[16:19], v[48:51], 0
	v_mfma_i32_16x16x64_i8 v[48:51], v[24:27], v[48:51], 0
	v_mfma_i32_16x16x64_i8 v[44:47], v[20:23], v[52:55], v[44:47]
	v_mfma_i32_16x16x64_i8 v[48:51], v[28:31], v[52:55], v[48:51]
	v_mfma_i32_16x16x64_i8 v[52:55], v[16:19], v[56:59], 0
	v_mfma_i32_16x16x64_i8 v[56:59], v[24:27], v[56:59], 0
	v_mfma_i32_16x16x64_i8 v[52:55], v[20:23], v[60:63], v[52:55]
	v_mfma_i32_16x16x64_i8 v[56:59], v[28:31], v[60:63], v[56:59]
	s_barrier
	ds_read_b128 v[60:63], v221 offset:16384
	ds_read_b128 v[100:103], v221 offset:17408
	ds_read_b128 v[104:107], v221 offset:18432
	ds_read_b128 v[108:111], v221 offset:19456
	ds_read_b128 v[112:115], v221 offset:20480
	ds_read_b128 v[116:119], v221 offset:21504
	ds_read_b128 v[120:123], v221 offset:22528
	ds_read_b128 v[124:127], v221 offset:23552
	s_add_i32 m0, s59, 0x10000
	s_nop 0
	global_load_lds_dwordx4 v216, s[52:53]
	s_nop 0
	s_add_i32 m0, s59, 0x12000
	s_nop 0
	global_load_lds_dwordx4 v218, s[52:53]
	s_add_u32 s52, s8, 0x40100
	s_addc_u32 s53, s9, 0
	s_add_i32 m0, s59, 0x14000
	s_nop 0
	global_load_lds_dwordx4 v216, s[52:53]
	s_nop 0
	s_add_i32 m0, s59, 0x16000
	s_nop 0
	global_load_lds_dwordx4 v218, s[52:53]
	s_nop 0
	s_add_i32 m0, s59, 0
	s_nop 0
	global_load_lds_dwordx4 v215, s[46:47]
	s_nop 0
	s_add_i32 m0, s59, 0x2000
	s_nop 0
	global_load_lds_dwordx4 v217, s[46:47]
	s_waitcnt vmcnt(8)
	s_waitcnt lgkmcnt(0)
	s_barrier
	v_mfma_i32_16x16x64_i8 v[136:139], v[0:3], v[104:107], 0
	v_mfma_i32_16x16x64_i8 v[228:231], v[4:7], v[108:111], v[136:139]
	v_mfma_i32_16x16x64_i8 v[136:139], v[8:11], v[104:107], 0
	v_mfma_i32_16x16x64_i8 v[128:131], v[0:3], v[60:63], 0
	v_mfma_i32_16x16x64_i8 v[132:135], v[8:11], v[60:63], 0
	v_mfma_i32_16x16x64_i8 v[232:235], v[12:15], v[108:111], v[136:139]
	v_mfma_i32_16x16x64_i8 v[136:139], v[0:3], v[112:115], 0
	v_mfma_i32_16x16x64_i8 v[0:3], v[0:3], v[120:123], 0
	v_mfma_i32_16x16x64_i8 v[128:131], v[4:7], v[100:103], v[128:131]
	v_mfma_i32_16x16x64_i8 v[132:135], v[12:15], v[100:103], v[132:135]
	v_mfma_i32_16x16x64_i8 v[236:239], v[4:7], v[116:119], v[136:139]
	v_mfma_i32_16x16x64_i8 v[136:139], v[8:11], v[112:115], 0
	v_mfma_i32_16x16x64_i8 v[0:3], v[4:7], v[124:127], v[0:3]
	v_mfma_i32_16x16x64_i8 v[4:7], v[8:11], v[120:123], 0
	v_mfma_i32_16x16x64_i8 v[240:243], v[12:15], v[116:119], v[136:139]
	v_mfma_i32_16x16x64_i8 v[4:7], v[12:15], v[124:127], v[4:7]
	v_mfma_i32_16x16x64_i8 v[8:11], v[16:19], v[60:63], 0
	v_mfma_i32_16x16x64_i8 v[12:15], v[24:27], v[60:63], 0
	v_mfma_i32_16x16x64_i8 v[8:11], v[20:23], v[100:103], v[8:11]
	v_mfma_i32_16x16x64_i8 v[12:15], v[28:31], v[100:103], v[12:15]
	v_mfma_i32_16x16x64_i8 v[60:63], v[16:19], v[104:107], 0
	v_mfma_i32_16x16x64_i8 v[100:103], v[24:27], v[104:107], 0
	v_mfma_i32_16x16x64_i8 v[104:107], v[16:19], v[112:115], 0
	v_mfma_i32_16x16x64_i8 v[16:19], v[16:19], v[120:123], 0
	v_mfma_i32_16x16x64_i8 v[60:63], v[20:23], v[108:111], v[60:63]
	v_mfma_i32_16x16x64_i8 v[100:103], v[28:31], v[108:111], v[100:103]
	v_mfma_i32_16x16x64_i8 v[244:247], v[20:23], v[116:119], v[104:107]
	v_mfma_i32_16x16x64_i8 v[104:107], v[24:27], v[112:115], 0
	v_mfma_i32_16x16x64_i8 v[16:19], v[20:23], v[124:127], v[16:19]
	v_mfma_i32_16x16x64_i8 v[20:23], v[24:27], v[120:123], 0
	v_mfma_i32_16x16x64_i8 v[248:251], v[28:31], v[116:119], v[104:107]
	v_mfma_i32_16x16x64_i8 v[20:23], v[28:31], v[124:127], v[20:23]
	s_barrier
	ds_read_b128 v[24:27], v222
	ds_read_b128 v[28:31], v222 offset:1024
	ds_read_b128 v[112:115], v222 offset:2048
	ds_read_b128 v[116:119], v222 offset:3072
	ds_read_b128 v[208:211], v223
	ds_read_b128 v[224:227], v223 offset:1024
	ds_read_b128 v[64:67], v223 offset:2048
	ds_read_b128 v[68:71], v223 offset:3072
	ds_read_b128 v[104:107], v221 offset:32768
	ds_read_b128 v[108:111], v221 offset:33792
	ds_read_b128 v[120:123], v221 offset:34816
	ds_read_b128 v[124:127], v221 offset:35840
	ds_read_b128 v[136:139], v221 offset:36864
	ds_read_b128 v[148:151], v221 offset:37888
	ds_read_b128 v[72:75], v221 offset:38912
	ds_read_b128 v[76:79], v221 offset:39936
	s_add_u32 s12, s12, 0x40100
	s_addc_u32 s13, s13, 0
	s_add_i32 m0, s59, 0x4000
	s_nop 0
	global_load_lds_dwordx4 v215, s[12:13]
	s_nop 0
	s_add_i32 m0, s59, 0x6000
	s_nop 0
	global_load_lds_dwordx4 v217, s[12:13]
	s_waitcnt vmcnt(8)
	s_waitcnt lgkmcnt(0)
	s_barrier
	v_mfma_i32_16x16x64_i8 v[140:143], v[24:27], v[104:107], v[140:143]
	v_mfma_i32_16x16x64_i8 v[80:83], v[24:27], v[136:139], v[80:83]
	v_mfma_i32_16x16x64_i8 v[204:207], v[28:31], v[108:111], v[140:143]
	v_mfma_i32_16x16x64_i8 v[140:143], v[112:115], v[104:107], v[144:147]
	v_mfma_i32_16x16x64_i8 v[172:175], v[28:31], v[148:151], v[80:83]
	v_mfma_i32_16x16x64_i8 v[80:83], v[112:115], v[136:139], v[84:87]
	v_mfma_i32_16x16x64_i8 v[200:203], v[116:119], v[108:111], v[140:143]
	v_mfma_i32_16x16x64_i8 v[140:143], v[24:27], v[120:123], v[152:155]
	v_mfma_i32_16x16x64_i8 v[168:171], v[116:119], v[148:151], v[80:83]
	v_mfma_i32_16x16x64_i8 v[80:83], v[24:27], v[72:75], v[88:91]
	v_mfma_i32_16x16x64_i8 v[188:191], v[28:31], v[124:127], v[140:143]
	v_mfma_i32_16x16x64_i8 v[140:143], v[112:115], v[120:123], v[156:159]
	v_mfma_i32_16x16x64_i8 v[156:159], v[28:31], v[76:79], v[80:83]
	v_mfma_i32_16x16x64_i8 v[80:83], v[112:115], v[72:75], v[92:95]
	v_mfma_i32_16x16x64_i8 v[184:187], v[116:119], v[124:127], v[140:143]
	v_mfma_i32_16x16x64_i8 v[152:155], v[116:119], v[76:79], v[80:83]
	v_mfma_i32_16x16x64_i8 v[32:35], v[64:67], v[104:107], v[32:35]
	v_mfma_i32_16x16x64_i8 v[192:195], v[68:71], v[108:111], v[32:35]
	v_mfma_i32_16x16x64_i8 v[32:35], v[208:211], v[120:123], v[36:39]
	v_mfma_i32_16x16x64_i8 v[180:183], v[224:227], v[124:127], v[32:35]
	v_mfma_i32_16x16x64_i8 v[32:35], v[64:67], v[120:123], v[40:43]
	v_mfma_i32_16x16x64_i8 v[176:179], v[68:71], v[124:127], v[32:35]
	v_mfma_i32_16x16x64_i8 v[32:35], v[208:211], v[136:139], v[44:47]
	v_mfma_i32_16x16x64_i8 v[164:167], v[224:227], v[148:151], v[32:35]
	v_mfma_i32_16x16x64_i8 v[32:35], v[64:67], v[136:139], v[48:51]
	v_mfma_i32_16x16x64_i8 v[160:163], v[68:71], v[148:151], v[32:35]
	v_mfma_i32_16x16x64_i8 v[32:35], v[208:211], v[72:75], v[52:55]
	v_mfma_i32_16x16x64_i8 v[80:83], v[208:211], v[104:107], v[96:99]
	v_mfma_i32_16x16x64_i8 v[148:151], v[224:227], v[76:79], v[32:35]
	v_mfma_i32_16x16x64_i8 v[32:35], v[64:67], v[72:75], v[56:59]
	v_mfma_i32_16x16x64_i8 v[196:199], v[224:227], v[108:111], v[80:83]
	v_mfma_i32_16x16x64_i8 v[144:147], v[68:71], v[76:79], v[32:35]
	s_barrier
	s_nop 3
	ds_read_b128 v[32:35], v221 offset:49152
	ds_read_b128 v[36:39], v221 offset:50176
	ds_read_b128 v[40:43], v221 offset:51200
	ds_read_b128 v[44:47], v221 offset:52224
	ds_read_b128 v[48:51], v221 offset:53248
	ds_read_b128 v[52:55], v221 offset:54272
	ds_read_b128 v[56:59], v221 offset:55296
	ds_read_b128 v[76:79], v221 offset:56320
	s_add_i32 m0, s59, 0x18000
	s_nop 0
	global_load_lds_dwordx4 v216, s[50:51]
	s_nop 0
	s_add_i32 m0, s59, 0x1a000
	s_nop 0
	global_load_lds_dwordx4 v218, s[50:51]
	s_add_u32 s12, s8, 0x40180
	s_addc_u32 s13, s9, 0
	s_add_i32 m0, s59, 0x1c000
	s_nop 0
	global_load_lds_dwordx4 v216, s[12:13]
	s_nop 0
	s_add_i32 m0, s59, 0x1e000
	s_nop 0
	global_load_lds_dwordx4 v218, s[12:13]
	s_nop 0
	s_add_i32 m0, s59, 0x8000
	s_nop 0
	global_load_lds_dwordx4 v215, s[48:49]
	s_nop 0
	s_add_i32 m0, s59, 0xa000
	s_nop 0
	global_load_lds_dwordx4 v217, s[48:49]
	s_waitcnt vmcnt(8)
	s_waitcnt lgkmcnt(0)
	s_barrier
	v_mfma_i32_16x16x64_i8 v[72:75], v[24:27], v[32:35], v[128:131]
	v_mfma_i32_16x16x64_i8 v[140:143], v[28:31], v[36:39], v[72:75]
	v_mfma_i32_16x16x64_i8 v[72:75], v[112:115], v[32:35], v[132:135]
	v_mfma_i32_16x16x64_i8 v[136:139], v[116:119], v[36:39], v[72:75]
	v_mfma_i32_16x16x64_i8 v[72:75], v[24:27], v[40:43], v[228:231]
	v_mfma_i32_16x16x64_i8 v[124:127], v[28:31], v[44:47], v[72:75]
	v_mfma_i32_16x16x64_i8 v[72:75], v[112:115], v[40:43], v[232:235]
	v_mfma_i32_16x16x64_i8 v[120:123], v[116:119], v[44:47], v[72:75]
	v_mfma_i32_16x16x64_i8 v[72:75], v[24:27], v[48:51], v[236:239]
	v_mfma_i32_16x16x64_i8 v[0:3], v[24:27], v[56:59], v[0:3]
	v_mfma_i32_16x16x64_i8 v[108:111], v[28:31], v[52:55], v[72:75]
	v_mfma_i32_16x16x64_i8 v[72:75], v[112:115], v[48:51], v[240:243]
	v_mfma_i32_16x16x64_i8 v[88:91], v[28:31], v[76:79], v[0:3]
	v_mfma_i32_16x16x64_i8 v[0:3], v[112:115], v[56:59], v[4:7]
	v_mfma_i32_16x16x64_i8 v[104:107], v[116:119], v[52:55], v[72:75]
	v_mfma_i32_16x16x64_i8 v[84:87], v[116:119], v[76:79], v[0:3]
	v_mfma_i32_16x16x64_i8 v[0:3], v[208:211], v[32:35], v[8:11]
	v_mfma_i32_16x16x64_i8 v[132:135], v[224:227], v[36:39], v[0:3]
	v_mfma_i32_16x16x64_i8 v[0:3], v[64:67], v[32:35], v[12:15]
	v_mfma_i32_16x16x64_i8 v[128:131], v[68:71], v[36:39], v[0:3]
	v_mfma_i32_16x16x64_i8 v[0:3], v[208:211], v[40:43], v[60:63]
	v_mfma_i32_16x16x64_i8 v[116:119], v[224:227], v[44:47], v[0:3]
	v_mfma_i32_16x16x64_i8 v[0:3], v[64:67], v[40:43], v[100:103]
	v_mfma_i32_16x16x64_i8 v[112:115], v[68:71], v[44:47], v[0:3]
	v_mfma_i32_16x16x64_i8 v[0:3], v[208:211], v[48:51], v[244:247]
	v_mfma_i32_16x16x64_i8 v[100:103], v[224:227], v[52:55], v[0:3]
	v_mfma_i32_16x16x64_i8 v[0:3], v[64:67], v[48:51], v[248:251]
	v_mfma_i32_16x16x64_i8 v[96:99], v[68:71], v[52:55], v[0:3]
	v_mfma_i32_16x16x64_i8 v[0:3], v[208:211], v[56:59], v[16:19]
	v_mfma_i32_16x16x64_i8 v[72:75], v[224:227], v[76:79], v[0:3]
	v_mfma_i32_16x16x64_i8 v[0:3], v[64:67], v[56:59], v[20:23]
	v_mfma_i32_16x16x64_i8 v[68:71], v[68:71], v[76:79], v[0:3]
	s_barrier
	s_add_u32 s77, s8, 0x200
	s_addc_u32 s80, s9, 0
.LBB0_261:
	s_nop 2
	ds_read_b128 v[0:3], v219
	ds_read_b128 v[4:7], v219 offset:1024
	ds_read_b128 v[8:11], v219 offset:2048
	ds_read_b128 v[12:15], v219 offset:3072
	ds_read_b128 v[16:19], v220
	ds_read_b128 v[20:23], v220 offset:1024
	ds_read_b128 v[24:27], v220 offset:2048
	ds_read_b128 v[28:31], v220 offset:3072
	s_add_u32 s8, s46, 0x100
	s_addc_u32 s9, s47, 0
	s_cmp_eq_u32 s76, 12
	s_cselect_b32 s52, s11, s8
	s_cselect_b32 s53, s7, s9
	s_cselect_b32 s48, s41, s77
	s_cselect_b32 s49, s39, s80
	s_add_u32 s12, s52, 0x80
	s_addc_u32 s13, s53, 0
	ds_read_b128 v[32:35], v221
	ds_read_b128 v[36:39], v221 offset:1024
	ds_read_b128 v[40:43], v221 offset:2048
	ds_read_b128 v[44:47], v221 offset:3072
	ds_read_b128 v[48:51], v221 offset:4096
	ds_read_b128 v[52:55], v221 offset:5120
	ds_read_b128 v[56:59], v221 offset:6144
	ds_read_b128 v[60:63], v221 offset:7168
	s_add_u32 s50, s48, 0x80
	s_addc_u32 s51, s49, 0
	s_add_u32 s46, s46, 0x40080
	s_addc_u32 s47, s47, 0
	s_add_i32 m0, s59, 0xc000
	s_nop 0
	global_load_lds_dwordx4 v215, s[46:47]
	s_nop 0
	s_add_i32 m0, s59, 0xe000
	s_nop 0
	global_load_lds_dwordx4 v217, s[46:47]
	s_waitcnt vmcnt(8)
	s_waitcnt lgkmcnt(0)
	s_barrier
	v_mfma_i32_16x16x64_i8 v[172:175], v[0:3], v[48:51], v[172:175]
	v_mfma_i32_16x16x64_i8 v[168:171], v[8:11], v[48:51], v[168:171]
	v_mfma_i32_16x16x64_i8 v[156:159], v[0:3], v[56:59], v[156:159]
	v_mfma_i32_16x16x64_i8 v[152:155], v[8:11], v[56:59], v[152:155]
	v_mfma_i32_16x16x64_i8 v[64:67], v[0:3], v[32:35], v[204:207]
	v_mfma_i32_16x16x64_i8 v[76:79], v[8:11], v[32:35], v[200:203]
	v_mfma_i32_16x16x64_i8 v[80:83], v[0:3], v[40:43], v[188:191]
	v_mfma_i32_16x16x64_i8 v[92:95], v[8:11], v[40:43], v[184:187]
	v_mfma_i32_16x16x64_i8 v[172:175], v[4:7], v[52:55], v[172:175]
	v_mfma_i32_16x16x64_i8 v[168:171], v[12:15], v[52:55], v[168:171]
	v_mfma_i32_16x16x64_i8 v[156:159], v[4:7], v[60:63], v[156:159]
	v_mfma_i32_16x16x64_i8 v[152:155], v[12:15], v[60:63], v[152:155]
	v_mfma_i32_16x16x64_i8 v[64:67], v[4:7], v[36:39], v[64:67]
	v_mfma_i32_16x16x64_i8 v[76:79], v[12:15], v[36:39], v[76:79]
	v_mfma_i32_16x16x64_i8 v[80:83], v[4:7], v[44:47], v[80:83]
	v_mfma_i32_16x16x64_i8 v[92:95], v[12:15], v[44:47], v[92:95]
	v_mfma_i32_16x16x64_i8 v[184:187], v[16:19], v[32:35], v[196:199]
	v_mfma_i32_16x16x64_i8 v[32:35], v[24:27], v[32:35], v[192:195]
	v_mfma_i32_16x16x64_i8 v[196:199], v[20:23], v[36:39], v[184:187]
	v_mfma_i32_16x16x64_i8 v[32:35], v[28:31], v[36:39], v[32:35]
	v_mfma_i32_16x16x64_i8 v[36:39], v[16:19], v[40:43], v[180:183]
	v_mfma_i32_16x16x64_i8 v[40:43], v[24:27], v[40:43], v[176:179]
	v_mfma_i32_16x16x64_i8 v[36:39], v[20:23], v[44:47], v[36:39]
	v_mfma_i32_16x16x64_i8 v[40:43], v[28:31], v[44:47], v[40:43]
	v_mfma_i32_16x16x64_i8 v[44:47], v[16:19], v[48:51], v[164:167]
	v_mfma_i32_16x16x64_i8 v[48:51], v[24:27], v[48:51], v[160:163]
	v_mfma_i32_16x16x64_i8 v[44:47], v[20:23], v[52:55], v[44:47]
	v_mfma_i32_16x16x64_i8 v[48:51], v[28:31], v[52:55], v[48:51]
	v_mfma_i32_16x16x64_i8 v[52:55], v[16:19], v[56:59], v[148:151]
	v_mfma_i32_16x16x64_i8 v[56:59], v[24:27], v[56:59], v[144:147]
	v_mfma_i32_16x16x64_i8 v[52:55], v[20:23], v[60:63], v[52:55]
	v_mfma_i32_16x16x64_i8 v[56:59], v[28:31], v[60:63], v[56:59]
	s_barrier
	ds_read_b128 v[60:63], v221 offset:16384
	ds_read_b128 v[144:147], v221 offset:17408
	ds_read_b128 v[148:151], v221 offset:18432
	ds_read_b128 v[160:163], v221 offset:19456
	ds_read_b128 v[164:167], v221 offset:20480
	ds_read_b128 v[176:179], v221 offset:21504
	ds_read_b128 v[180:183], v221 offset:22528
	ds_read_b128 v[184:187], v221 offset:23552
	s_add_i32 m0, s59, 0x10000
	s_nop 0
	global_load_lds_dwordx4 v216, s[48:49]
	s_nop 0
	s_add_i32 m0, s59, 0x12000
	s_nop 0
	global_load_lds_dwordx4 v218, s[48:49]
	s_add_u32 s46, s48, 0x40000
	s_addc_u32 s47, s49, 0
	s_add_i32 m0, s59, 0x14000
	s_nop 0
	global_load_lds_dwordx4 v216, s[46:47]
	s_nop 0
	s_add_i32 m0, s59, 0x16000
	s_nop 0
	global_load_lds_dwordx4 v218, s[46:47]
	s_nop 0
	s_add_i32 m0, s59, 0
	s_nop 0
	global_load_lds_dwordx4 v215, s[52:53]
	s_nop 0
	s_add_i32 m0, s59, 0x2000
	s_nop 0
	global_load_lds_dwordx4 v217, s[52:53]
	s_waitcnt vmcnt(8)
	s_waitcnt lgkmcnt(0)
	s_barrier
	v_mfma_i32_16x16x64_i8 v[140:143], v[0:3], v[60:63], v[140:143]
	v_mfma_i32_16x16x64_i8 v[124:127], v[0:3], v[148:151], v[124:127]
	v_mfma_i32_16x16x64_i8 v[108:111], v[0:3], v[164:167], v[108:111]
	v_mfma_i32_16x16x64_i8 v[0:3], v[0:3], v[180:183], v[88:91]
	v_mfma_i32_16x16x64_i8 v[136:139], v[8:11], v[60:63], v[136:139]
	v_mfma_i32_16x16x64_i8 v[120:123], v[8:11], v[148:151], v[120:123]
	v_mfma_i32_16x16x64_i8 v[104:107], v[8:11], v[164:167], v[104:107]
	v_mfma_i32_16x16x64_i8 v[88:91], v[4:7], v[184:187], v[0:3]
	v_mfma_i32_16x16x64_i8 v[0:3], v[8:11], v[180:183], v[84:87]
	v_mfma_i32_16x16x64_i8 v[140:143], v[4:7], v[144:147], v[140:143]
	v_mfma_i32_16x16x64_i8 v[136:139], v[12:15], v[144:147], v[136:139]
	v_mfma_i32_16x16x64_i8 v[124:127], v[4:7], v[160:163], v[124:127]
	v_mfma_i32_16x16x64_i8 v[120:123], v[12:15], v[160:163], v[120:123]
	v_mfma_i32_16x16x64_i8 v[108:111], v[4:7], v[176:179], v[108:111]
	v_mfma_i32_16x16x64_i8 v[104:107], v[12:15], v[176:179], v[104:107]
	v_mfma_i32_16x16x64_i8 v[84:87], v[12:15], v[184:187], v[0:3]
	v_mfma_i32_16x16x64_i8 v[0:3], v[16:19], v[60:63], v[132:135]
	v_mfma_i32_16x16x64_i8 v[132:135], v[20:23], v[144:147], v[0:3]
	v_mfma_i32_16x16x64_i8 v[0:3], v[24:27], v[60:63], v[128:131]
	v_mfma_i32_16x16x64_i8 v[128:131], v[28:31], v[144:147], v[0:3]
	v_mfma_i32_16x16x64_i8 v[0:3], v[16:19], v[148:151], v[116:119]
	v_mfma_i32_16x16x64_i8 v[116:119], v[20:23], v[160:163], v[0:3]
	v_mfma_i32_16x16x64_i8 v[0:3], v[24:27], v[148:151], v[112:115]
	v_mfma_i32_16x16x64_i8 v[112:115], v[28:31], v[160:163], v[0:3]
	v_mfma_i32_16x16x64_i8 v[0:3], v[16:19], v[164:167], v[100:103]
	v_mfma_i32_16x16x64_i8 v[100:103], v[20:23], v[176:179], v[0:3]
	v_mfma_i32_16x16x64_i8 v[0:3], v[24:27], v[164:167], v[96:99]
	v_mfma_i32_16x16x64_i8 v[96:99], v[28:31], v[176:179], v[0:3]
	v_mfma_i32_16x16x64_i8 v[0:3], v[16:19], v[180:183], v[72:75]
	v_mfma_i32_16x16x64_i8 v[72:75], v[20:23], v[184:187], v[0:3]
	v_mfma_i32_16x16x64_i8 v[0:3], v[24:27], v[180:183], v[68:71]
	v_mfma_i32_16x16x64_i8 v[68:71], v[28:31], v[184:187], v[0:3]
	s_barrier
	ds_read_b128 v[16:19], v222
	ds_read_b128 v[8:11], v222 offset:1024
	ds_read_b128 v[4:7], v222 offset:2048
	s_nop 1
	ds_read_b128 v[0:3], v222 offset:3072
	ds_read_b128 v[28:31], v223
	ds_read_b128 v[24:27], v223 offset:1024
	ds_read_b128 v[20:23], v223 offset:2048
	ds_read_b128 v[12:15], v223 offset:3072
	ds_read_b128 v[60:63], v221 offset:32768
	ds_read_b128 v[144:147], v221 offset:33792
	ds_read_b128 v[148:151], v221 offset:34816
	ds_read_b128 v[160:163], v221 offset:35840
	ds_read_b128 v[208:211], v221 offset:36864
	ds_read_b128 v[224:227], v221 offset:37888
	ds_read_b128 v[228:231], v221 offset:38912
	ds_read_b128 v[232:235], v221 offset:39936
	s_add_u32 s46, s52, 0x40000
	s_addc_u32 s47, s53, 0
	s_add_i32 m0, s59, 0x4000
	s_nop 0
	global_load_lds_dwordx4 v215, s[46:47]
	s_nop 0
	s_add_i32 m0, s59, 0x6000
	s_nop 0
	global_load_lds_dwordx4 v217, s[46:47]
	s_waitcnt vmcnt(8)
	s_waitcnt lgkmcnt(0)
	s_barrier
	v_mfma_i32_16x16x64_i8 v[64:67], v[16:19], v[60:63], v[64:67]
	v_mfma_i32_16x16x64_i8 v[204:207], v[8:11], v[144:147], v[64:67]
	v_mfma_i32_16x16x64_i8 v[64:67], v[4:7], v[60:63], v[76:79]
	v_mfma_i32_16x16x64_i8 v[200:203], v[0:3], v[144:147], v[64:67]
	v_mfma_i32_16x16x64_i8 v[64:67], v[16:19], v[148:151], v[80:83]
	v_mfma_i32_16x16x64_i8 v[188:191], v[8:11], v[160:163], v[64:67]
	v_mfma_i32_16x16x64_i8 v[64:67], v[4:7], v[148:151], v[92:95]
	v_mfma_i32_16x16x64_i8 v[184:187], v[0:3], v[160:163], v[64:67]
	v_mfma_i32_16x16x64_i8 v[64:67], v[16:19], v[208:211], v[172:175]
	v_mfma_i32_16x16x64_i8 v[172:175], v[8:11], v[224:227], v[64:67]
	v_mfma_i32_16x16x64_i8 v[64:67], v[4:7], v[208:211], v[168:171]
	v_mfma_i32_16x16x64_i8 v[168:171], v[0:3], v[224:227], v[64:67]
	v_mfma_i32_16x16x64_i8 v[64:67], v[16:19], v[228:231], v[156:159]
	v_mfma_i32_16x16x64_i8 v[156:159], v[8:11], v[232:235], v[64:67]
	v_mfma_i32_16x16x64_i8 v[64:67], v[4:7], v[228:231], v[152:155]
	v_mfma_i32_16x16x64_i8 v[152:155], v[0:3], v[232:235], v[64:67]
	v_mfma_i32_16x16x64_i8 v[32:35], v[20:23], v[60:63], v[32:35]
	v_mfma_i32_16x16x64_i8 v[192:195], v[12:15], v[144:147], v[32:35]
	v_mfma_i32_16x16x64_i8 v[32:35], v[28:31], v[148:151], v[36:39]
	v_mfma_i32_16x16x64_i8 v[180:183], v[24:27], v[160:163], v[32:35]
	v_mfma_i32_16x16x64_i8 v[32:35], v[20:23], v[148:151], v[40:43]
	v_mfma_i32_16x16x64_i8 v[176:179], v[12:15], v[160:163], v[32:35]
	v_mfma_i32_16x16x64_i8 v[32:35], v[28:31], v[208:211], v[44:47]
	v_mfma_i32_16x16x64_i8 v[164:167], v[24:27], v[224:227], v[32:35]
	v_mfma_i32_16x16x64_i8 v[32:35], v[20:23], v[208:211], v[48:51]
	v_mfma_i32_16x16x64_i8 v[160:163], v[12:15], v[224:227], v[32:35]
	v_mfma_i32_16x16x64_i8 v[32:35], v[28:31], v[228:231], v[52:55]
	v_mfma_i32_16x16x64_i8 v[64:67], v[28:31], v[60:63], v[196:199]
	v_mfma_i32_16x16x64_i8 v[148:151], v[24:27], v[232:235], v[32:35]
	v_mfma_i32_16x16x64_i8 v[32:35], v[20:23], v[228:231], v[56:59]
	v_mfma_i32_16x16x64_i8 v[196:199], v[24:27], v[144:147], v[64:67]
	v_mfma_i32_16x16x64_i8 v[144:147], v[12:15], v[232:235], v[32:35]
	s_barrier
	ds_read_b128 v[60:63], v221 offset:49152
	ds_read_b128 v[56:59], v221 offset:50176
	ds_read_b128 v[52:55], v221 offset:51200
	ds_read_b128 v[48:51], v221 offset:52224
	ds_read_b128 v[44:47], v221 offset:53248
	ds_read_b128 v[40:43], v221 offset:54272
	ds_read_b128 v[36:39], v221 offset:55296
	ds_read_b128 v[32:35], v221 offset:56320
	s_add_i32 m0, s59, 0x18000
	s_nop 0
	global_load_lds_dwordx4 v216, s[50:51]
	s_nop 0
	s_add_i32 m0, s59, 0x1a000
	s_nop 0
	global_load_lds_dwordx4 v218, s[50:51]
	s_add_u32 s46, s48, 0x40080
	s_addc_u32 s47, s49, 0
	s_add_i32 m0, s59, 0x1c000
	s_nop 0
	global_load_lds_dwordx4 v216, s[46:47]
	s_nop 0
	s_add_i32 m0, s59, 0x1e000
	s_nop 0
	global_load_lds_dwordx4 v218, s[46:47]
	s_nop 0
	s_add_i32 m0, s59, 0x8000
	s_nop 0
	global_load_lds_dwordx4 v215, s[12:13]
	s_nop 0
	s_add_i32 m0, s59, 0xa000
	s_nop 0
	global_load_lds_dwordx4 v217, s[12:13]
	s_waitcnt vmcnt(8)
	s_waitcnt lgkmcnt(0)
	s_barrier
	v_mfma_i32_16x16x64_i8 v[64:67], v[16:19], v[60:63], v[140:143]
	v_mfma_i32_16x16x64_i8 v[140:143], v[8:11], v[56:59], v[64:67]
	v_mfma_i32_16x16x64_i8 v[64:67], v[4:7], v[60:63], v[136:139]
	v_mfma_i32_16x16x64_i8 v[136:139], v[0:3], v[56:59], v[64:67]
	v_mfma_i32_16x16x64_i8 v[64:67], v[16:19], v[52:55], v[124:127]
	v_mfma_i32_16x16x64_i8 v[124:127], v[8:11], v[48:51], v[64:67]
	v_mfma_i32_16x16x64_i8 v[64:67], v[4:7], v[52:55], v[120:123]
	v_mfma_i32_16x16x64_i8 v[120:123], v[0:3], v[48:51], v[64:67]
	v_mfma_i32_16x16x64_i8 v[64:67], v[16:19], v[44:47], v[108:111]
	v_mfma_i32_16x16x64_i8 v[108:111], v[8:11], v[40:43], v[64:67]
	v_mfma_i32_16x16x64_i8 v[64:67], v[4:7], v[44:47], v[104:107]
	v_mfma_i32_16x16x64_i8 v[104:107], v[0:3], v[40:43], v[64:67]
	v_mfma_i32_16x16x64_i8 v[64:67], v[16:19], v[36:39], v[88:91]
	v_mfma_i32_16x16x64_i8 v[88:91], v[8:11], v[32:35], v[64:67]
	v_mfma_i32_16x16x64_i8 v[64:67], v[4:7], v[36:39], v[84:87]
	v_mfma_i32_16x16x64_i8 v[84:87], v[0:3], v[32:35], v[64:67]
	v_mfma_i32_16x16x64_i8 v[64:67], v[28:31], v[60:63], v[132:135]
	v_mfma_i32_16x16x64_i8 v[132:135], v[24:27], v[56:59], v[64:67]
	v_mfma_i32_16x16x64_i8 v[64:67], v[20:23], v[60:63], v[128:131]
	v_mfma_i32_16x16x64_i8 v[128:131], v[12:15], v[56:59], v[64:67]
	v_mfma_i32_16x16x64_i8 v[64:67], v[28:31], v[52:55], v[116:119]
	v_mfma_i32_16x16x64_i8 v[116:119], v[24:27], v[48:51], v[64:67]
	v_mfma_i32_16x16x64_i8 v[64:67], v[20:23], v[52:55], v[112:115]
	v_mfma_i32_16x16x64_i8 v[112:115], v[12:15], v[48:51], v[64:67]
	v_mfma_i32_16x16x64_i8 v[64:67], v[28:31], v[44:47], v[100:103]
	v_mfma_i32_16x16x64_i8 v[100:103], v[24:27], v[40:43], v[64:67]
	v_mfma_i32_16x16x64_i8 v[64:67], v[20:23], v[44:47], v[96:99]
	v_mfma_i32_16x16x64_i8 v[96:99], v[12:15], v[40:43], v[64:67]
	v_mfma_i32_16x16x64_i8 v[64:67], v[28:31], v[36:39], v[72:75]
	v_mfma_i32_16x16x64_i8 v[72:75], v[24:27], v[32:35], v[64:67]
	v_mfma_i32_16x16x64_i8 v[64:67], v[20:23], v[36:39], v[68:71]
	v_mfma_i32_16x16x64_i8 v[68:71], v[12:15], v[32:35], v[64:67]
	s_barrier
	s_add_i32 s76, s76, 2
	s_add_u32 s77, s77, 0x100
	s_addc_u32 s80, s80, 0
	s_cmp_gt_u32 s76, 13
	s_mov_b64 s[46:47], s[8:9]
	s_cbranch_scc0 .LBB0_261
	s_and_b64 vcc, exec, s[28:29]
	s_cbranch_vccz .LBB0_264
	s_barrier

.LBB0_602:
	s_ashr_i32 s25, s24, 31
	s_lshl_b64 s[26:27], s[24:25], 20
	s_add_u32 s26, s44, s26
	s_addc_u32 s27, s45, s27
	s_and_b64 s[28:29], s[4:5], exec
	s_waitcnt lgkmcnt(0)
	ds_read_b128 v[0:3], v217
	ds_read_b128 v[4:7], v217 offset:1024
	ds_read_b128 v[8:11], v217 offset:2048
	ds_read_b128 v[12:15], v217 offset:3072
	ds_read_b128 v[16:19], v218
	ds_read_b128 v[20:23], v218 offset:1024
	ds_read_b128 v[24:27], v218 offset:2048
	ds_read_b128 v[28:31], v218 offset:3072
	s_cselect_b32 s7, s27, s35
	s_cselect_b32 s9, s26, s34
	s_ashr_i32 s23, s22, 31
	s_lshl_b64 s[28:29], s[22:23], 20
	s_add_u32 s28, s46, s28
	s_addc_u32 s29, s47, s29
	s_and_b64 s[36:37], s[4:5], exec
	s_cselect_b32 s23, s29, s31
	s_cselect_b32 s25, s28, s30
	s_add_u32 s36, s34, 0x100
	s_addc_u32 s37, s35, 0
	s_add_u32 s42, s30, 0x100
	s_addc_u32 s43, s31, 0
	s_add_u32 s38, s34, 0x180
	s_addc_u32 s39, s35, 0
	ds_read_b128 v[32:35], v219
	ds_read_b128 v[36:39], v219 offset:1024
	ds_read_b128 v[40:43], v219 offset:2048
	ds_read_b128 v[44:47], v219 offset:3072
	ds_read_b128 v[48:51], v219 offset:4096
	ds_read_b128 v[52:55], v219 offset:5120
	ds_read_b128 v[56:59], v219 offset:6144
	ds_read_b128 v[60:63], v219 offset:7168
	s_add_u32 s40, s30, 0x180
	s_addc_u32 s41, s31, 0
	s_add_u32 s60, s34, 0x80080
	s_addc_u32 s61, s35, 0
	s_add_i32 m0, s48, 0xc000
	s_nop 0
	global_load_lds_dwordx4 v213, s[60:61]
	s_nop 0
	s_add_i32 m0, s48, 0xe000
	s_nop 0
	global_load_lds_dwordx4 v214, s[60:61]
	s_waitcnt vmcnt(8)
	s_waitcnt lgkmcnt(0)
	s_barrier
	v_mfma_f32_16x16x32_bf16 v[64:67], v[0:3], v[32:35], 0
	v_mfma_f32_16x16x32_bf16 v[68:71], v[8:11], v[32:35], 0
	v_mfma_f32_16x16x32_bf16 v[72:75], v[0:3], v[40:43], 0
	v_mfma_f32_16x16x32_bf16 v[76:79], v[8:11], v[40:43], 0
	v_mfma_f32_16x16x32_bf16 v[80:83], v[0:3], v[48:51], 0
	v_mfma_f32_16x16x32_bf16 v[84:87], v[8:11], v[48:51], 0
	v_mfma_f32_16x16x32_bf16 v[88:91], v[0:3], v[56:59], 0
	v_mfma_f32_16x16x32_bf16 v[64:67], v[4:7], v[36:39], v[64:67]
	v_mfma_f32_16x16x32_bf16 v[68:71], v[12:15], v[36:39], v[68:71]
	v_mfma_f32_16x16x32_bf16 v[72:75], v[4:7], v[44:47], v[72:75]
	v_mfma_f32_16x16x32_bf16 v[76:79], v[12:15], v[44:47], v[76:79]
	v_mfma_f32_16x16x32_bf16 v[80:83], v[4:7], v[52:55], v[80:83]
	v_mfma_f32_16x16x32_bf16 v[84:87], v[12:15], v[52:55], v[84:87]
	v_mfma_f32_16x16x32_bf16 v[96:99], v[4:7], v[60:63], v[88:91]
	v_mfma_f32_16x16x32_bf16 v[88:91], v[8:11], v[56:59], 0
	v_mfma_f32_16x16x32_bf16 v[100:103], v[12:15], v[60:63], v[88:91]
	v_mfma_f32_16x16x32_bf16 v[88:91], v[16:19], v[32:35], 0
	v_mfma_f32_16x16x32_bf16 v[32:35], v[24:27], v[32:35], 0
	v_mfma_f32_16x16x32_bf16 v[104:107], v[20:23], v[36:39], v[88:91]
	v_mfma_f32_16x16x32_bf16 v[32:35], v[28:31], v[36:39], v[32:35]
	v_mfma_f32_16x16x32_bf16 v[36:39], v[16:19], v[40:43], 0
	v_mfma_f32_16x16x32_bf16 v[40:43], v[24:27], v[40:43], 0
	v_mfma_f32_16x16x32_bf16 v[36:39], v[20:23], v[44:47], v[36:39]
	v_mfma_f32_16x16x32_bf16 v[40:43], v[28:31], v[44:47], v[40:43]
	v_mfma_f32_16x16x32_bf16 v[44:47], v[16:19], v[48:51], 0
	v_mfma_f32_16x16x32_bf16 v[48:51], v[24:27], v[48:51], 0
	v_mfma_f32_16x16x32_bf16 v[44:47], v[20:23], v[52:55], v[44:47]
	v_mfma_f32_16x16x32_bf16 v[48:51], v[28:31], v[52:55], v[48:51]
	v_mfma_f32_16x16x32_bf16 v[52:55], v[16:19], v[56:59], 0
	v_mfma_f32_16x16x32_bf16 v[56:59], v[24:27], v[56:59], 0
	v_mfma_f32_16x16x32_bf16 v[52:55], v[20:23], v[60:63], v[52:55]
	v_mfma_f32_16x16x32_bf16 v[56:59], v[28:31], v[60:63], v[56:59]
	s_barrier
	ds_read_b128 v[60:63], v219 offset:16384
	ds_read_b128 v[88:91], v219 offset:17408
	ds_read_b128 v[92:95], v219 offset:18432
	ds_read_b128 v[108:111], v219 offset:19456
	ds_read_b128 v[112:115], v219 offset:20480
	ds_read_b128 v[116:119], v219 offset:21504
	ds_read_b128 v[120:123], v219 offset:22528
	ds_read_b128 v[124:127], v219 offset:23552
	s_add_i32 m0, s48, 0x10000
	s_nop 0
	global_load_lds_dwordx4 v213, s[42:43]
	s_nop 0
	s_add_i32 m0, s48, 0x12000
	s_nop 0
	global_load_lds_dwordx4 v214, s[42:43]
	s_add_u32 s42, s30, 0x80100
	s_addc_u32 s43, s31, 0
	s_add_i32 m0, s48, 0x14000
	s_nop 0
	global_load_lds_dwordx4 v213, s[42:43]
	s_nop 0
	s_add_i32 m0, s48, 0x16000
	s_nop 0
	global_load_lds_dwordx4 v214, s[42:43]
	s_nop 0
	s_add_i32 m0, s48, 0
	s_nop 0
	global_load_lds_dwordx4 v213, s[36:37]
	s_nop 0
	s_add_i32 m0, s48, 0x2000
	s_nop 0
	global_load_lds_dwordx4 v214, s[36:37]
	s_waitcnt vmcnt(8)
	s_waitcnt lgkmcnt(0)
	s_barrier
	v_mfma_f32_16x16x32_bf16 v[128:131], v[0:3], v[60:63], 0
	v_mfma_f32_16x16x32_bf16 v[132:135], v[4:7], v[88:91], v[128:131]
	v_mfma_f32_16x16x32_bf16 v[128:131], v[8:11], v[60:63], 0
	v_mfma_f32_16x16x32_bf16 v[140:143], v[12:15], v[88:91], v[128:131]
	v_mfma_f32_16x16x32_bf16 v[128:131], v[0:3], v[92:95], 0
	v_mfma_f32_16x16x32_bf16 v[148:151], v[4:7], v[108:111], v[128:131]
	v_mfma_f32_16x16x32_bf16 v[128:131], v[8:11], v[92:95], 0
	v_mfma_f32_16x16x32_bf16 v[156:159], v[12:15], v[108:111], v[128:131]
	v_mfma_f32_16x16x32_bf16 v[128:131], v[0:3], v[112:115], 0
	v_mfma_f32_16x16x32_bf16 v[0:3], v[0:3], v[120:123], 0
	v_mfma_f32_16x16x32_bf16 v[160:163], v[4:7], v[116:119], v[128:131]
	v_mfma_f32_16x16x32_bf16 v[0:3], v[4:7], v[124:127], v[0:3]
	v_mfma_f32_16x16x32_bf16 v[4:7], v[8:11], v[120:123], 0
	v_mfma_f32_16x16x32_bf16 v[128:131], v[8:11], v[112:115], 0
	v_mfma_f32_16x16x32_bf16 v[4:7], v[12:15], v[124:127], v[4:7]
	v_mfma_f32_16x16x32_bf16 v[164:167], v[12:15], v[116:119], v[128:131]
	v_mfma_f32_16x16x32_bf16 v[8:11], v[16:19], v[60:63], 0
	v_mfma_f32_16x16x32_bf16 v[168:171], v[20:23], v[88:91], v[8:11]
	v_mfma_f32_16x16x32_bf16 v[8:11], v[24:27], v[60:63], 0
	v_mfma_f32_16x16x32_bf16 v[172:175], v[28:31], v[88:91], v[8:11]
	v_mfma_f32_16x16x32_bf16 v[8:11], v[16:19], v[92:95], 0
	v_mfma_f32_16x16x32_bf16 v[176:179], v[20:23], v[108:111], v[8:11]
	v_mfma_f32_16x16x32_bf16 v[8:11], v[24:27], v[92:95], 0
	v_mfma_f32_16x16x32_bf16 v[108:111], v[28:31], v[108:111], v[8:11]
	v_mfma_f32_16x16x32_bf16 v[8:11], v[16:19], v[112:115], 0
	v_mfma_f32_16x16x32_bf16 v[180:183], v[20:23], v[116:119], v[8:11]
	v_mfma_f32_16x16x32_bf16 v[8:11], v[24:27], v[112:115], 0
	v_mfma_f32_16x16x32_bf16 v[116:119], v[28:31], v[116:119], v[8:11]
	v_mfma_f32_16x16x32_bf16 v[8:11], v[16:19], v[120:123], 0
	v_mfma_f32_16x16x32_bf16 v[184:187], v[20:23], v[124:127], v[8:11]
	v_mfma_f32_16x16x32_bf16 v[8:11], v[24:27], v[120:123], 0
	v_mfma_f32_16x16x32_bf16 v[124:127], v[28:31], v[124:127], v[8:11]
	s_barrier
	s_nop 4
	ds_read_b128 v[8:11], v220
	ds_read_b128 v[12:15], v220 offset:1024
	ds_read_b128 v[16:19], v220 offset:2048
	ds_read_b128 v[20:23], v220 offset:3072
	ds_read_b128 v[194:197], v221
	ds_read_b128 v[198:201], v221 offset:1024
	ds_read_b128 v[202:205], v221 offset:2048
	ds_read_b128 v[206:209], v221 offset:3072
	ds_read_b128 v[24:27], v219 offset:32768
	ds_read_b128 v[28:31], v219 offset:33792
	ds_read_b128 v[60:63], v219 offset:34816
	ds_read_b128 v[224:227], v219 offset:35840
	ds_read_b128 v[228:231], v219 offset:36864
	ds_read_b128 v[232:235], v219 offset:37888
	ds_read_b128 v[236:239], v219 offset:38912
	ds_read_b128 v[240:243], v219 offset:39936
	s_add_u32 s34, s34, 0x80100
	s_addc_u32 s35, s35, 0
	s_add_i32 m0, s48, 0x4000
	s_nop 0
	global_load_lds_dwordx4 v213, s[34:35]
	s_nop 0
	s_add_i32 m0, s48, 0x6000
	s_nop 0
	global_load_lds_dwordx4 v214, s[34:35]
	s_waitcnt vmcnt(8)
	s_waitcnt lgkmcnt(0)
	s_barrier
	v_mfma_f32_16x16x32_bf16 v[64:67], v[8:11], v[24:27], v[64:67]
	v_mfma_f32_16x16x32_bf16 v[152:155], v[12:15], v[28:31], v[64:67]
	v_mfma_f32_16x16x32_bf16 v[64:67], v[16:19], v[24:27], v[68:71]
	v_mfma_f32_16x16x32_bf16 v[144:147], v[20:23], v[28:31], v[64:67]
	v_mfma_f32_16x16x32_bf16 v[64:67], v[8:11], v[60:63], v[72:75]
	v_mfma_f32_16x16x32_bf16 v[120:123], v[12:15], v[224:227], v[64:67]
	v_mfma_f32_16x16x32_bf16 v[64:67], v[16:19], v[60:63], v[76:79]
	v_mfma_f32_16x16x32_bf16 v[112:115], v[20:23], v[224:227], v[64:67]
	v_mfma_f32_16x16x32_bf16 v[64:67], v[8:11], v[228:231], v[80:83]
	v_mfma_f32_16x16x32_bf16 v[92:95], v[12:15], v[232:235], v[64:67]
	v_mfma_f32_16x16x32_bf16 v[64:67], v[16:19], v[228:231], v[84:87]
	v_mfma_f32_16x16x32_bf16 v[88:91], v[20:23], v[232:235], v[64:67]
	v_mfma_f32_16x16x32_bf16 v[64:67], v[8:11], v[236:239], v[96:99]
	v_mfma_f32_16x16x32_bf16 v[76:79], v[12:15], v[240:243], v[64:67]
	v_mfma_f32_16x16x32_bf16 v[64:67], v[16:19], v[236:239], v[100:103]
	v_mfma_f32_16x16x32_bf16 v[72:75], v[20:23], v[240:243], v[64:67]
	v_mfma_f32_16x16x32_bf16 v[64:67], v[194:197], v[24:27], v[104:107]
	v_mfma_f32_16x16x32_bf16 v[24:27], v[202:205], v[24:27], v[32:35]
	v_mfma_f32_16x16x32_bf16 v[128:131], v[206:209], v[28:31], v[24:27]
	v_mfma_f32_16x16x32_bf16 v[24:27], v[194:197], v[60:63], v[36:39]
	v_mfma_f32_16x16x32_bf16 v[104:107], v[198:201], v[224:227], v[24:27]
	v_mfma_f32_16x16x32_bf16 v[24:27], v[202:205], v[60:63], v[40:43]
	v_mfma_f32_16x16x32_bf16 v[96:99], v[206:209], v[224:227], v[24:27]
	v_mfma_f32_16x16x32_bf16 v[24:27], v[194:197], v[228:231], v[44:47]
	v_mfma_f32_16x16x32_bf16 v[84:87], v[198:201], v[232:235], v[24:27]
	v_mfma_f32_16x16x32_bf16 v[24:27], v[202:205], v[228:231], v[48:51]
	v_mfma_f32_16x16x32_bf16 v[80:83], v[206:209], v[232:235], v[24:27]
	v_mfma_f32_16x16x32_bf16 v[24:27], v[194:197], v[236:239], v[52:55]
	v_mfma_f32_16x16x32_bf16 v[68:71], v[198:201], v[240:243], v[24:27]
	v_mfma_f32_16x16x32_bf16 v[24:27], v[202:205], v[236:239], v[56:59]
	v_mfma_f32_16x16x32_bf16 v[136:139], v[198:201], v[28:31], v[64:67]
	v_mfma_f32_16x16x32_bf16 v[64:67], v[206:209], v[240:243], v[24:27]
	s_barrier
	ds_read_b128 v[32:35], v219 offset:49152
	ds_read_b128 v[36:39], v219 offset:50176
	ds_read_b128 v[100:103], v219 offset:51200
	ds_read_b128 v[224:227], v219 offset:52224
	ds_read_b128 v[228:231], v219 offset:53248
	ds_read_b128 v[232:235], v219 offset:54272
	ds_read_b128 v[236:239], v219 offset:55296
	ds_read_b128 v[240:243], v219 offset:56320
	s_add_i32 m0, s48, 0x18000
	s_nop 0
	global_load_lds_dwordx4 v213, s[40:41]
	s_nop 0
	s_add_i32 m0, s48, 0x1a000
	s_nop 0
	global_load_lds_dwordx4 v214, s[40:41]
	s_add_u32 s34, s30, 0x80180
	s_addc_u32 s35, s31, 0
	s_add_i32 m0, s48, 0x1c000
	s_nop 0
	global_load_lds_dwordx4 v213, s[34:35]
	s_nop 0
	s_add_i32 m0, s48, 0x1e000
	s_nop 0
	global_load_lds_dwordx4 v214, s[34:35]
	s_nop 0
	s_add_i32 m0, s48, 0x8000
	s_nop 0
	global_load_lds_dwordx4 v213, s[38:39]
	s_nop 0
	s_add_i32 m0, s48, 0xa000
	s_nop 0
	global_load_lds_dwordx4 v214, s[38:39]
	s_waitcnt vmcnt(8)
	s_waitcnt lgkmcnt(0)
	s_barrier
	v_mfma_f32_16x16x32_bf16 v[24:27], v[8:11], v[32:35], v[132:135]
	v_mfma_f32_16x16x32_bf16 v[60:63], v[12:15], v[36:39], v[24:27]
	v_mfma_f32_16x16x32_bf16 v[24:27], v[16:19], v[32:35], v[140:143]
	v_mfma_f32_16x16x32_bf16 v[56:59], v[20:23], v[36:39], v[24:27]
	v_mfma_f32_16x16x32_bf16 v[24:27], v[8:11], v[100:103], v[148:151]
	v_mfma_f32_16x16x32_bf16 v[44:47], v[12:15], v[224:227], v[24:27]
	v_mfma_f32_16x16x32_bf16 v[24:27], v[16:19], v[100:103], v[156:159]
	v_mfma_f32_16x16x32_bf16 v[40:43], v[20:23], v[224:227], v[24:27]
	v_mfma_f32_16x16x32_bf16 v[24:27], v[8:11], v[228:231], v[160:163]
	v_mfma_f32_16x16x32_bf16 v[0:3], v[8:11], v[236:239], v[0:3]
	v_mfma_f32_16x16x32_bf16 v[28:31], v[12:15], v[232:235], v[24:27]
	v_mfma_f32_16x16x32_bf16 v[24:27], v[16:19], v[228:231], v[164:167]
	v_mfma_f32_16x16x32_bf16 v[12:15], v[12:15], v[240:243], v[0:3]
	v_mfma_f32_16x16x32_bf16 v[0:3], v[16:19], v[236:239], v[4:7]
	v_mfma_f32_16x16x32_bf16 v[24:27], v[20:23], v[232:235], v[24:27]
	v_mfma_f32_16x16x32_bf16 v[8:11], v[20:23], v[240:243], v[0:3]
	v_mfma_f32_16x16x32_bf16 v[0:3], v[194:197], v[32:35], v[168:171]
	v_mfma_f32_16x16x32_bf16 v[52:55], v[198:201], v[36:39], v[0:3]
	v_mfma_f32_16x16x32_bf16 v[0:3], v[202:205], v[32:35], v[172:175]
	v_mfma_f32_16x16x32_bf16 v[48:51], v[206:209], v[36:39], v[0:3]
	v_mfma_f32_16x16x32_bf16 v[0:3], v[194:197], v[100:103], v[176:179]
	v_mfma_f32_16x16x32_bf16 v[36:39], v[198:201], v[224:227], v[0:3]
	v_mfma_f32_16x16x32_bf16 v[0:3], v[202:205], v[100:103], v[108:111]
	v_mfma_f32_16x16x32_bf16 v[32:35], v[206:209], v[224:227], v[0:3]
	v_mfma_f32_16x16x32_bf16 v[0:3], v[194:197], v[228:231], v[180:183]
	v_mfma_f32_16x16x32_bf16 v[20:23], v[198:201], v[232:235], v[0:3]
	v_mfma_f32_16x16x32_bf16 v[0:3], v[202:205], v[228:231], v[116:119]
	v_mfma_f32_16x16x32_bf16 v[16:19], v[206:209], v[232:235], v[0:3]
	v_mfma_f32_16x16x32_bf16 v[0:3], v[194:197], v[236:239], v[184:187]
	v_mfma_f32_16x16x32_bf16 v[4:7], v[198:201], v[240:243], v[0:3]
	v_mfma_f32_16x16x32_bf16 v[0:3], v[202:205], v[236:239], v[124:127]
	v_mfma_f32_16x16x32_bf16 v[0:3], v[206:209], v[240:243], v[0:3]
	s_barrier
	s_add_u32 s59, s30, 0x200
	s_addc_u32 s60, s31, 0
	s_mov_b32 s61, 0
.LBB0_603:
	ds_read_b128 v[100:103], v217
	ds_read_b128 v[108:111], v217 offset:1024
	ds_read_b128 v[116:119], v217 offset:2048
	ds_read_b128 v[124:127], v217 offset:3072
	ds_read_b128 v[132:135], v218
	ds_read_b128 v[140:143], v218 offset:1024
	ds_read_b128 v[148:151], v218 offset:2048
	ds_read_b128 v[156:159], v218 offset:3072
	s_add_u32 s30, s36, 0x100
	s_addc_u32 s31, s37, 0
	s_cmp_eq_u32 s61, 28
	s_cselect_b32 s42, s9, s30
	s_cselect_b32 s43, s7, s31
	s_cselect_b32 s38, s25, s59
	s_cselect_b32 s39, s23, s60
	s_add_u32 s34, s42, 0x80
	s_addc_u32 s35, s43, 0
	ds_read_b128 v[160:163], v219
	ds_read_b128 v[164:167], v219 offset:1024
	ds_read_b128 v[168:171], v219 offset:2048
	ds_read_b128 v[172:175], v219 offset:3072
	ds_read_b128 v[176:179], v219 offset:4096
	ds_read_b128 v[180:183], v219 offset:5120
	ds_read_b128 v[184:187], v219 offset:6144
	ds_read_b128 v[194:197], v219 offset:7168
	s_add_u32 s40, s38, 0x80
	s_addc_u32 s41, s39, 0
	s_add_u32 s36, s36, 0x80080
	s_addc_u32 s37, s37, 0
	s_add_i32 m0, s48, 0xc000
	s_nop 0
	global_load_lds_dwordx4 v213, s[36:37]
	s_nop 0
	s_add_i32 m0, s48, 0xe000
	s_nop 0
	global_load_lds_dwordx4 v214, s[36:37]
	s_waitcnt vmcnt(8)
	s_waitcnt lgkmcnt(0)
	s_barrier
	v_mfma_f32_16x16x32_bf16 v[152:155], v[100:103], v[160:163], v[152:155]
	v_mfma_f32_16x16x32_bf16 v[144:147], v[116:119], v[160:163], v[144:147]
	v_mfma_f32_16x16x32_bf16 v[120:123], v[100:103], v[168:171], v[120:123]
	v_mfma_f32_16x16x32_bf16 v[112:115], v[116:119], v[168:171], v[112:115]
	v_mfma_f32_16x16x32_bf16 v[92:95], v[100:103], v[176:179], v[92:95]
	v_mfma_f32_16x16x32_bf16 v[88:91], v[116:119], v[176:179], v[88:91]
	v_mfma_f32_16x16x32_bf16 v[76:79], v[100:103], v[184:187], v[76:79]
	v_mfma_f32_16x16x32_bf16 v[72:75], v[116:119], v[184:187], v[72:75]
	v_mfma_f32_16x16x32_bf16 v[152:155], v[108:111], v[164:167], v[152:155]
	v_mfma_f32_16x16x32_bf16 v[144:147], v[124:127], v[164:167], v[144:147]
	v_mfma_f32_16x16x32_bf16 v[120:123], v[108:111], v[172:175], v[120:123]
	v_mfma_f32_16x16x32_bf16 v[112:115], v[124:127], v[172:175], v[112:115]
	v_mfma_f32_16x16x32_bf16 v[92:95], v[108:111], v[180:183], v[92:95]
	v_mfma_f32_16x16x32_bf16 v[88:91], v[124:127], v[180:183], v[88:91]
	v_mfma_f32_16x16x32_bf16 v[76:79], v[108:111], v[194:197], v[76:79]
	v_mfma_f32_16x16x32_bf16 v[72:75], v[124:127], v[194:197], v[72:75]
	v_mfma_f32_16x16x32_bf16 v[136:139], v[132:135], v[160:163], v[136:139]
	v_mfma_f32_16x16x32_bf16 v[128:131], v[148:151], v[160:163], v[128:131]
	v_mfma_f32_16x16x32_bf16 v[104:107], v[132:135], v[168:171], v[104:107]
	v_mfma_f32_16x16x32_bf16 v[96:99], v[148:151], v[168:171], v[96:99]
	v_mfma_f32_16x16x32_bf16 v[84:87], v[132:135], v[176:179], v[84:87]
	v_mfma_f32_16x16x32_bf16 v[80:83], v[148:151], v[176:179], v[80:83]
	v_mfma_f32_16x16x32_bf16 v[68:71], v[132:135], v[184:187], v[68:71]
	v_mfma_f32_16x16x32_bf16 v[64:67], v[148:151], v[184:187], v[64:67]
	v_mfma_f32_16x16x32_bf16 v[136:139], v[140:143], v[164:167], v[136:139]
	v_mfma_f32_16x16x32_bf16 v[128:131], v[156:159], v[164:167], v[128:131]
	v_mfma_f32_16x16x32_bf16 v[104:107], v[140:143], v[172:175], v[104:107]
	v_mfma_f32_16x16x32_bf16 v[96:99], v[156:159], v[172:175], v[96:99]
	v_mfma_f32_16x16x32_bf16 v[84:87], v[140:143], v[180:183], v[84:87]
	v_mfma_f32_16x16x32_bf16 v[80:83], v[156:159], v[180:183], v[80:83]
	v_mfma_f32_16x16x32_bf16 v[68:71], v[140:143], v[194:197], v[68:71]
	v_mfma_f32_16x16x32_bf16 v[64:67], v[156:159], v[194:197], v[64:67]
	s_barrier
	ds_read_b128 v[160:163], v219 offset:16384
	ds_read_b128 v[164:167], v219 offset:17408
	ds_read_b128 v[168:171], v219 offset:18432
	ds_read_b128 v[172:175], v219 offset:19456
	ds_read_b128 v[176:179], v219 offset:20480
	ds_read_b128 v[180:183], v219 offset:21504
	ds_read_b128 v[184:187], v219 offset:22528
	ds_read_b128 v[194:197], v219 offset:23552
	s_add_i32 m0, s48, 0x10000
	s_nop 0
	global_load_lds_dwordx4 v213, s[38:39]
	s_nop 0
	s_add_i32 m0, s48, 0x12000
	s_nop 0
	global_load_lds_dwordx4 v214, s[38:39]
	s_add_u32 s36, s38, 0x80000
	s_addc_u32 s37, s39, 0
	s_add_i32 m0, s48, 0x14000
	s_nop 0
	global_load_lds_dwordx4 v213, s[36:37]
	s_nop 0
	s_add_i32 m0, s48, 0x16000
	s_nop 0
	global_load_lds_dwordx4 v214, s[36:37]
	s_nop 0
	s_add_i32 m0, s48, 0
	s_nop 0
	global_load_lds_dwordx4 v213, s[42:43]
	s_nop 0
	s_add_i32 m0, s48, 0x2000
	s_nop 0
	global_load_lds_dwordx4 v214, s[42:43]
	s_waitcnt vmcnt(8)
	s_waitcnt lgkmcnt(0)
	s_barrier
	v_mfma_f32_16x16x32_bf16 v[60:63], v[100:103], v[160:163], v[60:63]
	v_mfma_f32_16x16x32_bf16 v[56:59], v[116:119], v[160:163], v[56:59]
	v_mfma_f32_16x16x32_bf16 v[44:47], v[100:103], v[168:171], v[44:47]
	v_mfma_f32_16x16x32_bf16 v[40:43], v[116:119], v[168:171], v[40:43]
	v_mfma_f32_16x16x32_bf16 v[28:31], v[100:103], v[176:179], v[28:31]
	v_mfma_f32_16x16x32_bf16 v[24:27], v[116:119], v[176:179], v[24:27]
	v_mfma_f32_16x16x32_bf16 v[12:15], v[100:103], v[184:187], v[12:15]
	v_mfma_f32_16x16x32_bf16 v[8:11], v[116:119], v[184:187], v[8:11]
	v_mfma_f32_16x16x32_bf16 v[60:63], v[108:111], v[164:167], v[60:63]
	v_mfma_f32_16x16x32_bf16 v[56:59], v[124:127], v[164:167], v[56:59]
	v_mfma_f32_16x16x32_bf16 v[44:47], v[108:111], v[172:175], v[44:47]
	v_mfma_f32_16x16x32_bf16 v[40:43], v[124:127], v[172:175], v[40:43]
	v_mfma_f32_16x16x32_bf16 v[28:31], v[108:111], v[180:183], v[28:31]
	v_mfma_f32_16x16x32_bf16 v[24:27], v[124:127], v[180:183], v[24:27]
	v_mfma_f32_16x16x32_bf16 v[12:15], v[108:111], v[194:197], v[12:15]
	v_mfma_f32_16x16x32_bf16 v[8:11], v[124:127], v[194:197], v[8:11]
	v_mfma_f32_16x16x32_bf16 v[52:55], v[132:135], v[160:163], v[52:55]
	v_mfma_f32_16x16x32_bf16 v[48:51], v[148:151], v[160:163], v[48:51]
	v_mfma_f32_16x16x32_bf16 v[36:39], v[132:135], v[168:171], v[36:39]
	v_mfma_f32_16x16x32_bf16 v[32:35], v[148:151], v[168:171], v[32:35]
	v_mfma_f32_16x16x32_bf16 v[20:23], v[132:135], v[176:179], v[20:23]
	v_mfma_f32_16x16x32_bf16 v[16:19], v[148:151], v[176:179], v[16:19]
	v_mfma_f32_16x16x32_bf16 v[4:7], v[132:135], v[184:187], v[4:7]
	v_mfma_f32_16x16x32_bf16 v[0:3], v[148:151], v[184:187], v[0:3]
	v_mfma_f32_16x16x32_bf16 v[52:55], v[140:143], v[164:167], v[52:55]
	v_mfma_f32_16x16x32_bf16 v[48:51], v[156:159], v[164:167], v[48:51]
	v_mfma_f32_16x16x32_bf16 v[36:39], v[140:143], v[172:175], v[36:39]
	v_mfma_f32_16x16x32_bf16 v[32:35], v[156:159], v[172:175], v[32:35]
	v_mfma_f32_16x16x32_bf16 v[20:23], v[140:143], v[180:183], v[20:23]
	v_mfma_f32_16x16x32_bf16 v[16:19], v[156:159], v[180:183], v[16:19]
	v_mfma_f32_16x16x32_bf16 v[4:7], v[140:143], v[194:197], v[4:7]
	v_mfma_f32_16x16x32_bf16 v[0:3], v[156:159], v[194:197], v[0:3]
	s_barrier
	ds_read_b128 v[100:103], v220
	ds_read_b128 v[108:111], v220 offset:1024
	ds_read_b128 v[116:119], v220 offset:2048
	ds_read_b128 v[124:127], v220 offset:3072
	ds_read_b128 v[132:135], v221
	ds_read_b128 v[140:143], v221 offset:1024
	ds_read_b128 v[148:151], v221 offset:2048
	ds_read_b128 v[156:159], v221 offset:3072
	ds_read_b128 v[160:163], v219 offset:32768
	ds_read_b128 v[164:167], v219 offset:33792
	ds_read_b128 v[168:171], v219 offset:34816
	ds_read_b128 v[172:175], v219 offset:35840
	ds_read_b128 v[176:179], v219 offset:36864
	ds_read_b128 v[180:183], v219 offset:37888
	ds_read_b128 v[184:187], v219 offset:38912
	ds_read_b128 v[194:197], v219 offset:39936
	s_add_u32 s36, s42, 0x80000
	s_addc_u32 s37, s43, 0
	s_add_i32 m0, s48, 0x4000
	s_nop 0
	global_load_lds_dwordx4 v213, s[36:37]
	s_nop 0
	s_add_i32 m0, s48, 0x6000
	s_nop 0
	global_load_lds_dwordx4 v214, s[36:37]
	s_waitcnt vmcnt(8)
	s_waitcnt lgkmcnt(0)
	s_barrier
	v_mfma_f32_16x16x32_bf16 v[152:155], v[100:103], v[160:163], v[152:155]
	v_mfma_f32_16x16x32_bf16 v[144:147], v[116:119], v[160:163], v[144:147]
	v_mfma_f32_16x16x32_bf16 v[120:123], v[100:103], v[168:171], v[120:123]
	v_mfma_f32_16x16x32_bf16 v[112:115], v[116:119], v[168:171], v[112:115]
	v_mfma_f32_16x16x32_bf16 v[92:95], v[100:103], v[176:179], v[92:95]
	v_mfma_f32_16x16x32_bf16 v[88:91], v[116:119], v[176:179], v[88:91]
	v_mfma_f32_16x16x32_bf16 v[76:79], v[100:103], v[184:187], v[76:79]
	v_mfma_f32_16x16x32_bf16 v[72:75], v[116:119], v[184:187], v[72:75]
	v_mfma_f32_16x16x32_bf16 v[152:155], v[108:111], v[164:167], v[152:155]
	v_mfma_f32_16x16x32_bf16 v[144:147], v[124:127], v[164:167], v[144:147]
	v_mfma_f32_16x16x32_bf16 v[120:123], v[108:111], v[172:175], v[120:123]
	v_mfma_f32_16x16x32_bf16 v[112:115], v[124:127], v[172:175], v[112:115]
	v_mfma_f32_16x16x32_bf16 v[92:95], v[108:111], v[180:183], v[92:95]
	v_mfma_f32_16x16x32_bf16 v[88:91], v[124:127], v[180:183], v[88:91]
	v_mfma_f32_16x16x32_bf16 v[76:79], v[108:111], v[194:197], v[76:79]
	v_mfma_f32_16x16x32_bf16 v[72:75], v[124:127], v[194:197], v[72:75]
	v_mfma_f32_16x16x32_bf16 v[136:139], v[132:135], v[160:163], v[136:139]
	v_mfma_f32_16x16x32_bf16 v[128:131], v[148:151], v[160:163], v[128:131]
	v_mfma_f32_16x16x32_bf16 v[104:107], v[132:135], v[168:171], v[104:107]
	v_mfma_f32_16x16x32_bf16 v[96:99], v[148:151], v[168:171], v[96:99]
	v_mfma_f32_16x16x32_bf16 v[84:87], v[132:135], v[176:179], v[84:87]
	v_mfma_f32_16x16x32_bf16 v[80:83], v[148:151], v[176:179], v[80:83]
	v_mfma_f32_16x16x32_bf16 v[68:71], v[132:135], v[184:187], v[68:71]
	v_mfma_f32_16x16x32_bf16 v[64:67], v[148:151], v[184:187], v[64:67]
	v_mfma_f32_16x16x32_bf16 v[136:139], v[140:143], v[164:167], v[136:139]
	v_mfma_f32_16x16x32_bf16 v[128:131], v[156:159], v[164:167], v[128:131]
	v_mfma_f32_16x16x32_bf16 v[104:107], v[140:143], v[172:175], v[104:107]
	v_mfma_f32_16x16x32_bf16 v[96:99], v[156:159], v[172:175], v[96:99]
	v_mfma_f32_16x16x32_bf16 v[84:87], v[140:143], v[180:183], v[84:87]
	v_mfma_f32_16x16x32_bf16 v[80:83], v[156:159], v[180:183], v[80:83]
	v_mfma_f32_16x16x32_bf16 v[68:71], v[140:143], v[194:197], v[68:71]
	v_mfma_f32_16x16x32_bf16 v[64:67], v[156:159], v[194:197], v[64:67]
	s_barrier
	ds_read_b128 v[160:163], v219 offset:49152
	ds_read_b128 v[164:167], v219 offset:50176
	ds_read_b128 v[168:171], v219 offset:51200
	ds_read_b128 v[172:175], v219 offset:52224
	ds_read_b128 v[176:179], v219 offset:53248
	ds_read_b128 v[180:183], v219 offset:54272
	ds_read_b128 v[184:187], v219 offset:55296
	ds_read_b128 v[194:197], v219 offset:56320
	s_add_i32 m0, s48, 0x18000
	s_nop 0
	global_load_lds_dwordx4 v213, s[40:41]
	s_nop 0
	s_add_i32 m0, s48, 0x1a000
	s_nop 0
	global_load_lds_dwordx4 v214, s[40:41]
	s_add_u32 s36, s38, 0x80080
	s_addc_u32 s37, s39, 0
	s_add_i32 m0, s48, 0x1c000
	s_nop 0
	global_load_lds_dwordx4 v213, s[36:37]
	s_nop 0
	s_add_i32 m0, s48, 0x1e000
	s_nop 0
	global_load_lds_dwordx4 v214, s[36:37]
	s_nop 0
	s_add_i32 m0, s48, 0x8000
	s_nop 0
	global_load_lds_dwordx4 v213, s[34:35]
	s_nop 0
	s_add_i32 m0, s48, 0xa000
	s_nop 0
	global_load_lds_dwordx4 v214, s[34:35]
	s_waitcnt vmcnt(8)
	s_waitcnt lgkmcnt(0)
	s_barrier
	v_mfma_f32_16x16x32_bf16 v[60:63], v[100:103], v[160:163], v[60:63]
	v_mfma_f32_16x16x32_bf16 v[56:59], v[116:119], v[160:163], v[56:59]
	v_mfma_f32_16x16x32_bf16 v[44:47], v[100:103], v[168:171], v[44:47]
	v_mfma_f32_16x16x32_bf16 v[40:43], v[116:119], v[168:171], v[40:43]
	v_mfma_f32_16x16x32_bf16 v[28:31], v[100:103], v[176:179], v[28:31]
	v_mfma_f32_16x16x32_bf16 v[24:27], v[116:119], v[176:179], v[24:27]
	v_mfma_f32_16x16x32_bf16 v[12:15], v[100:103], v[184:187], v[12:15]
	v_mfma_f32_16x16x32_bf16 v[8:11], v[116:119], v[184:187], v[8:11]
	v_mfma_f32_16x16x32_bf16 v[60:63], v[108:111], v[164:167], v[60:63]
	v_mfma_f32_16x16x32_bf16 v[56:59], v[124:127], v[164:167], v[56:59]
	v_mfma_f32_16x16x32_bf16 v[44:47], v[108:111], v[172:175], v[44:47]
	v_mfma_f32_16x16x32_bf16 v[40:43], v[124:127], v[172:175], v[40:43]
	v_mfma_f32_16x16x32_bf16 v[28:31], v[108:111], v[180:183], v[28:31]
	v_mfma_f32_16x16x32_bf16 v[24:27], v[124:127], v[180:183], v[24:27]
	v_mfma_f32_16x16x32_bf16 v[12:15], v[108:111], v[194:197], v[12:15]
	v_mfma_f32_16x16x32_bf16 v[8:11], v[124:127], v[194:197], v[8:11]
	v_mfma_f32_16x16x32_bf16 v[52:55], v[132:135], v[160:163], v[52:55]
	v_mfma_f32_16x16x32_bf16 v[48:51], v[148:151], v[160:163], v[48:51]
	v_mfma_f32_16x16x32_bf16 v[36:39], v[132:135], v[168:171], v[36:39]
	v_mfma_f32_16x16x32_bf16 v[32:35], v[148:151], v[168:171], v[32:35]
	v_mfma_f32_16x16x32_bf16 v[20:23], v[132:135], v[176:179], v[20:23]
	v_mfma_f32_16x16x32_bf16 v[16:19], v[148:151], v[176:179], v[16:19]
	v_mfma_f32_16x16x32_bf16 v[4:7], v[132:135], v[184:187], v[4:7]
	v_mfma_f32_16x16x32_bf16 v[0:3], v[148:151], v[184:187], v[0:3]
	v_mfma_f32_16x16x32_bf16 v[52:55], v[140:143], v[164:167], v[52:55]
	v_mfma_f32_16x16x32_bf16 v[48:51], v[156:159], v[164:167], v[48:51]
	v_mfma_f32_16x16x32_bf16 v[36:39], v[140:143], v[172:175], v[36:39]
	v_mfma_f32_16x16x32_bf16 v[32:35], v[156:159], v[172:175], v[32:35]
	v_mfma_f32_16x16x32_bf16 v[20:23], v[140:143], v[180:183], v[20:23]
	v_mfma_f32_16x16x32_bf16 v[16:19], v[156:159], v[180:183], v[16:19]
	v_mfma_f32_16x16x32_bf16 v[4:7], v[140:143], v[194:197], v[4:7]
	v_mfma_f32_16x16x32_bf16 v[0:3], v[156:159], v[194:197], v[0:3]
	s_barrier
	s_add_i32 s61, s61, 2
	s_add_u32 s59, s59, 0x100
	s_addc_u32 s60, s60, 0
	s_cmp_gt_u32 s61, 29
	s_mov_b64 s[36:37], s[30:31]
	s_cbranch_scc0 .LBB0_603
	s_and_b64 vcc, exec, s[20:21]
	s_cbranch_vccz .LBB0_606
	s_barrier

.LBB0_752:
	s_ashr_i32 s17, s16, 31
	s_lshl_b64 s[18:19], s[16:17], 19
	s_add_u32 s18, s40, s18
	s_addc_u32 s19, s41, s19
	s_and_b64 s[20:21], s[4:5], exec
	s_cselect_b32 s58, s19, s29
	s_cselect_b32 s59, s18, s28
	s_ashr_i32 s15, s14, 31
	s_lshl_b64 s[20:21], s[14:15], 19
	s_add_u32 s20, s42, s20
	s_addc_u32 s21, s43, s21
	s_and_b64 s[26:27], s[4:5], exec
	ds_read_b128 v[0:3], v204 offset:3072
	ds_read_b128 v[4:7], v204 offset:2048
	ds_read_b128 v[8:11], v204 offset:1024
	ds_read_b128 v[12:15], v204
	ds_read_b128 v[16:19], v205 offset:3072
	ds_read_b128 v[20:23], v205 offset:2048
	ds_read_b128 v[24:27], v205 offset:1024
	ds_read_b128 v[28:31], v205
	s_cselect_b32 s15, s21, s25
	s_cselect_b32 s60, s20, s24
	s_lshl_b32 s26, s55, 11
	s_and_b32 s26, s26, 0x800
	s_or_b32 s38, s26, s49
	s_lshl_b64 s[30:31], s[16:17], 11
	s_add_u32 s26, s28, 0x100
	s_addc_u32 s27, s29, 0
	s_add_u32 s62, s24, 0x100
	s_addc_u32 s63, s25, 0
	s_add_u32 s34, s28, 0x180
	s_addc_u32 s35, s29, 0
	s_add_u32 s36, s24, 0x180
	s_addc_u32 s37, s25, 0
	ds_read_b128 v[32:35], v206
	ds_read_b128 v[36:39], v206 offset:1024
	ds_read_b128 v[40:43], v206 offset:2048
	ds_read_b128 v[44:47], v206 offset:3072
	ds_read_b128 v[48:51], v206 offset:4096
	ds_read_b128 v[52:55], v206 offset:5120
	ds_read_b128 v[56:59], v206 offset:6144
	ds_read_b128 v[60:63], v206 offset:7168
	s_add_u32 s66, s28, 0x40080
	s_addc_u32 s67, s29, 0
	s_add_i32 m0, s46, 0xc000
	s_nop 0
	global_load_lds_dwordx4 v199, s[66:67]
	s_nop 0
	s_add_i32 m0, s46, 0xe000
	s_nop 0
	global_load_lds_dwordx4 v201, s[66:67]
	s_waitcnt vmcnt(8)
	s_waitcnt lgkmcnt(0)
	s_barrier
	s_waitcnt lgkmcnt(7)
	v_mfma_i32_16x16x64_i8 v[64:67], v[28:31], v[32:35], 0
	s_mov_b32 s17, 0
	v_mfma_i32_16x16x64_i8 v[68:71], v[20:23], v[32:35], 0
	s_waitcnt lgkmcnt(5)
	v_mfma_i32_16x16x64_i8 v[72:75], v[28:31], v[40:43], 0
	v_mfma_i32_16x16x64_i8 v[132:135], v[24:27], v[36:39], v[64:67]
	v_mfma_i32_16x16x64_i8 v[136:139], v[16:19], v[36:39], v[68:71]
	s_waitcnt lgkmcnt(4)
	v_mfma_i32_16x16x64_i8 v[144:147], v[24:27], v[44:47], v[72:75]
	v_mfma_i32_16x16x64_i8 v[76:79], v[20:23], v[40:43], 0
	s_waitcnt lgkmcnt(3)
	v_mfma_i32_16x16x64_i8 v[80:83], v[28:31], v[48:51], 0
	v_mfma_i32_16x16x64_i8 v[84:87], v[20:23], v[48:51], 0
	s_waitcnt lgkmcnt(1)
	v_mfma_i32_16x16x64_i8 v[88:91], v[28:31], v[56:59], 0
	v_mfma_i32_16x16x64_i8 v[92:95], v[20:23], v[56:59], 0
	v_mfma_i32_16x16x64_i8 v[76:79], v[16:19], v[44:47], v[76:79]
	v_mfma_i32_16x16x64_i8 v[80:83], v[24:27], v[52:55], v[80:83]
	v_mfma_i32_16x16x64_i8 v[84:87], v[16:19], v[52:55], v[84:87]
	s_waitcnt lgkmcnt(0)
	v_mfma_i32_16x16x64_i8 v[88:91], v[24:27], v[60:63], v[88:91]
	v_mfma_i32_16x16x64_i8 v[92:95], v[16:19], v[60:63], v[92:95]
	v_mfma_i32_16x16x64_i8 v[96:99], v[12:15], v[32:35], 0
	v_mfma_i32_16x16x64_i8 v[32:35], v[4:7], v[32:35], 0
	v_mfma_i32_16x16x64_i8 v[96:99], v[8:11], v[36:39], v[96:99]
	v_mfma_i32_16x16x64_i8 v[32:35], v[0:3], v[36:39], v[32:35]
	v_mfma_i32_16x16x64_i8 v[36:39], v[12:15], v[40:43], 0
	v_mfma_i32_16x16x64_i8 v[40:43], v[4:7], v[40:43], 0
	v_mfma_i32_16x16x64_i8 v[36:39], v[8:11], v[44:47], v[36:39]
	v_mfma_i32_16x16x64_i8 v[40:43], v[0:3], v[44:47], v[40:43]
	v_mfma_i32_16x16x64_i8 v[44:47], v[12:15], v[48:51], 0
	v_mfma_i32_16x16x64_i8 v[48:51], v[4:7], v[48:51], 0
	v_mfma_i32_16x16x64_i8 v[44:47], v[8:11], v[52:55], v[44:47]
	v_mfma_i32_16x16x64_i8 v[48:51], v[0:3], v[52:55], v[48:51]
	v_mfma_i32_16x16x64_i8 v[52:55], v[12:15], v[56:59], 0
	v_mfma_i32_16x16x64_i8 v[56:59], v[4:7], v[56:59], 0
	v_mfma_i32_16x16x64_i8 v[52:55], v[8:11], v[60:63], v[52:55]
	v_mfma_i32_16x16x64_i8 v[56:59], v[0:3], v[60:63], v[56:59]
	s_barrier
	ds_read_b128 v[60:63], v206 offset:16384
	ds_read_b128 v[100:103], v206 offset:17408
	ds_read_b128 v[104:107], v206 offset:18432
	ds_read_b128 v[108:111], v206 offset:19456
	ds_read_b128 v[112:115], v206 offset:20480
	ds_read_b128 v[116:119], v206 offset:21504
	ds_read_b128 v[120:123], v206 offset:22528
	ds_read_b128 v[124:127], v206 offset:23552
	s_add_i32 m0, s46, 0x10000
	s_nop 0
	global_load_lds_dwordx4 v200, s[62:63]
	s_nop 0
	s_add_i32 m0, s46, 0x12000
	s_nop 0
	global_load_lds_dwordx4 v202, s[62:63]
	s_add_u32 s62, s24, 0x40100
	s_addc_u32 s63, s25, 0
	s_add_i32 m0, s46, 0x14000
	s_nop 0
	global_load_lds_dwordx4 v200, s[62:63]
	s_nop 0
	s_add_i32 m0, s46, 0x16000
	s_nop 0
	global_load_lds_dwordx4 v202, s[62:63]
	s_nop 0
	s_add_i32 m0, s46, 0
	s_nop 0
	global_load_lds_dwordx4 v199, s[26:27]
	s_nop 0
	s_add_i32 m0, s46, 0x2000
	s_nop 0
	global_load_lds_dwordx4 v201, s[26:27]
	s_waitcnt vmcnt(8)
	s_waitcnt lgkmcnt(0)
	s_barrier
	v_mfma_i32_16x16x64_i8 v[128:131], v[28:31], v[60:63], 0
	v_mfma_i32_16x16x64_i8 v[210:213], v[24:27], v[100:103], v[128:131]
	v_mfma_i32_16x16x64_i8 v[128:131], v[20:23], v[60:63], 0
	v_mfma_i32_16x16x64_i8 v[214:217], v[16:19], v[100:103], v[128:131]
	v_mfma_i32_16x16x64_i8 v[128:131], v[28:31], v[104:107], 0
	v_mfma_i32_16x16x64_i8 v[218:221], v[24:27], v[108:111], v[128:131]
	v_mfma_i32_16x16x64_i8 v[128:131], v[20:23], v[104:107], 0
	v_mfma_i32_16x16x64_i8 v[222:225], v[16:19], v[108:111], v[128:131]
	v_mfma_i32_16x16x64_i8 v[128:131], v[28:31], v[112:115], 0
	v_mfma_i32_16x16x64_i8 v[226:229], v[24:27], v[116:119], v[128:131]
	v_mfma_i32_16x16x64_i8 v[128:131], v[20:23], v[112:115], 0
	v_mfma_i32_16x16x64_i8 v[28:31], v[28:31], v[120:123], 0
	v_mfma_i32_16x16x64_i8 v[20:23], v[20:23], v[120:123], 0
	v_mfma_i32_16x16x64_i8 v[230:233], v[16:19], v[116:119], v[128:131]
	v_mfma_i32_16x16x64_i8 v[24:27], v[24:27], v[124:127], v[28:31]
	v_mfma_i32_16x16x64_i8 v[20:23], v[16:19], v[124:127], v[20:23]
	v_mfma_i32_16x16x64_i8 v[16:19], v[12:15], v[60:63], 0
	v_mfma_i32_16x16x64_i8 v[28:31], v[8:11], v[100:103], v[16:19]
	v_mfma_i32_16x16x64_i8 v[16:19], v[4:7], v[60:63], 0
	v_mfma_i32_16x16x64_i8 v[60:63], v[0:3], v[100:103], v[16:19]
	v_mfma_i32_16x16x64_i8 v[16:19], v[12:15], v[104:107], 0
	v_mfma_i32_16x16x64_i8 v[100:103], v[8:11], v[108:111], v[16:19]
	v_mfma_i32_16x16x64_i8 v[16:19], v[4:7], v[104:107], 0
	v_mfma_i32_16x16x64_i8 v[234:237], v[0:3], v[108:111], v[16:19]
	v_mfma_i32_16x16x64_i8 v[16:19], v[12:15], v[112:115], 0
	v_mfma_i32_16x16x64_i8 v[238:241], v[8:11], v[116:119], v[16:19]
	v_mfma_i32_16x16x64_i8 v[16:19], v[4:7], v[112:115], 0
	v_mfma_i32_16x16x64_i8 v[12:15], v[12:15], v[120:123], 0
	v_mfma_i32_16x16x64_i8 v[4:7], v[4:7], v[120:123], 0
	v_mfma_i32_16x16x64_i8 v[12:15], v[8:11], v[124:127], v[12:15]
	v_mfma_i32_16x16x64_i8 v[4:7], v[0:3], v[124:127], v[4:7]
	v_mfma_i32_16x16x64_i8 v[242:245], v[0:3], v[116:119], v[16:19]
	s_barrier
	ds_read_b128 v[0:3], v207
	ds_read_b128 v[8:11], v207 offset:1024
	ds_read_b128 v[108:111], v207 offset:2048
	ds_read_b128 v[116:119], v207 offset:3072
	ds_read_b128 v[246:249], v208
	ds_read_b128 v[250:253], v208 offset:1024
	ds_read_b128 v[192:195], v208 offset:2048
	ds_read_b128 v[64:67], v208 offset:3072
	ds_read_b128 v[16:19], v206 offset:32768
	ds_read_b128 v[104:107], v206 offset:33792
	ds_read_b128 v[112:115], v206 offset:34816
	ds_read_b128 v[120:123], v206 offset:35840
	ds_read_b128 v[124:127], v206 offset:36864
	ds_read_b128 v[140:143], v206 offset:37888
	ds_read_b128 v[68:71], v206 offset:38912
	ds_read_b128 v[72:75], v206 offset:39936
	s_add_u32 s28, s28, 0x40100
	s_addc_u32 s29, s29, 0
	s_add_i32 m0, s46, 0x4000
	s_nop 0
	global_load_lds_dwordx4 v199, s[28:29]
	s_nop 0
	s_add_i32 m0, s46, 0x6000
	s_nop 0
	global_load_lds_dwordx4 v201, s[28:29]
	s_waitcnt vmcnt(8)
	s_waitcnt lgkmcnt(0)
	s_barrier
	v_mfma_i32_16x16x64_i8 v[76:79], v[108:111], v[112:115], v[76:79]
	v_mfma_i32_16x16x64_i8 v[128:131], v[0:3], v[16:19], v[132:135]
	v_mfma_i32_16x16x64_i8 v[160:163], v[116:119], v[120:123], v[76:79]
	v_mfma_i32_16x16x64_i8 v[76:79], v[0:3], v[124:127], v[80:83]
	v_mfma_i32_16x16x64_i8 v[184:187], v[8:11], v[104:107], v[128:131]
	v_mfma_i32_16x16x64_i8 v[128:131], v[108:111], v[16:19], v[136:139]
	v_mfma_i32_16x16x64_i8 v[152:155], v[8:11], v[140:143], v[76:79]
	v_mfma_i32_16x16x64_i8 v[76:79], v[108:111], v[124:127], v[84:87]
	v_mfma_i32_16x16x64_i8 v[176:179], v[116:119], v[104:107], v[128:131]
	v_mfma_i32_16x16x64_i8 v[128:131], v[0:3], v[112:115], v[144:147]
	v_mfma_i32_16x16x64_i8 v[144:147], v[116:119], v[140:143], v[76:79]
	v_mfma_i32_16x16x64_i8 v[76:79], v[0:3], v[68:71], v[88:91]
	v_mfma_i32_16x16x64_i8 v[136:139], v[8:11], v[72:75], v[76:79]
	v_mfma_i32_16x16x64_i8 v[76:79], v[108:111], v[68:71], v[92:95]
	v_mfma_i32_16x16x64_i8 v[168:171], v[8:11], v[120:123], v[128:131]
	v_mfma_i32_16x16x64_i8 v[128:131], v[116:119], v[72:75], v[76:79]
	v_mfma_i32_16x16x64_i8 v[76:79], v[246:249], v[16:19], v[96:99]
	v_mfma_i32_16x16x64_i8 v[16:19], v[192:195], v[16:19], v[32:35]
	v_mfma_i32_16x16x64_i8 v[180:183], v[64:67], v[104:107], v[16:19]
	v_mfma_i32_16x16x64_i8 v[16:19], v[246:249], v[112:115], v[36:39]
	v_mfma_i32_16x16x64_i8 v[172:175], v[250:253], v[120:123], v[16:19]
	v_mfma_i32_16x16x64_i8 v[16:19], v[192:195], v[112:115], v[40:43]
	v_mfma_i32_16x16x64_i8 v[164:167], v[64:67], v[120:123], v[16:19]
	v_mfma_i32_16x16x64_i8 v[16:19], v[246:249], v[124:127], v[44:47]
	v_mfma_i32_16x16x64_i8 v[156:159], v[250:253], v[140:143], v[16:19]
	v_mfma_i32_16x16x64_i8 v[16:19], v[192:195], v[124:127], v[48:51]
	v_mfma_i32_16x16x64_i8 v[148:151], v[64:67], v[140:143], v[16:19]
	v_mfma_i32_16x16x64_i8 v[16:19], v[246:249], v[68:71], v[52:55]
	v_mfma_i32_16x16x64_i8 v[140:143], v[250:253], v[72:75], v[16:19]
	v_mfma_i32_16x16x64_i8 v[16:19], v[192:195], v[68:71], v[56:59]
	v_mfma_i32_16x16x64_i8 v[188:191], v[250:253], v[104:107], v[76:79]
	v_mfma_i32_16x16x64_i8 v[132:135], v[64:67], v[72:75], v[16:19]
	s_barrier
	ds_read_b128 v[32:35], v206 offset:49152
	ds_read_b128 v[36:39], v206 offset:50176
	ds_read_b128 v[40:43], v206 offset:51200
	ds_read_b128 v[44:47], v206 offset:52224
	ds_read_b128 v[52:55], v206 offset:53248
	ds_read_b128 v[56:59], v206 offset:54272
	ds_read_b128 v[68:71], v206 offset:55296
	ds_read_b128 v[72:75], v206 offset:56320
	s_add_i32 m0, s46, 0x18000
	s_nop 0
	global_load_lds_dwordx4 v200, s[36:37]
	s_nop 0
	s_add_i32 m0, s46, 0x1a000
	s_nop 0
	global_load_lds_dwordx4 v202, s[36:37]
	s_add_u32 s28, s24, 0x40180
	s_addc_u32 s29, s25, 0
	s_add_i32 m0, s46, 0x1c000
	s_nop 0
	global_load_lds_dwordx4 v200, s[28:29]
	s_nop 0
	s_add_i32 m0, s46, 0x1e000
	s_nop 0
	global_load_lds_dwordx4 v202, s[28:29]
	s_nop 0
	s_add_i32 m0, s46, 0x8000
	s_nop 0
	global_load_lds_dwordx4 v199, s[34:35]
	s_nop 0
	s_add_i32 m0, s46, 0xa000
	s_nop 0
	global_load_lds_dwordx4 v201, s[34:35]
	s_waitcnt vmcnt(8)
	s_waitcnt lgkmcnt(0)
	s_barrier
	v_mfma_i32_16x16x64_i8 v[16:19], v[0:3], v[32:35], v[210:213]
	v_mfma_i32_16x16x64_i8 v[120:123], v[8:11], v[36:39], v[16:19]
	v_mfma_i32_16x16x64_i8 v[16:19], v[108:111], v[32:35], v[214:217]
	v_mfma_i32_16x16x64_i8 v[112:115], v[116:119], v[36:39], v[16:19]
	v_mfma_i32_16x16x64_i8 v[16:19], v[0:3], v[40:43], v[218:221]
	v_mfma_i32_16x16x64_i8 v[104:107], v[8:11], v[44:47], v[16:19]
	v_mfma_i32_16x16x64_i8 v[16:19], v[108:111], v[40:43], v[222:225]
	v_mfma_i32_16x16x64_i8 v[96:99], v[116:119], v[44:47], v[16:19]
	v_mfma_i32_16x16x64_i8 v[16:19], v[0:3], v[52:55], v[226:229]
	v_mfma_i32_16x16x64_i8 v[0:3], v[0:3], v[68:71], v[24:27]
	v_mfma_i32_16x16x64_i8 v[48:51], v[8:11], v[56:59], v[16:19]
	v_mfma_i32_16x16x64_i8 v[16:19], v[108:111], v[52:55], v[230:233]
	v_mfma_i32_16x16x64_i8 v[8:11], v[8:11], v[72:75], v[0:3]
	v_mfma_i32_16x16x64_i8 v[0:3], v[108:111], v[68:71], v[20:23]
	v_mfma_i32_16x16x64_i8 v[16:19], v[116:119], v[56:59], v[16:19]
	v_mfma_i32_16x16x64_i8 v[0:3], v[116:119], v[72:75], v[0:3]
	v_mfma_i32_16x16x64_i8 v[20:23], v[246:249], v[32:35], v[28:31]
	v_mfma_i32_16x16x64_i8 v[124:127], v[250:253], v[36:39], v[20:23]
	v_mfma_i32_16x16x64_i8 v[20:23], v[192:195], v[32:35], v[60:63]
	v_mfma_i32_16x16x64_i8 v[116:119], v[64:67], v[36:39], v[20:23]
	v_mfma_i32_16x16x64_i8 v[20:23], v[246:249], v[40:43], v[100:103]
	v_mfma_i32_16x16x64_i8 v[108:111], v[250:253], v[44:47], v[20:23]
	v_mfma_i32_16x16x64_i8 v[20:23], v[192:195], v[40:43], v[234:237]
	v_mfma_i32_16x16x64_i8 v[100:103], v[64:67], v[44:47], v[20:23]
	v_mfma_i32_16x16x64_i8 v[20:23], v[246:249], v[52:55], v[238:241]
	v_mfma_i32_16x16x64_i8 v[60:63], v[250:253], v[56:59], v[20:23]
	v_mfma_i32_16x16x64_i8 v[20:23], v[192:195], v[52:55], v[242:245]
	v_mfma_i32_16x16x64_i8 v[12:15], v[246:249], v[68:71], v[12:15]
	v_mfma_i32_16x16x64_i8 v[4:7], v[192:195], v[68:71], v[4:7]
	v_mfma_i32_16x16x64_i8 v[44:47], v[64:67], v[56:59], v[20:23]
	v_mfma_i32_16x16x64_i8 v[12:15], v[250:253], v[72:75], v[12:15]
	v_mfma_i32_16x16x64_i8 v[4:7], v[64:67], v[72:75], v[4:7]
	s_barrier
	s_add_u32 s28, s44, s30
	s_addc_u32 s29, s45, s31
	s_add_u32 s61, s24, 0x200
	s_addc_u32 s62, s25, 0
	s_add_i32 s63, s38, 0
	s_add_i32 s63, s63, 0x20000

.LBB0_755:
	ds_read_b128 v[20:23], v205
	ds_read_b128 v[24:27], v205 offset:1024
	ds_read_b128 v[28:31], v205 offset:2048
	ds_read_b128 v[32:35], v205 offset:3072
	ds_read_b128 v[36:39], v204
	ds_read_b128 v[40:43], v204 offset:1024
	ds_read_b128 v[52:55], v204 offset:2048
	ds_read_b128 v[56:59], v204 offset:3072
	s_add_u32 s24, s26, 0x100
	s_addc_u32 s25, s27, 0
	s_and_b64 s[30:31], s[30:31], exec
	s_cselect_b32 s38, s59, s24
	s_cselect_b32 s39, s58, s25
	s_cselect_b32 s35, s15, s62
	s_cselect_b32 s34, s60, s61
	s_add_u32 s30, s38, 0x80
	s_addc_u32 s31, s39, 0
	s_add_u32 s36, s34, 0x80
	s_addc_u32 s37, s35, 0
	ds_read_b128 v[64:67], v206
	ds_read_b128 v[68:71], v206 offset:1024
	ds_read_b128 v[72:75], v206 offset:2048
	ds_read_b128 v[76:79], v206 offset:3072
	ds_read_b128 v[80:83], v206 offset:4096
	ds_read_b128 v[84:87], v206 offset:5120
	ds_read_b128 v[88:91], v206 offset:6144
	ds_read_b128 v[92:95], v206 offset:7168
	s_add_u32 s26, s26, 0x40080
	s_addc_u32 s27, s27, 0
	s_add_i32 m0, s46, 0xc000
	s_nop 0
	global_load_lds_dwordx4 v199, s[26:27]
	s_nop 0
	s_add_i32 m0, s46, 0xe000
	s_nop 0
	global_load_lds_dwordx4 v201, s[26:27]
	s_waitcnt vmcnt(8)
	s_waitcnt lgkmcnt(0)
	s_barrier
	v_mfma_i32_16x16x64_i8 v[184:187], v[20:23], v[64:67], v[184:187]
	v_mfma_i32_16x16x64_i8 v[176:179], v[28:31], v[64:67], v[176:179]
	v_mfma_i32_16x16x64_i8 v[168:171], v[20:23], v[72:75], v[168:171]
	v_mfma_i32_16x16x64_i8 v[160:163], v[28:31], v[72:75], v[160:163]
	v_mfma_i32_16x16x64_i8 v[152:155], v[20:23], v[80:83], v[152:155]
	v_mfma_i32_16x16x64_i8 v[144:147], v[28:31], v[80:83], v[144:147]
	v_mfma_i32_16x16x64_i8 v[136:139], v[20:23], v[88:91], v[136:139]
	v_mfma_i32_16x16x64_i8 v[128:131], v[28:31], v[88:91], v[128:131]
	v_mfma_i32_16x16x64_i8 v[184:187], v[24:27], v[68:71], v[184:187]
	v_mfma_i32_16x16x64_i8 v[176:179], v[32:35], v[68:71], v[176:179]
	v_mfma_i32_16x16x64_i8 v[168:171], v[24:27], v[76:79], v[168:171]
	v_mfma_i32_16x16x64_i8 v[160:163], v[32:35], v[76:79], v[160:163]
	v_mfma_i32_16x16x64_i8 v[152:155], v[24:27], v[84:87], v[152:155]
	v_mfma_i32_16x16x64_i8 v[144:147], v[32:35], v[84:87], v[144:147]
	v_mfma_i32_16x16x64_i8 v[136:139], v[24:27], v[92:95], v[136:139]
	v_mfma_i32_16x16x64_i8 v[128:131], v[32:35], v[92:95], v[128:131]
	v_mfma_i32_16x16x64_i8 v[188:191], v[36:39], v[64:67], v[188:191]
	v_mfma_i32_16x16x64_i8 v[64:67], v[52:55], v[64:67], v[180:183]
	v_mfma_i32_16x16x64_i8 v[188:191], v[40:43], v[68:71], v[188:191]
	v_mfma_i32_16x16x64_i8 v[64:67], v[56:59], v[68:71], v[64:67]
	v_mfma_i32_16x16x64_i8 v[68:71], v[36:39], v[72:75], v[172:175]
	v_mfma_i32_16x16x64_i8 v[72:75], v[52:55], v[72:75], v[164:167]
	v_mfma_i32_16x16x64_i8 v[68:71], v[40:43], v[76:79], v[68:71]
	v_mfma_i32_16x16x64_i8 v[72:75], v[56:59], v[76:79], v[72:75]
	v_mfma_i32_16x16x64_i8 v[76:79], v[36:39], v[80:83], v[156:159]
	v_mfma_i32_16x16x64_i8 v[80:83], v[52:55], v[80:83], v[148:151]
	v_mfma_i32_16x16x64_i8 v[76:79], v[40:43], v[84:87], v[76:79]
	v_mfma_i32_16x16x64_i8 v[80:83], v[56:59], v[84:87], v[80:83]
	v_mfma_i32_16x16x64_i8 v[84:87], v[36:39], v[88:91], v[140:143]
	v_mfma_i32_16x16x64_i8 v[88:91], v[52:55], v[88:91], v[132:135]
	v_mfma_i32_16x16x64_i8 v[84:87], v[40:43], v[92:95], v[84:87]
	v_mfma_i32_16x16x64_i8 v[88:91], v[56:59], v[92:95], v[88:91]
	s_barrier
	ds_read_b128 v[92:95], v206 offset:16384
	ds_read_b128 v[132:135], v206 offset:17408
	ds_read_b128 v[140:143], v206 offset:18432
	ds_read_b128 v[148:151], v206 offset:19456
	ds_read_b128 v[156:159], v206 offset:20480
	ds_read_b128 v[164:167], v206 offset:21504
	ds_read_b128 v[172:175], v206 offset:22528
	ds_read_b128 v[180:183], v206 offset:23552
	s_add_i32 m0, s46, 0x10000
	s_nop 0
	global_load_lds_dwordx4 v200, s[34:35]
	s_nop 0
	s_add_i32 m0, s46, 0x12000
	s_nop 0
	global_load_lds_dwordx4 v202, s[34:35]
	s_add_u32 s26, s34, 0x40000
	s_addc_u32 s27, s35, 0
	s_add_i32 m0, s46, 0x14000
	s_nop 0
	global_load_lds_dwordx4 v200, s[26:27]
	s_nop 0
	s_add_i32 m0, s46, 0x16000
	s_nop 0
	global_load_lds_dwordx4 v202, s[26:27]
	s_nop 0
	s_add_i32 m0, s46, 0
	s_nop 0
	global_load_lds_dwordx4 v199, s[38:39]
	s_nop 0
	s_add_i32 m0, s46, 0x2000
	s_nop 0
	global_load_lds_dwordx4 v201, s[38:39]
	s_waitcnt vmcnt(8)
	s_waitcnt lgkmcnt(0)
	s_barrier
	v_mfma_i32_16x16x64_i8 v[120:123], v[20:23], v[92:95], v[120:123]
	v_mfma_i32_16x16x64_i8 v[112:115], v[28:31], v[92:95], v[112:115]
	v_mfma_i32_16x16x64_i8 v[104:107], v[20:23], v[140:143], v[104:107]
	v_mfma_i32_16x16x64_i8 v[96:99], v[28:31], v[140:143], v[96:99]
	v_mfma_i32_16x16x64_i8 v[48:51], v[20:23], v[156:159], v[48:51]
	v_mfma_i32_16x16x64_i8 v[16:19], v[28:31], v[156:159], v[16:19]
	v_mfma_i32_16x16x64_i8 v[8:11], v[20:23], v[172:175], v[8:11]
	v_mfma_i32_16x16x64_i8 v[0:3], v[28:31], v[172:175], v[0:3]
	v_mfma_i32_16x16x64_i8 v[120:123], v[24:27], v[132:135], v[120:123]
	v_mfma_i32_16x16x64_i8 v[112:115], v[32:35], v[132:135], v[112:115]
	v_mfma_i32_16x16x64_i8 v[104:107], v[24:27], v[148:151], v[104:107]
	v_mfma_i32_16x16x64_i8 v[96:99], v[32:35], v[148:151], v[96:99]
	v_mfma_i32_16x16x64_i8 v[48:51], v[24:27], v[164:167], v[48:51]
	v_mfma_i32_16x16x64_i8 v[16:19], v[32:35], v[164:167], v[16:19]
	v_mfma_i32_16x16x64_i8 v[8:11], v[24:27], v[180:183], v[8:11]
	v_mfma_i32_16x16x64_i8 v[0:3], v[32:35], v[180:183], v[0:3]
	v_mfma_i32_16x16x64_i8 v[20:23], v[36:39], v[92:95], v[124:127]
	v_mfma_i32_16x16x64_i8 v[124:127], v[40:43], v[132:135], v[20:23]
	v_mfma_i32_16x16x64_i8 v[20:23], v[52:55], v[92:95], v[116:119]
	v_mfma_i32_16x16x64_i8 v[116:119], v[56:59], v[132:135], v[20:23]
	v_mfma_i32_16x16x64_i8 v[20:23], v[36:39], v[140:143], v[108:111]
	v_mfma_i32_16x16x64_i8 v[108:111], v[40:43], v[148:151], v[20:23]
	v_mfma_i32_16x16x64_i8 v[20:23], v[52:55], v[140:143], v[100:103]
	v_mfma_i32_16x16x64_i8 v[100:103], v[56:59], v[148:151], v[20:23]
	v_mfma_i32_16x16x64_i8 v[20:23], v[36:39], v[156:159], v[60:63]
	v_mfma_i32_16x16x64_i8 v[60:63], v[40:43], v[164:167], v[20:23]
	v_mfma_i32_16x16x64_i8 v[20:23], v[52:55], v[156:159], v[44:47]
	v_mfma_i32_16x16x64_i8 v[12:15], v[36:39], v[172:175], v[12:15]
	v_mfma_i32_16x16x64_i8 v[4:7], v[52:55], v[172:175], v[4:7]
	v_mfma_i32_16x16x64_i8 v[44:47], v[56:59], v[164:167], v[20:23]
	v_mfma_i32_16x16x64_i8 v[12:15], v[40:43], v[180:183], v[12:15]
	v_mfma_i32_16x16x64_i8 v[4:7], v[56:59], v[180:183], v[4:7]
	s_barrier
	ds_read_b128 v[36:39], v207
	ds_read_b128 v[28:31], v207 offset:1024
	ds_read_b128 v[24:27], v207 offset:2048
	ds_read_b128 v[20:23], v207 offset:3072
	ds_read_b128 v[56:59], v208
	ds_read_b128 v[52:55], v208 offset:1024
	ds_read_b128 v[40:43], v208 offset:2048
	ds_read_b128 v[32:35], v208 offset:3072
	ds_read_b128 v[92:95], v206 offset:32768
	ds_read_b128 v[132:135], v206 offset:33792
	ds_read_b128 v[140:143], v206 offset:34816
	ds_read_b128 v[148:151], v206 offset:35840
	ds_read_b128 v[192:195], v206 offset:36864
	ds_read_b128 v[210:213], v206 offset:37888
	ds_read_b128 v[214:217], v206 offset:38912
	ds_read_b128 v[218:221], v206 offset:39936
	s_add_u32 s26, s38, 0x40000
	s_addc_u32 s27, s39, 0
	s_add_i32 m0, s46, 0x4000
	s_nop 0
	global_load_lds_dwordx4 v199, s[26:27]
	s_nop 0
	s_add_i32 m0, s46, 0x6000
	s_nop 0
	global_load_lds_dwordx4 v201, s[26:27]
	s_waitcnt vmcnt(8)
	s_waitcnt lgkmcnt(0)
	s_barrier
	v_mfma_i32_16x16x64_i8 v[156:159], v[36:39], v[92:95], v[184:187]
	v_mfma_i32_16x16x64_i8 v[184:187], v[28:31], v[132:135], v[156:159]
	v_mfma_i32_16x16x64_i8 v[156:159], v[24:27], v[92:95], v[176:179]
	v_mfma_i32_16x16x64_i8 v[176:179], v[20:23], v[132:135], v[156:159]
	v_mfma_i32_16x16x64_i8 v[156:159], v[36:39], v[140:143], v[168:171]
	v_mfma_i32_16x16x64_i8 v[168:171], v[28:31], v[148:151], v[156:159]
	v_mfma_i32_16x16x64_i8 v[156:159], v[24:27], v[140:143], v[160:163]
	v_mfma_i32_16x16x64_i8 v[152:155], v[36:39], v[192:195], v[152:155]
	v_mfma_i32_16x16x64_i8 v[144:147], v[24:27], v[192:195], v[144:147]
	v_mfma_i32_16x16x64_i8 v[136:139], v[36:39], v[214:217], v[136:139]
	v_mfma_i32_16x16x64_i8 v[128:131], v[24:27], v[214:217], v[128:131]
	v_mfma_i32_16x16x64_i8 v[160:163], v[20:23], v[148:151], v[156:159]
	v_mfma_i32_16x16x64_i8 v[152:155], v[28:31], v[210:213], v[152:155]
	v_mfma_i32_16x16x64_i8 v[144:147], v[20:23], v[210:213], v[144:147]
	v_mfma_i32_16x16x64_i8 v[136:139], v[28:31], v[218:221], v[136:139]
	v_mfma_i32_16x16x64_i8 v[128:131], v[20:23], v[218:221], v[128:131]
	v_mfma_i32_16x16x64_i8 v[64:67], v[40:43], v[92:95], v[64:67]
	v_mfma_i32_16x16x64_i8 v[180:183], v[32:35], v[132:135], v[64:67]
	v_mfma_i32_16x16x64_i8 v[64:67], v[56:59], v[140:143], v[68:71]
	v_mfma_i32_16x16x64_i8 v[172:175], v[52:55], v[148:151], v[64:67]
	v_mfma_i32_16x16x64_i8 v[64:67], v[40:43], v[140:143], v[72:75]
	v_mfma_i32_16x16x64_i8 v[156:159], v[56:59], v[92:95], v[188:191]
	v_mfma_i32_16x16x64_i8 v[164:167], v[32:35], v[148:151], v[64:67]
	v_mfma_i32_16x16x64_i8 v[64:67], v[56:59], v[192:195], v[76:79]
	v_mfma_i32_16x16x64_i8 v[188:191], v[52:55], v[132:135], v[156:159]
	v_mfma_i32_16x16x64_i8 v[156:159], v[52:55], v[210:213], v[64:67]
	v_mfma_i32_16x16x64_i8 v[64:67], v[40:43], v[192:195], v[80:83]
	v_mfma_i32_16x16x64_i8 v[148:151], v[32:35], v[210:213], v[64:67]
	v_mfma_i32_16x16x64_i8 v[64:67], v[56:59], v[214:217], v[84:87]
	v_mfma_i32_16x16x64_i8 v[140:143], v[52:55], v[218:221], v[64:67]
	v_mfma_i32_16x16x64_i8 v[64:67], v[40:43], v[214:217], v[88:91]
	v_mfma_i32_16x16x64_i8 v[132:135], v[32:35], v[218:221], v[64:67]
	s_barrier
	ds_read_b128 v[92:95], v206 offset:49152
	ds_read_b128 v[88:91], v206 offset:50176
	ds_read_b128 v[84:87], v206 offset:51200
	ds_read_b128 v[80:83], v206 offset:52224
	ds_read_b128 v[76:79], v206 offset:53248
	ds_read_b128 v[72:75], v206 offset:54272
	ds_read_b128 v[68:71], v206 offset:55296
	ds_read_b128 v[64:67], v206 offset:56320
	s_add_i32 m0, s46, 0x18000
	s_nop 0
	global_load_lds_dwordx4 v200, s[36:37]
	s_nop 0
	s_add_i32 m0, s46, 0x1a000
	s_nop 0
	global_load_lds_dwordx4 v202, s[36:37]
	s_add_u32 s26, s34, 0x40080
	s_addc_u32 s27, s35, 0
	s_add_i32 m0, s46, 0x1c000
	s_nop 0
	global_load_lds_dwordx4 v200, s[26:27]
	s_nop 0
	s_add_i32 m0, s46, 0x1e000
	s_nop 0
	global_load_lds_dwordx4 v202, s[26:27]
	s_nop 0
	s_add_i32 m0, s46, 0x8000
	s_nop 0
	global_load_lds_dwordx4 v199, s[30:31]
	s_nop 0
	s_add_i32 m0, s46, 0xa000
	s_nop 0
	global_load_lds_dwordx4 v201, s[30:31]
	s_waitcnt vmcnt(8)
	s_waitcnt lgkmcnt(0)
	s_barrier
	v_mfma_i32_16x16x64_i8 v[120:123], v[36:39], v[92:95], v[120:123]
	v_mfma_i32_16x16x64_i8 v[112:115], v[24:27], v[92:95], v[112:115]
	v_mfma_i32_16x16x64_i8 v[104:107], v[36:39], v[84:87], v[104:107]
	v_mfma_i32_16x16x64_i8 v[96:99], v[24:27], v[84:87], v[96:99]
	v_mfma_i32_16x16x64_i8 v[48:51], v[36:39], v[76:79], v[48:51]
	v_mfma_i32_16x16x64_i8 v[16:19], v[24:27], v[76:79], v[16:19]
	v_mfma_i32_16x16x64_i8 v[8:11], v[36:39], v[68:71], v[8:11]
	v_mfma_i32_16x16x64_i8 v[0:3], v[24:27], v[68:71], v[0:3]
	v_mfma_i32_16x16x64_i8 v[120:123], v[28:31], v[88:91], v[120:123]
	v_mfma_i32_16x16x64_i8 v[112:115], v[20:23], v[88:91], v[112:115]
	v_mfma_i32_16x16x64_i8 v[104:107], v[28:31], v[80:83], v[104:107]
	v_mfma_i32_16x16x64_i8 v[96:99], v[20:23], v[80:83], v[96:99]
	v_mfma_i32_16x16x64_i8 v[48:51], v[28:31], v[72:75], v[48:51]
	v_mfma_i32_16x16x64_i8 v[16:19], v[20:23], v[72:75], v[16:19]
	v_mfma_i32_16x16x64_i8 v[8:11], v[28:31], v[64:67], v[8:11]
	v_mfma_i32_16x16x64_i8 v[0:3], v[20:23], v[64:67], v[0:3]
	v_mfma_i32_16x16x64_i8 v[124:127], v[56:59], v[92:95], v[124:127]
	v_mfma_i32_16x16x64_i8 v[116:119], v[40:43], v[92:95], v[116:119]
	v_mfma_i32_16x16x64_i8 v[108:111], v[56:59], v[84:87], v[108:111]
	v_mfma_i32_16x16x64_i8 v[100:103], v[40:43], v[84:87], v[100:103]
	v_mfma_i32_16x16x64_i8 v[60:63], v[56:59], v[76:79], v[60:63]
	v_mfma_i32_16x16x64_i8 v[44:47], v[40:43], v[76:79], v[44:47]
	v_mfma_i32_16x16x64_i8 v[12:15], v[56:59], v[68:71], v[12:15]
	v_mfma_i32_16x16x64_i8 v[4:7], v[40:43], v[68:71], v[4:7]
	v_mfma_i32_16x16x64_i8 v[124:127], v[52:55], v[88:91], v[124:127]
	v_mfma_i32_16x16x64_i8 v[116:119], v[32:35], v[88:91], v[116:119]
	v_mfma_i32_16x16x64_i8 v[108:111], v[52:55], v[80:83], v[108:111]
	v_mfma_i32_16x16x64_i8 v[100:103], v[32:35], v[80:83], v[100:103]
	v_mfma_i32_16x16x64_i8 v[60:63], v[52:55], v[72:75], v[60:63]
	v_mfma_i32_16x16x64_i8 v[44:47], v[32:35], v[72:75], v[44:47]
	v_mfma_i32_16x16x64_i8 v[12:15], v[52:55], v[64:67], v[12:15]
	v_mfma_i32_16x16x64_i8 v[4:7], v[32:35], v[64:67], v[4:7]
	s_barrier
	s_add_i32 s17, s17, 2
	s_add_u32 s61, s61, 0x100
	s_addc_u32 s62, s62, 0
	s_cmp_gt_u32 s17, 13
	s_cbranch_scc1 .LBB0_757
	s_mov_b64 s[26:27], s[24:25]
	s_branch .LBB0_753

.LBB0_837:
	s_waitcnt lgkmcnt(0)
	ds_read_b128 v[0:3], v181
	ds_read_b128 v[4:7], v181 offset:1024
	ds_read_b128 v[8:11], v181 offset:2048
	ds_read_b128 v[12:15], v181 offset:3072
	ds_read_b128 v[16:19], v182
	ds_read_b128 v[20:23], v182 offset:1024
	ds_read_b128 v[24:27], v182 offset:2048
	ds_read_b128 v[28:31], v182 offset:3072
	s_add_u32 s28, s22, 0x100
	s_addc_u32 s29, s23, 0
	s_add_u32 s52, s24, 0x100
	s_addc_u32 s53, s25, 0
	s_add_u32 s6, s22, 0x180
	s_addc_u32 s7, s23, 0
	ds_read_b128 v[32:35], v183
	ds_read_b128 v[36:39], v183 offset:1024
	ds_read_b128 v[40:43], v183 offset:2048
	ds_read_b128 v[44:47], v183 offset:3072
	ds_read_b128 v[48:51], v183 offset:4096
	ds_read_b128 v[52:55], v183 offset:5120
	ds_read_b128 v[56:59], v183 offset:6144
	ds_read_b128 v[60:63], v183 offset:7168
	s_add_u32 s26, s24, 0x180
	s_addc_u32 s27, s25, 0
	s_add_u32 s54, s22, 0x160080
	s_addc_u32 s55, s23, 0
	s_add_i32 m0, s36, 0xc000
	s_nop 0
	global_load_lds_dwordx4 v175, s[54:55]
	s_nop 0
	s_add_i32 m0, s36, 0xe000
	s_nop 0
	global_load_lds_dwordx4 v177, s[54:55]
	s_waitcnt vmcnt(8)
	s_waitcnt lgkmcnt(0)
	s_barrier
	v_mfma_f32_16x16x32_bf16 v[88:91], v[0:3], v[56:59], 0
	v_mfma_f32_16x16x32_bf16 v[64:67], v[0:3], v[32:35], 0
	v_mfma_f32_16x16x32_bf16 v[68:71], v[8:11], v[32:35], 0
	v_mfma_f32_16x16x32_bf16 v[72:75], v[0:3], v[40:43], 0
	v_mfma_f32_16x16x32_bf16 v[76:79], v[8:11], v[40:43], 0
	v_mfma_f32_16x16x32_bf16 v[80:83], v[0:3], v[48:51], 0
	v_mfma_f32_16x16x32_bf16 v[84:87], v[8:11], v[48:51], 0
	v_mfma_f32_16x16x32_bf16 v[96:99], v[4:7], v[60:63], v[88:91]
	v_mfma_f32_16x16x32_bf16 v[88:91], v[8:11], v[56:59], 0
	v_mfma_f32_16x16x32_bf16 v[64:67], v[4:7], v[36:39], v[64:67]
	v_mfma_f32_16x16x32_bf16 v[68:71], v[12:15], v[36:39], v[68:71]
	v_mfma_f32_16x16x32_bf16 v[72:75], v[4:7], v[44:47], v[72:75]
	v_mfma_f32_16x16x32_bf16 v[76:79], v[12:15], v[44:47], v[76:79]
	v_mfma_f32_16x16x32_bf16 v[80:83], v[4:7], v[52:55], v[80:83]
	v_mfma_f32_16x16x32_bf16 v[84:87], v[12:15], v[52:55], v[84:87]
	v_mfma_f32_16x16x32_bf16 v[100:103], v[12:15], v[60:63], v[88:91]
	v_mfma_f32_16x16x32_bf16 v[88:91], v[16:19], v[32:35], 0
	v_mfma_f32_16x16x32_bf16 v[32:35], v[24:27], v[32:35], 0
	v_mfma_f32_16x16x32_bf16 v[112:115], v[20:23], v[36:39], v[88:91]
	v_mfma_f32_16x16x32_bf16 v[32:35], v[28:31], v[36:39], v[32:35]
	v_mfma_f32_16x16x32_bf16 v[36:39], v[16:19], v[40:43], 0
	v_mfma_f32_16x16x32_bf16 v[40:43], v[24:27], v[40:43], 0
	v_mfma_f32_16x16x32_bf16 v[36:39], v[20:23], v[44:47], v[36:39]
	v_mfma_f32_16x16x32_bf16 v[40:43], v[28:31], v[44:47], v[40:43]
	v_mfma_f32_16x16x32_bf16 v[44:47], v[16:19], v[48:51], 0
	v_mfma_f32_16x16x32_bf16 v[48:51], v[24:27], v[48:51], 0
	v_mfma_f32_16x16x32_bf16 v[44:47], v[20:23], v[52:55], v[44:47]
	v_mfma_f32_16x16x32_bf16 v[48:51], v[28:31], v[52:55], v[48:51]
	v_mfma_f32_16x16x32_bf16 v[52:55], v[16:19], v[56:59], 0
	v_mfma_f32_16x16x32_bf16 v[56:59], v[24:27], v[56:59], 0
	v_mfma_f32_16x16x32_bf16 v[52:55], v[20:23], v[60:63], v[52:55]
	v_mfma_f32_16x16x32_bf16 v[56:59], v[28:31], v[60:63], v[56:59]
	s_barrier
	ds_read_b128 v[60:63], v183 offset:16384
	ds_read_b128 v[88:91], v183 offset:17408
	ds_read_b128 v[92:95], v183 offset:18432
	ds_read_b128 v[104:107], v183 offset:19456
	ds_read_b128 v[108:111], v183 offset:20480
	ds_read_b128 v[116:119], v183 offset:21504
	ds_read_b128 v[120:123], v183 offset:22528
	ds_read_b128 v[124:127], v183 offset:23552
	s_add_i32 m0, s36, 0x10000
	s_nop 0
	global_load_lds_dwordx4 v176, s[52:53]
	s_nop 0
	s_add_i32 m0, s36, 0x12000
	s_nop 0
	global_load_lds_dwordx4 v178, s[52:53]
	s_add_u32 s52, s24, 0x160100
	s_addc_u32 s53, s25, 0
	s_add_i32 m0, s36, 0x14000
	s_nop 0
	global_load_lds_dwordx4 v176, s[52:53]
	s_nop 0
	s_add_i32 m0, s36, 0x16000
	s_nop 0
	global_load_lds_dwordx4 v178, s[52:53]
	s_nop 0
	s_add_i32 m0, s36, 0
	s_nop 0
	global_load_lds_dwordx4 v175, s[28:29]
	s_nop 0
	s_add_i32 m0, s36, 0x2000
	s_nop 0
	global_load_lds_dwordx4 v177, s[28:29]
	s_waitcnt vmcnt(8)
	s_waitcnt lgkmcnt(0)
	s_barrier
	v_mfma_f32_16x16x32_bf16 v[128:131], v[0:3], v[60:63], 0
	v_mfma_f32_16x16x32_bf16 v[136:139], v[4:7], v[88:91], v[128:131]
	v_mfma_f32_16x16x32_bf16 v[128:131], v[8:11], v[60:63], 0
	v_mfma_f32_16x16x32_bf16 v[140:143], v[12:15], v[88:91], v[128:131]
	v_mfma_f32_16x16x32_bf16 v[128:131], v[0:3], v[92:95], 0
	v_mfma_f32_16x16x32_bf16 v[144:147], v[4:7], v[104:107], v[128:131]
	v_mfma_f32_16x16x32_bf16 v[128:131], v[8:11], v[92:95], 0
	v_mfma_f32_16x16x32_bf16 v[148:151], v[12:15], v[104:107], v[128:131]
	v_mfma_f32_16x16x32_bf16 v[128:131], v[0:3], v[108:111], 0
	v_mfma_f32_16x16x32_bf16 v[0:3], v[0:3], v[120:123], 0
	v_mfma_f32_16x16x32_bf16 v[156:159], v[4:7], v[116:119], v[128:131]
	v_mfma_f32_16x16x32_bf16 v[0:3], v[4:7], v[124:127], v[0:3]
	v_mfma_f32_16x16x32_bf16 v[4:7], v[8:11], v[120:123], 0
	v_mfma_f32_16x16x32_bf16 v[128:131], v[8:11], v[108:111], 0
	v_mfma_f32_16x16x32_bf16 v[4:7], v[12:15], v[124:127], v[4:7]
	v_mfma_f32_16x16x32_bf16 v[160:163], v[12:15], v[116:119], v[128:131]
	v_mfma_f32_16x16x32_bf16 v[8:11], v[16:19], v[60:63], 0
	v_mfma_f32_16x16x32_bf16 v[164:167], v[20:23], v[88:91], v[8:11]
	v_mfma_f32_16x16x32_bf16 v[8:11], v[24:27], v[60:63], 0
	v_mfma_f32_16x16x32_bf16 v[168:171], v[28:31], v[88:91], v[8:11]
	v_mfma_f32_16x16x32_bf16 v[8:11], v[16:19], v[92:95], 0
	v_mfma_f32_16x16x32_bf16 v[188:191], v[20:23], v[104:107], v[8:11]
	v_mfma_f32_16x16x32_bf16 v[8:11], v[24:27], v[92:95], 0
	v_mfma_f32_16x16x32_bf16 v[192:195], v[28:31], v[104:107], v[8:11]
	v_mfma_f32_16x16x32_bf16 v[8:11], v[16:19], v[108:111], 0
	v_mfma_f32_16x16x32_bf16 v[196:199], v[20:23], v[116:119], v[8:11]
	v_mfma_f32_16x16x32_bf16 v[8:11], v[24:27], v[108:111], 0
	v_mfma_f32_16x16x32_bf16 v[116:119], v[28:31], v[116:119], v[8:11]
	v_mfma_f32_16x16x32_bf16 v[8:11], v[16:19], v[120:123], 0
	v_mfma_f32_16x16x32_bf16 v[200:203], v[20:23], v[124:127], v[8:11]
	v_mfma_f32_16x16x32_bf16 v[8:11], v[24:27], v[120:123], 0
	v_mfma_f32_16x16x32_bf16 v[204:207], v[28:31], v[124:127], v[8:11]
	s_barrier
	s_nop 4
	ds_read_b128 v[8:11], v184
	ds_read_b128 v[12:15], v184 offset:1024
	ds_read_b128 v[16:19], v184 offset:2048
	ds_read_b128 v[20:23], v184 offset:3072
	ds_read_b128 v[208:211], v185
	ds_read_b128 v[212:215], v185 offset:1024
	ds_read_b128 v[216:219], v185 offset:2048
	ds_read_b128 v[220:223], v185 offset:3072
	ds_read_b128 v[24:27], v183 offset:32768
	ds_read_b128 v[28:31], v183 offset:33792
	ds_read_b128 v[60:63], v183 offset:34816
	ds_read_b128 v[224:227], v183 offset:35840
	ds_read_b128 v[228:231], v183 offset:36864
	ds_read_b128 v[232:235], v183 offset:37888
	ds_read_b128 v[236:239], v183 offset:38912
	ds_read_b128 v[240:243], v183 offset:39936
	s_add_u32 s28, s22, 0x160100
	s_addc_u32 s29, s23, 0
	s_add_i32 m0, s36, 0x4000
	s_nop 0
	global_load_lds_dwordx4 v175, s[28:29]
	s_nop 0
	s_add_i32 m0, s36, 0x6000
	s_nop 0
	global_load_lds_dwordx4 v177, s[28:29]
	s_waitcnt vmcnt(8)
	s_waitcnt lgkmcnt(0)
	s_barrier
	v_mfma_f32_16x16x32_bf16 v[64:67], v[8:11], v[24:27], v[64:67]
	v_mfma_f32_16x16x32_bf16 v[132:135], v[12:15], v[28:31], v[64:67]
	v_mfma_f32_16x16x32_bf16 v[64:67], v[16:19], v[24:27], v[68:71]
	v_mfma_f32_16x16x32_bf16 v[128:131], v[20:23], v[28:31], v[64:67]
	v_mfma_f32_16x16x32_bf16 v[64:67], v[8:11], v[60:63], v[72:75]
	v_mfma_f32_16x16x32_bf16 v[108:111], v[12:15], v[224:227], v[64:67]
	v_mfma_f32_16x16x32_bf16 v[64:67], v[16:19], v[60:63], v[76:79]
	v_mfma_f32_16x16x32_bf16 v[104:107], v[20:23], v[224:227], v[64:67]
	v_mfma_f32_16x16x32_bf16 v[64:67], v[8:11], v[228:231], v[80:83]
	v_mfma_f32_16x16x32_bf16 v[92:95], v[12:15], v[232:235], v[64:67]
	v_mfma_f32_16x16x32_bf16 v[64:67], v[16:19], v[228:231], v[84:87]
	v_mfma_f32_16x16x32_bf16 v[88:91], v[20:23], v[232:235], v[64:67]
	v_mfma_f32_16x16x32_bf16 v[64:67], v[8:11], v[236:239], v[96:99]
	v_mfma_f32_16x16x32_bf16 v[76:79], v[12:15], v[240:243], v[64:67]
	v_mfma_f32_16x16x32_bf16 v[64:67], v[16:19], v[236:239], v[100:103]
	v_mfma_f32_16x16x32_bf16 v[72:75], v[20:23], v[240:243], v[64:67]
	v_mfma_f32_16x16x32_bf16 v[64:67], v[208:211], v[24:27], v[112:115]
	v_mfma_f32_16x16x32_bf16 v[24:27], v[216:219], v[24:27], v[32:35]
	v_mfma_f32_16x16x32_bf16 v[120:123], v[220:223], v[28:31], v[24:27]
	v_mfma_f32_16x16x32_bf16 v[24:27], v[208:211], v[60:63], v[36:39]
	v_mfma_f32_16x16x32_bf16 v[100:103], v[212:215], v[224:227], v[24:27]
	v_mfma_f32_16x16x32_bf16 v[24:27], v[216:219], v[60:63], v[40:43]
	v_mfma_f32_16x16x32_bf16 v[96:99], v[220:223], v[224:227], v[24:27]
	v_mfma_f32_16x16x32_bf16 v[24:27], v[208:211], v[228:231], v[44:47]
	v_mfma_f32_16x16x32_bf16 v[84:87], v[212:215], v[232:235], v[24:27]
	v_mfma_f32_16x16x32_bf16 v[24:27], v[216:219], v[228:231], v[48:51]
	v_mfma_f32_16x16x32_bf16 v[80:83], v[220:223], v[232:235], v[24:27]
	v_mfma_f32_16x16x32_bf16 v[24:27], v[208:211], v[236:239], v[52:55]
	v_mfma_f32_16x16x32_bf16 v[68:71], v[212:215], v[240:243], v[24:27]
	v_mfma_f32_16x16x32_bf16 v[24:27], v[216:219], v[236:239], v[56:59]
	v_mfma_f32_16x16x32_bf16 v[124:127], v[212:215], v[28:31], v[64:67]
	v_mfma_f32_16x16x32_bf16 v[64:67], v[220:223], v[240:243], v[24:27]
	s_barrier
	ds_read_b128 v[32:35], v183 offset:49152
	ds_read_b128 v[36:39], v183 offset:50176
	ds_read_b128 v[112:115], v183 offset:51200
	ds_read_b128 v[224:227], v183 offset:52224
	ds_read_b128 v[228:231], v183 offset:53248
	ds_read_b128 v[232:235], v183 offset:54272
	ds_read_b128 v[236:239], v183 offset:55296
	ds_read_b128 v[240:243], v183 offset:56320
	s_add_i32 m0, s36, 0x18000
	s_nop 0
	global_load_lds_dwordx4 v176, s[26:27]
	s_nop 0
	s_add_i32 m0, s36, 0x1a000
	s_nop 0
	global_load_lds_dwordx4 v178, s[26:27]
	s_add_u32 s26, s24, 0x160180
	s_addc_u32 s27, s25, 0
	s_add_i32 m0, s36, 0x1c000
	s_nop 0
	global_load_lds_dwordx4 v176, s[26:27]
	s_nop 0
	s_add_i32 m0, s36, 0x1e000
	s_nop 0
	global_load_lds_dwordx4 v178, s[26:27]
	s_nop 0
	s_add_i32 m0, s36, 0x8000
	s_nop 0
	global_load_lds_dwordx4 v175, s[6:7]
	s_nop 0
	s_add_i32 m0, s36, 0xa000
	s_nop 0
	global_load_lds_dwordx4 v177, s[6:7]
	s_waitcnt vmcnt(8)
	s_waitcnt lgkmcnt(0)
	s_barrier
	v_mfma_f32_16x16x32_bf16 v[24:27], v[8:11], v[32:35], v[136:139]
	v_mfma_f32_16x16x32_bf16 v[60:63], v[12:15], v[36:39], v[24:27]
	v_mfma_f32_16x16x32_bf16 v[24:27], v[16:19], v[32:35], v[140:143]
	v_mfma_f32_16x16x32_bf16 v[56:59], v[20:23], v[36:39], v[24:27]
	v_mfma_f32_16x16x32_bf16 v[24:27], v[8:11], v[112:115], v[144:147]
	v_mfma_f32_16x16x32_bf16 v[44:47], v[12:15], v[224:227], v[24:27]
	v_mfma_f32_16x16x32_bf16 v[24:27], v[16:19], v[112:115], v[148:151]
	v_mfma_f32_16x16x32_bf16 v[40:43], v[20:23], v[224:227], v[24:27]
	v_mfma_f32_16x16x32_bf16 v[24:27], v[8:11], v[228:231], v[156:159]
	v_mfma_f32_16x16x32_bf16 v[0:3], v[8:11], v[236:239], v[0:3]
	v_mfma_f32_16x16x32_bf16 v[28:31], v[12:15], v[232:235], v[24:27]
	v_mfma_f32_16x16x32_bf16 v[24:27], v[16:19], v[228:231], v[160:163]
	v_mfma_f32_16x16x32_bf16 v[12:15], v[12:15], v[240:243], v[0:3]
	v_mfma_f32_16x16x32_bf16 v[0:3], v[16:19], v[236:239], v[4:7]
	v_mfma_f32_16x16x32_bf16 v[24:27], v[20:23], v[232:235], v[24:27]
	v_mfma_f32_16x16x32_bf16 v[8:11], v[20:23], v[240:243], v[0:3]
	v_mfma_f32_16x16x32_bf16 v[0:3], v[208:211], v[32:35], v[164:167]
	v_mfma_f32_16x16x32_bf16 v[52:55], v[212:215], v[36:39], v[0:3]
	v_mfma_f32_16x16x32_bf16 v[0:3], v[216:219], v[32:35], v[168:171]
	v_mfma_f32_16x16x32_bf16 v[48:51], v[220:223], v[36:39], v[0:3]
	v_mfma_f32_16x16x32_bf16 v[0:3], v[208:211], v[112:115], v[188:191]
	v_mfma_f32_16x16x32_bf16 v[36:39], v[212:215], v[224:227], v[0:3]
	v_mfma_f32_16x16x32_bf16 v[0:3], v[216:219], v[112:115], v[192:195]
	v_mfma_f32_16x16x32_bf16 v[32:35], v[220:223], v[224:227], v[0:3]
	v_mfma_f32_16x16x32_bf16 v[0:3], v[208:211], v[228:231], v[196:199]
	v_mfma_f32_16x16x32_bf16 v[20:23], v[212:215], v[232:235], v[0:3]
	v_mfma_f32_16x16x32_bf16 v[0:3], v[216:219], v[228:231], v[116:119]
	v_mfma_f32_16x16x32_bf16 v[16:19], v[220:223], v[232:235], v[0:3]
	v_mfma_f32_16x16x32_bf16 v[0:3], v[208:211], v[236:239], v[200:203]
	v_mfma_f32_16x16x32_bf16 v[4:7], v[212:215], v[240:243], v[0:3]
	v_mfma_f32_16x16x32_bf16 v[0:3], v[216:219], v[236:239], v[204:207]
	v_mfma_f32_16x16x32_bf16 v[0:3], v[220:223], v[240:243], v[0:3]
	s_barrier
	s_add_u32 s51, s22, 0x200
	s_addc_u32 s52, s23, 0
	s_add_u32 s53, s24, 0x200
	s_addc_u32 s54, s25, 0
	s_add_u32 s6, s22, 0x160180
	s_addc_u32 s7, s23, 0
	s_mov_b32 s55, 0
.LBB0_838:
	ds_read_b128 v[112:115], v181
	ds_read_b128 v[116:119], v181 offset:1024
	ds_read_b128 v[136:139], v181 offset:2048
	ds_read_b128 v[140:143], v181 offset:3072
	ds_read_b128 v[144:147], v182
	ds_read_b128 v[148:151], v182 offset:1024
	ds_read_b128 v[156:159], v182 offset:2048
	ds_read_b128 v[160:163], v182 offset:3072
	s_cmpk_eq_i32 s55, 0x54
	s_cselect_b32 s28, s18, s51
	s_cselect_b32 s29, s19, s52
	s_cselect_b32 s24, s20, s53
	s_cselect_b32 s25, s21, s54
	s_add_u32 s22, s28, 0x80
	s_addc_u32 s23, s29, 0
	ds_read_b128 v[164:167], v183
	ds_read_b128 v[168:171], v183 offset:1024
	ds_read_b128 v[188:191], v183 offset:2048
	ds_read_b128 v[192:195], v183 offset:3072
	ds_read_b128 v[196:199], v183 offset:4096
	ds_read_b128 v[200:203], v183 offset:5120
	ds_read_b128 v[204:207], v183 offset:6144
	ds_read_b128 v[208:211], v183 offset:7168
	s_add_u32 s26, s24, 0x80
	s_addc_u32 s27, s25, 0
	s_add_i32 m0, s36, 0xc000
	s_nop 0
	global_load_lds_dwordx4 v175, s[6:7]
	s_nop 0
	s_add_i32 m0, s36, 0xe000
	s_nop 0
	global_load_lds_dwordx4 v177, s[6:7]
	s_waitcnt vmcnt(8)
	s_waitcnt lgkmcnt(0)
	s_barrier
	v_mfma_f32_16x16x32_bf16 v[132:135], v[112:115], v[164:167], v[132:135]
	v_mfma_f32_16x16x32_bf16 v[128:131], v[136:139], v[164:167], v[128:131]
	v_mfma_f32_16x16x32_bf16 v[108:111], v[112:115], v[188:191], v[108:111]
	v_mfma_f32_16x16x32_bf16 v[104:107], v[136:139], v[188:191], v[104:107]
	v_mfma_f32_16x16x32_bf16 v[92:95], v[112:115], v[196:199], v[92:95]
	v_mfma_f32_16x16x32_bf16 v[88:91], v[136:139], v[196:199], v[88:91]
	v_mfma_f32_16x16x32_bf16 v[76:79], v[112:115], v[204:207], v[76:79]
	v_mfma_f32_16x16x32_bf16 v[72:75], v[136:139], v[204:207], v[72:75]
	v_mfma_f32_16x16x32_bf16 v[132:135], v[116:119], v[168:171], v[132:135]
	v_mfma_f32_16x16x32_bf16 v[128:131], v[140:143], v[168:171], v[128:131]
	v_mfma_f32_16x16x32_bf16 v[108:111], v[116:119], v[192:195], v[108:111]
	v_mfma_f32_16x16x32_bf16 v[104:107], v[140:143], v[192:195], v[104:107]
	v_mfma_f32_16x16x32_bf16 v[92:95], v[116:119], v[200:203], v[92:95]
	v_mfma_f32_16x16x32_bf16 v[88:91], v[140:143], v[200:203], v[88:91]
	v_mfma_f32_16x16x32_bf16 v[76:79], v[116:119], v[208:211], v[76:79]
	v_mfma_f32_16x16x32_bf16 v[72:75], v[140:143], v[208:211], v[72:75]
	v_mfma_f32_16x16x32_bf16 v[124:127], v[144:147], v[164:167], v[124:127]
	v_mfma_f32_16x16x32_bf16 v[120:123], v[156:159], v[164:167], v[120:123]
	v_mfma_f32_16x16x32_bf16 v[100:103], v[144:147], v[188:191], v[100:103]
	v_mfma_f32_16x16x32_bf16 v[96:99], v[156:159], v[188:191], v[96:99]
	v_mfma_f32_16x16x32_bf16 v[84:87], v[144:147], v[196:199], v[84:87]
	v_mfma_f32_16x16x32_bf16 v[80:83], v[156:159], v[196:199], v[80:83]
	v_mfma_f32_16x16x32_bf16 v[68:71], v[144:147], v[204:207], v[68:71]
	v_mfma_f32_16x16x32_bf16 v[64:67], v[156:159], v[204:207], v[64:67]
	v_mfma_f32_16x16x32_bf16 v[124:127], v[148:151], v[168:171], v[124:127]
	v_mfma_f32_16x16x32_bf16 v[120:123], v[160:163], v[168:171], v[120:123]
	v_mfma_f32_16x16x32_bf16 v[100:103], v[148:151], v[192:195], v[100:103]
	v_mfma_f32_16x16x32_bf16 v[96:99], v[160:163], v[192:195], v[96:99]
	v_mfma_f32_16x16x32_bf16 v[84:87], v[148:151], v[200:203], v[84:87]
	v_mfma_f32_16x16x32_bf16 v[80:83], v[160:163], v[200:203], v[80:83]
	v_mfma_f32_16x16x32_bf16 v[68:71], v[148:151], v[208:211], v[68:71]
	v_mfma_f32_16x16x32_bf16 v[64:67], v[160:163], v[208:211], v[64:67]
	s_barrier
	ds_read_b128 v[164:167], v183 offset:16384
	ds_read_b128 v[168:171], v183 offset:17408
	ds_read_b128 v[188:191], v183 offset:18432
	ds_read_b128 v[192:195], v183 offset:19456
	ds_read_b128 v[196:199], v183 offset:20480
	ds_read_b128 v[200:203], v183 offset:21504
	ds_read_b128 v[204:207], v183 offset:22528
	ds_read_b128 v[208:211], v183 offset:23552
	s_add_i32 m0, s36, 0x10000
	s_nop 0
	global_load_lds_dwordx4 v176, s[24:25]
	s_nop 0
	s_add_i32 m0, s36, 0x12000
	s_nop 0
	global_load_lds_dwordx4 v178, s[24:25]
	s_add_u32 s56, s24, 0x160000
	s_addc_u32 s57, s25, 0
	s_add_i32 m0, s36, 0x14000
	s_nop 0
	global_load_lds_dwordx4 v176, s[56:57]
	s_nop 0
	s_add_i32 m0, s36, 0x16000
	s_nop 0
	global_load_lds_dwordx4 v178, s[56:57]
	s_nop 0
	s_add_i32 m0, s36, 0
	s_nop 0
	global_load_lds_dwordx4 v175, s[28:29]
	s_nop 0
	s_add_i32 m0, s36, 0x2000
	s_nop 0
	global_load_lds_dwordx4 v177, s[28:29]
	s_waitcnt vmcnt(8)
	s_waitcnt lgkmcnt(0)
	s_barrier
	v_mfma_f32_16x16x32_bf16 v[60:63], v[112:115], v[164:167], v[60:63]
	v_mfma_f32_16x16x32_bf16 v[56:59], v[136:139], v[164:167], v[56:59]
	v_mfma_f32_16x16x32_bf16 v[44:47], v[112:115], v[188:191], v[44:47]
	v_mfma_f32_16x16x32_bf16 v[40:43], v[136:139], v[188:191], v[40:43]
	v_mfma_f32_16x16x32_bf16 v[28:31], v[112:115], v[196:199], v[28:31]
	v_mfma_f32_16x16x32_bf16 v[24:27], v[136:139], v[196:199], v[24:27]
	v_mfma_f32_16x16x32_bf16 v[12:15], v[112:115], v[204:207], v[12:15]
	v_mfma_f32_16x16x32_bf16 v[8:11], v[136:139], v[204:207], v[8:11]
	v_mfma_f32_16x16x32_bf16 v[60:63], v[116:119], v[168:171], v[60:63]
	v_mfma_f32_16x16x32_bf16 v[56:59], v[140:143], v[168:171], v[56:59]
	v_mfma_f32_16x16x32_bf16 v[44:47], v[116:119], v[192:195], v[44:47]
	v_mfma_f32_16x16x32_bf16 v[40:43], v[140:143], v[192:195], v[40:43]
	v_mfma_f32_16x16x32_bf16 v[28:31], v[116:119], v[200:203], v[28:31]
	v_mfma_f32_16x16x32_bf16 v[24:27], v[140:143], v[200:203], v[24:27]
	v_mfma_f32_16x16x32_bf16 v[12:15], v[116:119], v[208:211], v[12:15]
	v_mfma_f32_16x16x32_bf16 v[8:11], v[140:143], v[208:211], v[8:11]
	v_mfma_f32_16x16x32_bf16 v[52:55], v[144:147], v[164:167], v[52:55]
	v_mfma_f32_16x16x32_bf16 v[48:51], v[156:159], v[164:167], v[48:51]
	v_mfma_f32_16x16x32_bf16 v[36:39], v[144:147], v[188:191], v[36:39]
	v_mfma_f32_16x16x32_bf16 v[32:35], v[156:159], v[188:191], v[32:35]
	v_mfma_f32_16x16x32_bf16 v[20:23], v[144:147], v[196:199], v[20:23]
	v_mfma_f32_16x16x32_bf16 v[16:19], v[156:159], v[196:199], v[16:19]
	v_mfma_f32_16x16x32_bf16 v[4:7], v[144:147], v[204:207], v[4:7]
	v_mfma_f32_16x16x32_bf16 v[0:3], v[156:159], v[204:207], v[0:3]
	v_mfma_f32_16x16x32_bf16 v[52:55], v[148:151], v[168:171], v[52:55]
	v_mfma_f32_16x16x32_bf16 v[48:51], v[160:163], v[168:171], v[48:51]
	v_mfma_f32_16x16x32_bf16 v[36:39], v[148:151], v[192:195], v[36:39]
	v_mfma_f32_16x16x32_bf16 v[32:35], v[160:163], v[192:195], v[32:35]
	v_mfma_f32_16x16x32_bf16 v[20:23], v[148:151], v[200:203], v[20:23]
	v_mfma_f32_16x16x32_bf16 v[16:19], v[160:163], v[200:203], v[16:19]
	v_mfma_f32_16x16x32_bf16 v[4:7], v[148:151], v[208:211], v[4:7]
	v_mfma_f32_16x16x32_bf16 v[0:3], v[160:163], v[208:211], v[0:3]
	s_barrier
	ds_read_b128 v[112:115], v184
	ds_read_b128 v[116:119], v184 offset:1024
	ds_read_b128 v[136:139], v184 offset:2048
	ds_read_b128 v[140:143], v184 offset:3072
	ds_read_b128 v[144:147], v185
	ds_read_b128 v[148:151], v185 offset:1024
	ds_read_b128 v[156:159], v185 offset:2048
	ds_read_b128 v[160:163], v185 offset:3072
	ds_read_b128 v[164:167], v183 offset:32768
	ds_read_b128 v[168:171], v183 offset:33792
	ds_read_b128 v[188:191], v183 offset:34816
	ds_read_b128 v[192:195], v183 offset:35840
	ds_read_b128 v[196:199], v183 offset:36864
	ds_read_b128 v[200:203], v183 offset:37888
	ds_read_b128 v[204:207], v183 offset:38912
	ds_read_b128 v[208:211], v183 offset:39936
	s_add_u32 s28, s28, 0x160000
	s_addc_u32 s29, s29, 0
	s_add_i32 m0, s36, 0x4000
	s_nop 0
	global_load_lds_dwordx4 v175, s[28:29]
	s_nop 0
	s_add_i32 m0, s36, 0x6000
	s_nop 0
	global_load_lds_dwordx4 v177, s[28:29]
	s_waitcnt vmcnt(8)
	s_waitcnt lgkmcnt(0)
	s_barrier
	v_mfma_f32_16x16x32_bf16 v[132:135], v[112:115], v[164:167], v[132:135]
	v_mfma_f32_16x16x32_bf16 v[128:131], v[136:139], v[164:167], v[128:131]
	v_mfma_f32_16x16x32_bf16 v[108:111], v[112:115], v[188:191], v[108:111]
	v_mfma_f32_16x16x32_bf16 v[104:107], v[136:139], v[188:191], v[104:107]
	v_mfma_f32_16x16x32_bf16 v[92:95], v[112:115], v[196:199], v[92:95]
	v_mfma_f32_16x16x32_bf16 v[88:91], v[136:139], v[196:199], v[88:91]
	v_mfma_f32_16x16x32_bf16 v[76:79], v[112:115], v[204:207], v[76:79]
	v_mfma_f32_16x16x32_bf16 v[72:75], v[136:139], v[204:207], v[72:75]
	v_mfma_f32_16x16x32_bf16 v[132:135], v[116:119], v[168:171], v[132:135]
	v_mfma_f32_16x16x32_bf16 v[128:131], v[140:143], v[168:171], v[128:131]
	v_mfma_f32_16x16x32_bf16 v[108:111], v[116:119], v[192:195], v[108:111]
	v_mfma_f32_16x16x32_bf16 v[104:107], v[140:143], v[192:195], v[104:107]
	v_mfma_f32_16x16x32_bf16 v[92:95], v[116:119], v[200:203], v[92:95]
	v_mfma_f32_16x16x32_bf16 v[88:91], v[140:143], v[200:203], v[88:91]
	v_mfma_f32_16x16x32_bf16 v[76:79], v[116:119], v[208:211], v[76:79]
	v_mfma_f32_16x16x32_bf16 v[72:75], v[140:143], v[208:211], v[72:75]
	v_mfma_f32_16x16x32_bf16 v[124:127], v[144:147], v[164:167], v[124:127]
	v_mfma_f32_16x16x32_bf16 v[120:123], v[156:159], v[164:167], v[120:123]
	v_mfma_f32_16x16x32_bf16 v[100:103], v[144:147], v[188:191], v[100:103]
	v_mfma_f32_16x16x32_bf16 v[96:99], v[156:159], v[188:191], v[96:99]
	v_mfma_f32_16x16x32_bf16 v[84:87], v[144:147], v[196:199], v[84:87]
	v_mfma_f32_16x16x32_bf16 v[80:83], v[156:159], v[196:199], v[80:83]
	v_mfma_f32_16x16x32_bf16 v[68:71], v[144:147], v[204:207], v[68:71]
	v_mfma_f32_16x16x32_bf16 v[64:67], v[156:159], v[204:207], v[64:67]
	v_mfma_f32_16x16x32_bf16 v[124:127], v[148:151], v[168:171], v[124:127]
	v_mfma_f32_16x16x32_bf16 v[120:123], v[160:163], v[168:171], v[120:123]
	v_mfma_f32_16x16x32_bf16 v[100:103], v[148:151], v[192:195], v[100:103]
	v_mfma_f32_16x16x32_bf16 v[96:99], v[160:163], v[192:195], v[96:99]
	v_mfma_f32_16x16x32_bf16 v[84:87], v[148:151], v[200:203], v[84:87]
	v_mfma_f32_16x16x32_bf16 v[80:83], v[160:163], v[200:203], v[80:83]
	v_mfma_f32_16x16x32_bf16 v[68:71], v[148:151], v[208:211], v[68:71]
	v_mfma_f32_16x16x32_bf16 v[64:67], v[160:163], v[208:211], v[64:67]
	s_barrier
	ds_read_b128 v[164:167], v183 offset:49152
	ds_read_b128 v[168:171], v183 offset:50176
	ds_read_b128 v[188:191], v183 offset:51200
	ds_read_b128 v[192:195], v183 offset:52224
	ds_read_b128 v[196:199], v183 offset:53248
	ds_read_b128 v[200:203], v183 offset:54272
	ds_read_b128 v[204:207], v183 offset:55296
	ds_read_b128 v[208:211], v183 offset:56320
	s_add_i32 m0, s36, 0x18000
	s_nop 0
	global_load_lds_dwordx4 v176, s[26:27]
	s_nop 0
	s_add_i32 m0, s36, 0x1a000
	s_nop 0
	global_load_lds_dwordx4 v178, s[26:27]
	s_add_u32 s24, s24, 0x160080
	s_addc_u32 s25, s25, 0
	s_add_i32 m0, s36, 0x1c000
	s_nop 0
	global_load_lds_dwordx4 v176, s[24:25]
	s_nop 0
	s_add_i32 m0, s36, 0x1e000
	s_nop 0
	global_load_lds_dwordx4 v178, s[24:25]
	s_nop 0
	s_add_i32 m0, s36, 0x8000
	s_nop 0
	global_load_lds_dwordx4 v175, s[22:23]
	s_nop 0
	s_add_i32 m0, s36, 0xa000
	s_nop 0
	global_load_lds_dwordx4 v177, s[22:23]
	s_waitcnt vmcnt(8)
	s_waitcnt lgkmcnt(0)
	s_barrier
	v_mfma_f32_16x16x32_bf16 v[60:63], v[112:115], v[164:167], v[60:63]
	v_mfma_f32_16x16x32_bf16 v[56:59], v[136:139], v[164:167], v[56:59]
	v_mfma_f32_16x16x32_bf16 v[44:47], v[112:115], v[188:191], v[44:47]
	v_mfma_f32_16x16x32_bf16 v[40:43], v[136:139], v[188:191], v[40:43]
	v_mfma_f32_16x16x32_bf16 v[28:31], v[112:115], v[196:199], v[28:31]
	v_mfma_f32_16x16x32_bf16 v[24:27], v[136:139], v[196:199], v[24:27]
	v_mfma_f32_16x16x32_bf16 v[12:15], v[112:115], v[204:207], v[12:15]
	v_mfma_f32_16x16x32_bf16 v[8:11], v[136:139], v[204:207], v[8:11]
	v_mfma_f32_16x16x32_bf16 v[60:63], v[116:119], v[168:171], v[60:63]
	v_mfma_f32_16x16x32_bf16 v[56:59], v[140:143], v[168:171], v[56:59]
	v_mfma_f32_16x16x32_bf16 v[44:47], v[116:119], v[192:195], v[44:47]
	v_mfma_f32_16x16x32_bf16 v[40:43], v[140:143], v[192:195], v[40:43]
	v_mfma_f32_16x16x32_bf16 v[28:31], v[116:119], v[200:203], v[28:31]
	v_mfma_f32_16x16x32_bf16 v[24:27], v[140:143], v[200:203], v[24:27]
	v_mfma_f32_16x16x32_bf16 v[12:15], v[116:119], v[208:211], v[12:15]
	v_mfma_f32_16x16x32_bf16 v[8:11], v[140:143], v[208:211], v[8:11]
	v_mfma_f32_16x16x32_bf16 v[52:55], v[144:147], v[164:167], v[52:55]
	v_mfma_f32_16x16x32_bf16 v[48:51], v[156:159], v[164:167], v[48:51]
	v_mfma_f32_16x16x32_bf16 v[36:39], v[144:147], v[188:191], v[36:39]
	v_mfma_f32_16x16x32_bf16 v[32:35], v[156:159], v[188:191], v[32:35]
	v_mfma_f32_16x16x32_bf16 v[20:23], v[144:147], v[196:199], v[20:23]
	v_mfma_f32_16x16x32_bf16 v[16:19], v[156:159], v[196:199], v[16:19]
	v_mfma_f32_16x16x32_bf16 v[4:7], v[144:147], v[204:207], v[4:7]
	v_mfma_f32_16x16x32_bf16 v[0:3], v[156:159], v[204:207], v[0:3]
	v_mfma_f32_16x16x32_bf16 v[52:55], v[148:151], v[168:171], v[52:55]
	v_mfma_f32_16x16x32_bf16 v[48:51], v[160:163], v[168:171], v[48:51]
	v_mfma_f32_16x16x32_bf16 v[36:39], v[148:151], v[192:195], v[36:39]
	v_mfma_f32_16x16x32_bf16 v[32:35], v[160:163], v[192:195], v[32:35]
	v_mfma_f32_16x16x32_bf16 v[20:23], v[148:151], v[200:203], v[20:23]
	v_mfma_f32_16x16x32_bf16 v[16:19], v[160:163], v[200:203], v[16:19]
	v_mfma_f32_16x16x32_bf16 v[4:7], v[148:151], v[208:211], v[4:7]
	v_mfma_f32_16x16x32_bf16 v[0:3], v[160:163], v[208:211], v[0:3]
	s_barrier
	s_add_i32 s55, s55, 2
	s_add_u32 s51, s51, 0x100
	s_addc_u32 s52, s52, 0
	s_add_u32 s53, s53, 0x100
	s_addc_u32 s54, s54, 0
	s_add_u32 s6, s6, 0x100
	s_addc_u32 s7, s7, 0
	s_cmpk_gt_u32 s55, 0x55
	s_cbranch_scc0 .LBB0_838
	s_and_b64 vcc, exec, s[16:17]
	s_cbranch_vccz .LBB0_841
	s_barrier

.LBB0_930:
	s_ashr_i32 s37, s36, 31
	s_lshl_b64 s[38:39], s[36:37], 19
	s_add_u32 s38, s19, s38
	s_addc_u32 s39, s21, s39
	s_and_b64 s[40:41], s[4:5], exec
	s_cselect_b32 s9, s39, s45
	s_cselect_b32 s76, s38, s44
	s_ashr_i32 s35, s34, 31
	s_lshl_b64 s[40:41], s[34:35], 19
	s_add_u32 s40, s23, s40
	s_addc_u32 s41, s25, s41
	s_and_b64 s[46:47], s[4:5], exec
	ds_read_b128 v[0:3], v226 offset:3072
	ds_read_b128 v[4:7], v226 offset:2048
	ds_read_b128 v[8:11], v226 offset:1024
	ds_read_b128 v[12:15], v226
	ds_read_b128 v[16:19], v227 offset:3072
	ds_read_b128 v[20:23], v227 offset:2048
	ds_read_b128 v[24:27], v227 offset:1024
	ds_read_b128 v[28:31], v227
	s_cselect_b32 s35, s41, s43
	s_cselect_b32 s77, s40, s42
	s_lshl_b32 s46, s78, 11
	s_and_b32 s46, s46, 0x800
	s_or_b32 s54, s46, s56
	s_lshl_b64 s[48:49], s[36:37], 11
	s_add_u32 s46, s44, 0x100
	s_addc_u32 s47, s45, 0
	s_add_u32 s80, s42, 0x100
	s_addc_u32 s81, s43, 0
	s_add_u32 s50, s44, 0x180
	s_addc_u32 s51, s45, 0
	s_add_u32 s52, s42, 0x180
	s_addc_u32 s53, s43, 0
	ds_read_b128 v[32:35], v228
	ds_read_b128 v[36:39], v228 offset:1024
	ds_read_b128 v[40:43], v228 offset:2048
	ds_read_b128 v[44:47], v228 offset:3072
	ds_read_b128 v[48:51], v228 offset:4096
	ds_read_b128 v[52:55], v228 offset:5120
	ds_read_b128 v[56:59], v228 offset:6144
	ds_read_b128 v[60:63], v228 offset:7168
	s_add_u32 s82, s44, 0x40080
	s_addc_u32 s83, s45, 0
	s_add_i32 m0, s31, 0xc000
	s_nop 0
	global_load_lds_dwordx4 v219, s[82:83]
	s_nop 0
	s_add_i32 m0, s31, 0xe000
	s_nop 0
	global_load_lds_dwordx4 v221, s[82:83]
	s_waitcnt vmcnt(8)
	s_waitcnt lgkmcnt(0)
	s_barrier
	s_waitcnt lgkmcnt(7)
	v_mfma_i32_16x16x64_i8 v[64:67], v[28:31], v[32:35], 0
	s_mov_b32 s37, 0
	v_mfma_i32_16x16x64_i8 v[68:71], v[20:23], v[32:35], 0
	s_waitcnt lgkmcnt(5)
	v_mfma_i32_16x16x64_i8 v[72:75], v[28:31], v[40:43], 0
	v_mfma_i32_16x16x64_i8 v[76:79], v[20:23], v[40:43], 0
	s_waitcnt lgkmcnt(3)
	v_mfma_i32_16x16x64_i8 v[80:83], v[28:31], v[48:51], 0
	v_mfma_i32_16x16x64_i8 v[84:87], v[20:23], v[48:51], 0
	s_waitcnt lgkmcnt(1)
	v_mfma_i32_16x16x64_i8 v[92:95], v[20:23], v[56:59], 0
	v_mfma_i32_16x16x64_i8 v[136:139], v[24:27], v[36:39], v[64:67]
	v_mfma_i32_16x16x64_i8 v[144:147], v[16:19], v[36:39], v[68:71]
	v_mfma_i32_16x16x64_i8 v[148:151], v[24:27], v[44:47], v[72:75]
	v_mfma_i32_16x16x64_i8 v[76:79], v[16:19], v[44:47], v[76:79]
	v_mfma_i32_16x16x64_i8 v[80:83], v[24:27], v[52:55], v[80:83]
	v_mfma_i32_16x16x64_i8 v[84:87], v[16:19], v[52:55], v[84:87]
	v_mfma_i32_16x16x64_i8 v[88:91], v[28:31], v[56:59], 0
	s_waitcnt lgkmcnt(0)
	v_mfma_i32_16x16x64_i8 v[92:95], v[16:19], v[60:63], v[92:95]
	v_mfma_i32_16x16x64_i8 v[88:91], v[24:27], v[60:63], v[88:91]
	v_mfma_i32_16x16x64_i8 v[96:99], v[12:15], v[32:35], 0
	v_mfma_i32_16x16x64_i8 v[32:35], v[4:7], v[32:35], 0
	v_mfma_i32_16x16x64_i8 v[96:99], v[8:11], v[36:39], v[96:99]
	v_mfma_i32_16x16x64_i8 v[32:35], v[0:3], v[36:39], v[32:35]
	v_mfma_i32_16x16x64_i8 v[36:39], v[12:15], v[40:43], 0
	v_mfma_i32_16x16x64_i8 v[40:43], v[4:7], v[40:43], 0
	v_mfma_i32_16x16x64_i8 v[36:39], v[8:11], v[44:47], v[36:39]
	v_mfma_i32_16x16x64_i8 v[40:43], v[0:3], v[44:47], v[40:43]
	v_mfma_i32_16x16x64_i8 v[44:47], v[12:15], v[48:51], 0
	v_mfma_i32_16x16x64_i8 v[48:51], v[4:7], v[48:51], 0
	v_mfma_i32_16x16x64_i8 v[44:47], v[8:11], v[52:55], v[44:47]
	v_mfma_i32_16x16x64_i8 v[48:51], v[0:3], v[52:55], v[48:51]
	v_mfma_i32_16x16x64_i8 v[52:55], v[12:15], v[56:59], 0
	v_mfma_i32_16x16x64_i8 v[56:59], v[4:7], v[56:59], 0
	v_mfma_i32_16x16x64_i8 v[52:55], v[8:11], v[60:63], v[52:55]
	v_mfma_i32_16x16x64_i8 v[56:59], v[0:3], v[60:63], v[56:59]
	s_barrier
	ds_read_b128 v[60:63], v228 offset:16384
	ds_read_b128 v[100:103], v228 offset:17408
	ds_read_b128 v[104:107], v228 offset:18432
	ds_read_b128 v[108:111], v228 offset:19456
	ds_read_b128 v[112:115], v228 offset:20480
	ds_read_b128 v[116:119], v228 offset:21504
	ds_read_b128 v[120:123], v228 offset:22528
	ds_read_b128 v[124:127], v228 offset:23552
	s_add_i32 m0, s31, 0x10000
	s_nop 0
	global_load_lds_dwordx4 v220, s[80:81]
	s_nop 0
	s_add_i32 m0, s31, 0x12000
	s_nop 0
	global_load_lds_dwordx4 v222, s[80:81]
	s_add_u32 s80, s42, 0x40100
	s_addc_u32 s81, s43, 0
	s_add_i32 m0, s31, 0x14000
	s_nop 0
	global_load_lds_dwordx4 v220, s[80:81]
	s_nop 0
	s_add_i32 m0, s31, 0x16000
	s_nop 0
	global_load_lds_dwordx4 v222, s[80:81]
	s_nop 0
	s_add_i32 m0, s31, 0
	s_nop 0
	global_load_lds_dwordx4 v219, s[46:47]
	s_nop 0
	s_add_i32 m0, s31, 0x2000
	s_nop 0
	global_load_lds_dwordx4 v221, s[46:47]
	s_waitcnt vmcnt(8)
	s_waitcnt lgkmcnt(0)
	s_barrier
	v_mfma_i32_16x16x64_i8 v[132:135], v[20:23], v[60:63], 0
	v_mfma_i32_16x16x64_i8 v[168:171], v[16:19], v[100:103], v[132:135]
	v_mfma_i32_16x16x64_i8 v[132:135], v[28:31], v[104:107], 0
	v_mfma_i32_16x16x64_i8 v[204:207], v[24:27], v[108:111], v[132:135]
	v_mfma_i32_16x16x64_i8 v[132:135], v[20:23], v[104:107], 0
	v_mfma_i32_16x16x64_i8 v[128:131], v[28:31], v[60:63], 0
	v_mfma_i32_16x16x64_i8 v[214:217], v[16:19], v[108:111], v[132:135]
	v_mfma_i32_16x16x64_i8 v[132:135], v[28:31], v[112:115], 0
	v_mfma_i32_16x16x64_i8 v[128:131], v[24:27], v[100:103], v[128:131]
	v_mfma_i32_16x16x64_i8 v[232:235], v[24:27], v[116:119], v[132:135]
	v_mfma_i32_16x16x64_i8 v[132:135], v[20:23], v[112:115], 0
	v_mfma_i32_16x16x64_i8 v[28:31], v[28:31], v[120:123], 0
	v_mfma_i32_16x16x64_i8 v[20:23], v[20:23], v[120:123], 0
	v_mfma_i32_16x16x64_i8 v[236:239], v[16:19], v[116:119], v[132:135]
	v_mfma_i32_16x16x64_i8 v[24:27], v[24:27], v[124:127], v[28:31]
	v_mfma_i32_16x16x64_i8 v[16:19], v[16:19], v[124:127], v[20:23]
	v_mfma_i32_16x16x64_i8 v[20:23], v[12:15], v[60:63], 0
	v_mfma_i32_16x16x64_i8 v[28:31], v[4:7], v[60:63], 0
	v_mfma_i32_16x16x64_i8 v[20:23], v[8:11], v[100:103], v[20:23]
	v_mfma_i32_16x16x64_i8 v[28:31], v[0:3], v[100:103], v[28:31]
	v_mfma_i32_16x16x64_i8 v[60:63], v[12:15], v[104:107], 0
	v_mfma_i32_16x16x64_i8 v[100:103], v[4:7], v[104:107], 0
	v_mfma_i32_16x16x64_i8 v[104:107], v[12:15], v[112:115], 0
	v_mfma_i32_16x16x64_i8 v[100:103], v[0:3], v[108:111], v[100:103]
	v_mfma_i32_16x16x64_i8 v[240:243], v[8:11], v[116:119], v[104:107]
	v_mfma_i32_16x16x64_i8 v[104:107], v[4:7], v[112:115], 0
	v_mfma_i32_16x16x64_i8 v[12:15], v[12:15], v[120:123], 0
	v_mfma_i32_16x16x64_i8 v[4:7], v[4:7], v[120:123], 0
	v_mfma_i32_16x16x64_i8 v[60:63], v[8:11], v[108:111], v[60:63]
	v_mfma_i32_16x16x64_i8 v[244:247], v[0:3], v[116:119], v[104:107]
	v_mfma_i32_16x16x64_i8 v[8:11], v[8:11], v[124:127], v[12:15]
	v_mfma_i32_16x16x64_i8 v[0:3], v[0:3], v[124:127], v[4:7]
	s_barrier
	s_nop 1
	ds_read_b128 v[4:7], v229
	ds_read_b128 v[12:15], v229 offset:1024
	ds_read_b128 v[104:107], v229 offset:2048
	ds_read_b128 v[116:119], v229 offset:3072
	ds_read_b128 v[124:127], v230
	ds_read_b128 v[248:251], v230 offset:1024
	ds_read_b128 v[208:211], v230 offset:2048
	ds_read_b128 v[64:67], v230 offset:3072
	ds_read_b128 v[108:111], v228 offset:32768
	ds_read_b128 v[112:115], v228 offset:33792
	ds_read_b128 v[120:123], v228 offset:34816
	ds_read_b128 v[132:135], v228 offset:35840
	ds_read_b128 v[140:143], v228 offset:36864
	ds_read_b128 v[152:155], v228 offset:37888
	ds_read_b128 v[68:71], v228 offset:38912
	ds_read_b128 v[72:75], v228 offset:39936
	s_add_u32 s44, s44, 0x40100
	s_addc_u32 s45, s45, 0
	s_add_i32 m0, s31, 0x4000
	s_nop 0
	global_load_lds_dwordx4 v219, s[44:45]
	s_nop 0
	s_add_i32 m0, s31, 0x6000
	s_nop 0
	global_load_lds_dwordx4 v221, s[44:45]
	s_waitcnt vmcnt(8)
	s_waitcnt lgkmcnt(0)
	s_barrier
	v_mfma_i32_16x16x64_i8 v[76:79], v[104:107], v[120:123], v[76:79]
	v_mfma_i32_16x16x64_i8 v[180:183], v[116:119], v[132:135], v[76:79]
	v_mfma_i32_16x16x64_i8 v[76:79], v[4:7], v[140:143], v[80:83]
	v_mfma_i32_16x16x64_i8 v[136:139], v[4:7], v[108:111], v[136:139]
	v_mfma_i32_16x16x64_i8 v[164:167], v[12:15], v[152:155], v[76:79]
	v_mfma_i32_16x16x64_i8 v[76:79], v[104:107], v[140:143], v[84:87]
	v_mfma_i32_16x16x64_i8 v[200:203], v[12:15], v[112:115], v[136:139]
	v_mfma_i32_16x16x64_i8 v[136:139], v[104:107], v[108:111], v[144:147]
	v_mfma_i32_16x16x64_i8 v[160:163], v[116:119], v[152:155], v[76:79]
	v_mfma_i32_16x16x64_i8 v[76:79], v[4:7], v[68:71], v[88:91]
	v_mfma_i32_16x16x64_i8 v[196:199], v[116:119], v[112:115], v[136:139]
	v_mfma_i32_16x16x64_i8 v[136:139], v[4:7], v[120:123], v[148:151]
	v_mfma_i32_16x16x64_i8 v[148:151], v[12:15], v[72:75], v[76:79]
	v_mfma_i32_16x16x64_i8 v[76:79], v[104:107], v[68:71], v[92:95]
	v_mfma_i32_16x16x64_i8 v[184:187], v[12:15], v[132:135], v[136:139]
	v_mfma_i32_16x16x64_i8 v[144:147], v[116:119], v[72:75], v[76:79]
	v_mfma_i32_16x16x64_i8 v[32:35], v[208:211], v[108:111], v[32:35]
	v_mfma_i32_16x16x64_i8 v[188:191], v[64:67], v[112:115], v[32:35]
	v_mfma_i32_16x16x64_i8 v[32:35], v[124:127], v[120:123], v[36:39]
	v_mfma_i32_16x16x64_i8 v[176:179], v[248:251], v[132:135], v[32:35]
	v_mfma_i32_16x16x64_i8 v[32:35], v[208:211], v[120:123], v[40:43]
	v_mfma_i32_16x16x64_i8 v[172:175], v[64:67], v[132:135], v[32:35]
	v_mfma_i32_16x16x64_i8 v[32:35], v[124:127], v[140:143], v[44:47]
	v_mfma_i32_16x16x64_i8 v[156:159], v[248:251], v[152:155], v[32:35]
	v_mfma_i32_16x16x64_i8 v[32:35], v[208:211], v[140:143], v[48:51]
	v_mfma_i32_16x16x64_i8 v[152:155], v[64:67], v[152:155], v[32:35]
	v_mfma_i32_16x16x64_i8 v[32:35], v[124:127], v[68:71], v[52:55]
	v_mfma_i32_16x16x64_i8 v[76:79], v[124:127], v[108:111], v[96:99]
	v_mfma_i32_16x16x64_i8 v[140:143], v[248:251], v[72:75], v[32:35]
	v_mfma_i32_16x16x64_i8 v[32:35], v[208:211], v[68:71], v[56:59]
	v_mfma_i32_16x16x64_i8 v[192:195], v[248:251], v[112:115], v[76:79]
	v_mfma_i32_16x16x64_i8 v[136:139], v[64:67], v[72:75], v[32:35]
	s_barrier
	s_nop 3
	ds_read_b128 v[32:35], v228 offset:49152
	ds_read_b128 v[36:39], v228 offset:50176
	ds_read_b128 v[40:43], v228 offset:51200
	ds_read_b128 v[44:47], v228 offset:52224
	ds_read_b128 v[48:51], v228 offset:53248
	ds_read_b128 v[52:55], v228 offset:54272
	ds_read_b128 v[56:59], v228 offset:55296
	ds_read_b128 v[88:91], v228 offset:56320
	s_add_i32 m0, s31, 0x18000
	s_nop 0
	global_load_lds_dwordx4 v220, s[52:53]
	s_nop 0
	s_add_i32 m0, s31, 0x1a000
	s_nop 0
	global_load_lds_dwordx4 v222, s[52:53]
	s_add_u32 s44, s42, 0x40180
	s_addc_u32 s45, s43, 0
	s_add_i32 m0, s31, 0x1c000
	s_nop 0
	global_load_lds_dwordx4 v220, s[44:45]
	s_nop 0
	s_add_i32 m0, s31, 0x1e000
	s_nop 0
	global_load_lds_dwordx4 v222, s[44:45]
	s_nop 0
	s_add_i32 m0, s31, 0x8000
	s_nop 0
	global_load_lds_dwordx4 v219, s[50:51]
	s_nop 0
	s_add_i32 m0, s31, 0xa000
	s_nop 0
	global_load_lds_dwordx4 v221, s[50:51]
	s_waitcnt vmcnt(8)
	s_waitcnt lgkmcnt(0)
	s_barrier
	v_mfma_i32_16x16x64_i8 v[68:71], v[4:7], v[32:35], v[128:131]
	v_mfma_i32_16x16x64_i8 v[132:135], v[12:15], v[36:39], v[68:71]
	v_mfma_i32_16x16x64_i8 v[68:71], v[104:107], v[32:35], v[168:171]
	v_mfma_i32_16x16x64_i8 v[128:131], v[116:119], v[36:39], v[68:71]
	v_mfma_i32_16x16x64_i8 v[68:71], v[4:7], v[40:43], v[204:207]
	v_mfma_i32_16x16x64_i8 v[112:115], v[12:15], v[44:47], v[68:71]
	v_mfma_i32_16x16x64_i8 v[68:71], v[104:107], v[40:43], v[214:217]
	v_mfma_i32_16x16x64_i8 v[108:111], v[116:119], v[44:47], v[68:71]
	v_mfma_i32_16x16x64_i8 v[68:71], v[4:7], v[48:51], v[232:235]
	v_mfma_i32_16x16x64_i8 v[4:7], v[4:7], v[56:59], v[24:27]
	v_mfma_i32_16x16x64_i8 v[96:99], v[12:15], v[52:55], v[68:71]
	v_mfma_i32_16x16x64_i8 v[68:71], v[104:107], v[48:51], v[236:239]
	v_mfma_i32_16x16x64_i8 v[76:79], v[12:15], v[88:91], v[4:7]
	v_mfma_i32_16x16x64_i8 v[4:7], v[104:107], v[56:59], v[16:19]
	v_mfma_i32_16x16x64_i8 v[92:95], v[116:119], v[52:55], v[68:71]
	v_mfma_i32_16x16x64_i8 v[72:75], v[116:119], v[88:91], v[4:7]
	v_mfma_i32_16x16x64_i8 v[4:7], v[124:127], v[32:35], v[20:23]
	v_mfma_i32_16x16x64_i8 v[120:123], v[248:251], v[36:39], v[4:7]
	v_mfma_i32_16x16x64_i8 v[4:7], v[208:211], v[32:35], v[28:31]
	v_mfma_i32_16x16x64_i8 v[116:119], v[64:67], v[36:39], v[4:7]
	v_mfma_i32_16x16x64_i8 v[4:7], v[124:127], v[40:43], v[60:63]
	v_mfma_i32_16x16x64_i8 v[104:107], v[248:251], v[44:47], v[4:7]
	v_mfma_i32_16x16x64_i8 v[4:7], v[208:211], v[40:43], v[100:103]
	v_mfma_i32_16x16x64_i8 v[100:103], v[64:67], v[44:47], v[4:7]
	v_mfma_i32_16x16x64_i8 v[4:7], v[124:127], v[48:51], v[240:243]
	v_mfma_i32_16x16x64_i8 v[84:87], v[248:251], v[52:55], v[4:7]
	v_mfma_i32_16x16x64_i8 v[4:7], v[208:211], v[48:51], v[244:247]
	v_mfma_i32_16x16x64_i8 v[80:83], v[64:67], v[52:55], v[4:7]
	v_mfma_i32_16x16x64_i8 v[4:7], v[124:127], v[56:59], v[8:11]
	v_mfma_i32_16x16x64_i8 v[0:3], v[208:211], v[56:59], v[0:3]
	v_mfma_i32_16x16x64_i8 v[68:71], v[248:251], v[88:91], v[4:7]
	v_mfma_i32_16x16x64_i8 v[64:67], v[64:67], v[88:91], v[0:3]
	s_barrier
	s_add_u32 s44, s27, s48
	s_addc_u32 s45, s29, s49
	s_add_u32 s79, s42, 0x200
	s_addc_u32 s80, s43, 0
	s_add_i32 s81, s54, 0
	s_add_i32 s81, s81, 0x20000

.LBB0_933:
	ds_read_b128 v[0:3], v227
	ds_read_b128 v[4:7], v227 offset:1024
	ds_read_b128 v[8:11], v227 offset:2048
	ds_read_b128 v[12:15], v227 offset:3072
	ds_read_b128 v[16:19], v226
	ds_read_b128 v[20:23], v226 offset:1024
	ds_read_b128 v[24:27], v226 offset:2048
	ds_read_b128 v[28:31], v226 offset:3072
	s_add_u32 s42, s46, 0x100
	s_addc_u32 s43, s47, 0
	s_and_b64 s[48:49], s[48:49], exec
	s_cselect_b32 s54, s76, s42
	s_cselect_b32 s55, s9, s43
	s_cselect_b32 s51, s35, s80
	s_cselect_b32 s50, s77, s79
	s_add_u32 s48, s54, 0x80
	s_addc_u32 s49, s55, 0
	s_add_u32 s52, s50, 0x80
	s_addc_u32 s53, s51, 0
	ds_read_b128 v[32:35], v228
	ds_read_b128 v[36:39], v228 offset:1024
	ds_read_b128 v[40:43], v228 offset:2048
	ds_read_b128 v[44:47], v228 offset:3072
	ds_read_b128 v[48:51], v228 offset:4096
	ds_read_b128 v[52:55], v228 offset:5120
	ds_read_b128 v[56:59], v228 offset:6144
	ds_read_b128 v[60:63], v228 offset:7168
	s_add_u32 s46, s46, 0x40080
	s_addc_u32 s47, s47, 0
	s_add_i32 m0, s31, 0xc000
	s_nop 0
	global_load_lds_dwordx4 v219, s[46:47]
	s_nop 0
	s_add_i32 m0, s31, 0xe000
	s_nop 0
	global_load_lds_dwordx4 v221, s[46:47]
	s_waitcnt vmcnt(8)
	s_waitcnt lgkmcnt(0)
	s_barrier
	v_mfma_i32_16x16x64_i8 v[180:183], v[8:11], v[40:43], v[180:183]
	v_mfma_i32_16x16x64_i8 v[164:167], v[0:3], v[48:51], v[164:167]
	v_mfma_i32_16x16x64_i8 v[160:163], v[8:11], v[48:51], v[160:163]
	v_mfma_i32_16x16x64_i8 v[148:151], v[0:3], v[56:59], v[148:151]
	v_mfma_i32_16x16x64_i8 v[144:147], v[8:11], v[56:59], v[144:147]
	v_mfma_i32_16x16x64_i8 v[88:91], v[0:3], v[32:35], v[200:203]
	v_mfma_i32_16x16x64_i8 v[124:127], v[8:11], v[32:35], v[196:199]
	v_mfma_i32_16x16x64_i8 v[168:171], v[0:3], v[40:43], v[184:187]
	v_mfma_i32_16x16x64_i8 v[180:183], v[12:15], v[44:47], v[180:183]
	v_mfma_i32_16x16x64_i8 v[164:167], v[4:7], v[52:55], v[164:167]
	v_mfma_i32_16x16x64_i8 v[160:163], v[12:15], v[52:55], v[160:163]
	v_mfma_i32_16x16x64_i8 v[148:151], v[4:7], v[60:63], v[148:151]
	v_mfma_i32_16x16x64_i8 v[144:147], v[12:15], v[60:63], v[144:147]
	v_mfma_i32_16x16x64_i8 v[88:91], v[4:7], v[36:39], v[88:91]
	v_mfma_i32_16x16x64_i8 v[124:127], v[12:15], v[36:39], v[124:127]
	v_mfma_i32_16x16x64_i8 v[168:171], v[4:7], v[44:47], v[168:171]
	v_mfma_i32_16x16x64_i8 v[184:187], v[16:19], v[32:35], v[192:195]
	v_mfma_i32_16x16x64_i8 v[32:35], v[24:27], v[32:35], v[188:191]
	v_mfma_i32_16x16x64_i8 v[192:195], v[20:23], v[36:39], v[184:187]
	v_mfma_i32_16x16x64_i8 v[32:35], v[28:31], v[36:39], v[32:35]
	v_mfma_i32_16x16x64_i8 v[36:39], v[16:19], v[40:43], v[176:179]
	v_mfma_i32_16x16x64_i8 v[40:43], v[24:27], v[40:43], v[172:175]
	v_mfma_i32_16x16x64_i8 v[36:39], v[20:23], v[44:47], v[36:39]
	v_mfma_i32_16x16x64_i8 v[40:43], v[28:31], v[44:47], v[40:43]
	v_mfma_i32_16x16x64_i8 v[44:47], v[16:19], v[48:51], v[156:159]
	v_mfma_i32_16x16x64_i8 v[48:51], v[24:27], v[48:51], v[152:155]
	v_mfma_i32_16x16x64_i8 v[44:47], v[20:23], v[52:55], v[44:47]
	v_mfma_i32_16x16x64_i8 v[48:51], v[28:31], v[52:55], v[48:51]
	v_mfma_i32_16x16x64_i8 v[52:55], v[16:19], v[56:59], v[140:143]
	v_mfma_i32_16x16x64_i8 v[56:59], v[24:27], v[56:59], v[136:139]
	v_mfma_i32_16x16x64_i8 v[52:55], v[20:23], v[60:63], v[52:55]
	v_mfma_i32_16x16x64_i8 v[56:59], v[28:31], v[60:63], v[56:59]
	s_barrier
	ds_read_b128 v[60:63], v228 offset:16384
	ds_read_b128 v[136:139], v228 offset:17408
	ds_read_b128 v[140:143], v228 offset:18432
	ds_read_b128 v[152:155], v228 offset:19456
	ds_read_b128 v[156:159], v228 offset:20480
	ds_read_b128 v[172:175], v228 offset:21504
	ds_read_b128 v[176:179], v228 offset:22528
	ds_read_b128 v[184:187], v228 offset:23552
	s_add_i32 m0, s31, 0x10000
	s_nop 0
	global_load_lds_dwordx4 v220, s[50:51]
	s_nop 0
	s_add_i32 m0, s31, 0x12000
	s_nop 0
	global_load_lds_dwordx4 v222, s[50:51]
	s_add_u32 s46, s50, 0x40000
	s_addc_u32 s47, s51, 0
	s_add_i32 m0, s31, 0x14000
	s_nop 0
	global_load_lds_dwordx4 v220, s[46:47]
	s_nop 0
	s_add_i32 m0, s31, 0x16000
	s_nop 0
	global_load_lds_dwordx4 v222, s[46:47]
	s_nop 0
	s_add_i32 m0, s31, 0
	s_nop 0
	global_load_lds_dwordx4 v219, s[54:55]
	s_nop 0
	s_add_i32 m0, s31, 0x2000
	s_nop 0
	global_load_lds_dwordx4 v221, s[54:55]
	s_waitcnt vmcnt(8)
	s_waitcnt lgkmcnt(0)
	s_barrier
	v_mfma_i32_16x16x64_i8 v[132:135], v[0:3], v[60:63], v[132:135]
	v_mfma_i32_16x16x64_i8 v[112:115], v[0:3], v[140:143], v[112:115]
	v_mfma_i32_16x16x64_i8 v[96:99], v[0:3], v[156:159], v[96:99]
	v_mfma_i32_16x16x64_i8 v[0:3], v[0:3], v[176:179], v[76:79]
	v_mfma_i32_16x16x64_i8 v[128:131], v[8:11], v[60:63], v[128:131]
	v_mfma_i32_16x16x64_i8 v[108:111], v[8:11], v[140:143], v[108:111]
	v_mfma_i32_16x16x64_i8 v[92:95], v[8:11], v[156:159], v[92:95]
	v_mfma_i32_16x16x64_i8 v[76:79], v[4:7], v[184:187], v[0:3]
	v_mfma_i32_16x16x64_i8 v[0:3], v[8:11], v[176:179], v[72:75]
	v_mfma_i32_16x16x64_i8 v[132:135], v[4:7], v[136:139], v[132:135]
	v_mfma_i32_16x16x64_i8 v[128:131], v[12:15], v[136:139], v[128:131]
	v_mfma_i32_16x16x64_i8 v[112:115], v[4:7], v[152:155], v[112:115]
	v_mfma_i32_16x16x64_i8 v[108:111], v[12:15], v[152:155], v[108:111]
	v_mfma_i32_16x16x64_i8 v[96:99], v[4:7], v[172:175], v[96:99]
	v_mfma_i32_16x16x64_i8 v[92:95], v[12:15], v[172:175], v[92:95]
	v_mfma_i32_16x16x64_i8 v[72:75], v[12:15], v[184:187], v[0:3]
	v_mfma_i32_16x16x64_i8 v[0:3], v[16:19], v[60:63], v[120:123]
	v_mfma_i32_16x16x64_i8 v[120:123], v[20:23], v[136:139], v[0:3]
	v_mfma_i32_16x16x64_i8 v[0:3], v[24:27], v[60:63], v[116:119]
	v_mfma_i32_16x16x64_i8 v[116:119], v[28:31], v[136:139], v[0:3]
	v_mfma_i32_16x16x64_i8 v[0:3], v[16:19], v[140:143], v[104:107]
	v_mfma_i32_16x16x64_i8 v[104:107], v[20:23], v[152:155], v[0:3]
	v_mfma_i32_16x16x64_i8 v[0:3], v[24:27], v[140:143], v[100:103]
	v_mfma_i32_16x16x64_i8 v[100:103], v[28:31], v[152:155], v[0:3]
	v_mfma_i32_16x16x64_i8 v[0:3], v[16:19], v[156:159], v[84:87]
	v_mfma_i32_16x16x64_i8 v[84:87], v[20:23], v[172:175], v[0:3]
	v_mfma_i32_16x16x64_i8 v[0:3], v[24:27], v[156:159], v[80:83]
	v_mfma_i32_16x16x64_i8 v[80:83], v[28:31], v[172:175], v[0:3]
	v_mfma_i32_16x16x64_i8 v[0:3], v[16:19], v[176:179], v[68:71]
	v_mfma_i32_16x16x64_i8 v[68:71], v[20:23], v[184:187], v[0:3]
	v_mfma_i32_16x16x64_i8 v[0:3], v[24:27], v[176:179], v[64:67]
	v_mfma_i32_16x16x64_i8 v[64:67], v[28:31], v[184:187], v[0:3]
	s_barrier
	ds_read_b128 v[16:19], v229
	ds_read_b128 v[8:11], v229 offset:1024
	ds_read_b128 v[4:7], v229 offset:2048
	s_nop 1
	ds_read_b128 v[0:3], v229 offset:3072
	ds_read_b128 v[28:31], v230
	ds_read_b128 v[24:27], v230 offset:1024
	ds_read_b128 v[20:23], v230 offset:2048
	ds_read_b128 v[12:15], v230 offset:3072
	ds_read_b128 v[60:63], v228 offset:32768
	ds_read_b128 v[136:139], v228 offset:33792
	ds_read_b128 v[140:143], v228 offset:34816
	ds_read_b128 v[152:155], v228 offset:35840
	ds_read_b128 v[204:207], v228 offset:36864
	ds_read_b128 v[208:211], v228 offset:37888
	ds_read_b128 v[214:217], v228 offset:38912
	ds_read_b128 v[232:235], v228 offset:39936
	s_add_u32 s46, s54, 0x40000
	s_addc_u32 s47, s55, 0
	s_add_i32 m0, s31, 0x4000
	s_nop 0
	global_load_lds_dwordx4 v219, s[46:47]
	s_nop 0
	s_add_i32 m0, s31, 0x6000
	s_nop 0
	global_load_lds_dwordx4 v221, s[46:47]
	s_waitcnt vmcnt(8)
	s_waitcnt lgkmcnt(0)
	s_barrier
	v_mfma_i32_16x16x64_i8 v[88:91], v[16:19], v[60:63], v[88:91]
	v_mfma_i32_16x16x64_i8 v[200:203], v[8:11], v[136:139], v[88:91]
	v_mfma_i32_16x16x64_i8 v[88:91], v[4:7], v[60:63], v[124:127]
	v_mfma_i32_16x16x64_i8 v[196:199], v[0:3], v[136:139], v[88:91]
	v_mfma_i32_16x16x64_i8 v[88:91], v[16:19], v[140:143], v[168:171]
	v_mfma_i32_16x16x64_i8 v[184:187], v[8:11], v[152:155], v[88:91]
	v_mfma_i32_16x16x64_i8 v[88:91], v[4:7], v[140:143], v[180:183]
	v_mfma_i32_16x16x64_i8 v[180:183], v[0:3], v[152:155], v[88:91]
	v_mfma_i32_16x16x64_i8 v[88:91], v[16:19], v[204:207], v[164:167]
	v_mfma_i32_16x16x64_i8 v[164:167], v[8:11], v[208:211], v[88:91]
	v_mfma_i32_16x16x64_i8 v[88:91], v[4:7], v[204:207], v[160:163]
	v_mfma_i32_16x16x64_i8 v[160:163], v[0:3], v[208:211], v[88:91]
	v_mfma_i32_16x16x64_i8 v[88:91], v[16:19], v[214:217], v[148:151]
	v_mfma_i32_16x16x64_i8 v[148:151], v[8:11], v[232:235], v[88:91]
	v_mfma_i32_16x16x64_i8 v[88:91], v[4:7], v[214:217], v[144:147]
	v_mfma_i32_16x16x64_i8 v[144:147], v[0:3], v[232:235], v[88:91]
	v_mfma_i32_16x16x64_i8 v[32:35], v[20:23], v[60:63], v[32:35]
	v_mfma_i32_16x16x64_i8 v[188:191], v[12:15], v[136:139], v[32:35]
	v_mfma_i32_16x16x64_i8 v[32:35], v[28:31], v[140:143], v[36:39]
	v_mfma_i32_16x16x64_i8 v[176:179], v[24:27], v[152:155], v[32:35]
	v_mfma_i32_16x16x64_i8 v[32:35], v[20:23], v[140:143], v[40:43]
	v_mfma_i32_16x16x64_i8 v[172:175], v[12:15], v[152:155], v[32:35]
	v_mfma_i32_16x16x64_i8 v[32:35], v[28:31], v[204:207], v[44:47]
	v_mfma_i32_16x16x64_i8 v[156:159], v[24:27], v[208:211], v[32:35]
	v_mfma_i32_16x16x64_i8 v[32:35], v[20:23], v[204:207], v[48:51]
	v_mfma_i32_16x16x64_i8 v[152:155], v[12:15], v[208:211], v[32:35]
	v_mfma_i32_16x16x64_i8 v[32:35], v[28:31], v[214:217], v[52:55]
	v_mfma_i32_16x16x64_i8 v[88:91], v[28:31], v[60:63], v[192:195]
	v_mfma_i32_16x16x64_i8 v[140:143], v[24:27], v[232:235], v[32:35]
	v_mfma_i32_16x16x64_i8 v[32:35], v[20:23], v[214:217], v[56:59]
	v_mfma_i32_16x16x64_i8 v[192:195], v[24:27], v[136:139], v[88:91]
	v_mfma_i32_16x16x64_i8 v[136:139], v[12:15], v[232:235], v[32:35]
	s_barrier
	ds_read_b128 v[60:63], v228 offset:49152
	ds_read_b128 v[56:59], v228 offset:50176
	ds_read_b128 v[52:55], v228 offset:51200
	ds_read_b128 v[48:51], v228 offset:52224
	ds_read_b128 v[44:47], v228 offset:53248
	ds_read_b128 v[40:43], v228 offset:54272
	ds_read_b128 v[36:39], v228 offset:55296
	ds_read_b128 v[32:35], v228 offset:56320
	s_add_i32 m0, s31, 0x18000
	s_nop 0
	global_load_lds_dwordx4 v220, s[52:53]
	s_nop 0
	s_add_i32 m0, s31, 0x1a000
	s_nop 0
	global_load_lds_dwordx4 v222, s[52:53]
	s_add_u32 s46, s50, 0x40080
	s_addc_u32 s47, s51, 0
	s_add_i32 m0, s31, 0x1c000
	s_nop 0
	global_load_lds_dwordx4 v220, s[46:47]
	s_nop 0
	s_add_i32 m0, s31, 0x1e000
	s_nop 0
	global_load_lds_dwordx4 v222, s[46:47]
	s_nop 0
	s_add_i32 m0, s31, 0x8000
	s_nop 0
	global_load_lds_dwordx4 v219, s[48:49]
	s_nop 0
	s_add_i32 m0, s31, 0xa000
	s_nop 0
	global_load_lds_dwordx4 v221, s[48:49]
	s_waitcnt vmcnt(8)
	s_waitcnt lgkmcnt(0)
	s_barrier
	v_mfma_i32_16x16x64_i8 v[88:91], v[16:19], v[60:63], v[132:135]
	v_mfma_i32_16x16x64_i8 v[132:135], v[8:11], v[56:59], v[88:91]
	v_mfma_i32_16x16x64_i8 v[88:91], v[4:7], v[60:63], v[128:131]
	v_mfma_i32_16x16x64_i8 v[128:131], v[0:3], v[56:59], v[88:91]
	v_mfma_i32_16x16x64_i8 v[88:91], v[16:19], v[52:55], v[112:115]
	v_mfma_i32_16x16x64_i8 v[112:115], v[8:11], v[48:51], v[88:91]
	v_mfma_i32_16x16x64_i8 v[88:91], v[4:7], v[52:55], v[108:111]
	v_mfma_i32_16x16x64_i8 v[108:111], v[0:3], v[48:51], v[88:91]
	v_mfma_i32_16x16x64_i8 v[88:91], v[16:19], v[44:47], v[96:99]
	v_mfma_i32_16x16x64_i8 v[96:99], v[8:11], v[40:43], v[88:91]
	v_mfma_i32_16x16x64_i8 v[88:91], v[4:7], v[44:47], v[92:95]
	v_mfma_i32_16x16x64_i8 v[76:79], v[16:19], v[36:39], v[76:79]
	v_mfma_i32_16x16x64_i8 v[72:75], v[4:7], v[36:39], v[72:75]
	v_mfma_i32_16x16x64_i8 v[92:95], v[0:3], v[40:43], v[88:91]
	v_mfma_i32_16x16x64_i8 v[76:79], v[8:11], v[32:35], v[76:79]
	v_mfma_i32_16x16x64_i8 v[72:75], v[0:3], v[32:35], v[72:75]
	v_mfma_i32_16x16x64_i8 v[88:91], v[28:31], v[60:63], v[120:123]
	v_mfma_i32_16x16x64_i8 v[120:123], v[24:27], v[56:59], v[88:91]
	v_mfma_i32_16x16x64_i8 v[88:91], v[20:23], v[60:63], v[116:119]
	v_mfma_i32_16x16x64_i8 v[116:119], v[12:15], v[56:59], v[88:91]
	v_mfma_i32_16x16x64_i8 v[88:91], v[28:31], v[52:55], v[104:107]
	v_mfma_i32_16x16x64_i8 v[104:107], v[24:27], v[48:51], v[88:91]
	v_mfma_i32_16x16x64_i8 v[88:91], v[20:23], v[52:55], v[100:103]
	v_mfma_i32_16x16x64_i8 v[84:87], v[28:31], v[44:47], v[84:87]
	v_mfma_i32_16x16x64_i8 v[80:83], v[20:23], v[44:47], v[80:83]
	v_mfma_i32_16x16x64_i8 v[68:71], v[28:31], v[36:39], v[68:71]
	v_mfma_i32_16x16x64_i8 v[64:67], v[20:23], v[36:39], v[64:67]
	v_mfma_i32_16x16x64_i8 v[100:103], v[12:15], v[48:51], v[88:91]
	v_mfma_i32_16x16x64_i8 v[84:87], v[24:27], v[40:43], v[84:87]
	v_mfma_i32_16x16x64_i8 v[80:83], v[12:15], v[40:43], v[80:83]
	v_mfma_i32_16x16x64_i8 v[68:71], v[24:27], v[32:35], v[68:71]
	v_mfma_i32_16x16x64_i8 v[64:67], v[12:15], v[32:35], v[64:67]
	s_barrier
	s_add_i32 s37, s37, 2
	s_add_u32 s79, s79, 0x100
	s_addc_u32 s80, s80, 0
	s_cmp_gt_u32 s37, 13
	s_cbranch_scc1 .LBB0_935
	s_mov_b64 s[46:47], s[42:43]
	s_branch .LBB0_931

.LBB0_1108:
	s_ashr_i32 s23, s22, 31
	s_lshl_b64 s[24:25], s[22:23], 20
	s_add_u32 s24, s42, s24
	s_addc_u32 s25, s43, s25
	s_and_b64 s[26:27], s[4:5], exec
	ds_read_b128 v[0:3], v143
	ds_read_b128 v[4:7], v143 offset:1024
	ds_read_b128 v[8:11], v143 offset:2048
	s_waitcnt vmcnt(2)
	ds_read_b128 v[12:15], v143 offset:3072
	s_waitcnt vmcnt(1)
	ds_read_b128 v[16:19], v144
	s_waitcnt vmcnt(0)
	ds_read_b128 v[20:23], v144 offset:1024
	ds_read_b128 v[24:27], v144 offset:2048
	ds_read_b128 v[28:31], v144 offset:3072
	s_cselect_b32 s23, s25, s31
	s_cselect_b32 s51, s24, s30
	s_ashr_i32 s21, s20, 31
	s_lshl_b64 s[26:27], s[20:21], 20
	s_add_u32 s26, s44, s26
	s_addc_u32 s27, s45, s27
	s_and_b64 s[36:37], s[4:5], exec
	s_cselect_b32 s21, s27, s35
	s_cselect_b32 s52, s26, s34
	s_add_u32 s40, s30, 0x100
	s_addc_u32 s41, s31, 0
	s_add_u32 s54, s34, 0x100
	s_addc_u32 s55, s35, 0
	s_add_u32 s36, s30, 0x180
	s_addc_u32 s37, s31, 0
	ds_read_b128 v[32:35], v145
	ds_read_b128 v[36:39], v145 offset:1024
	ds_read_b128 v[40:43], v145 offset:2048
	ds_read_b128 v[44:47], v145 offset:3072
	ds_read_b128 v[48:51], v145 offset:4096
	ds_read_b128 v[52:55], v145 offset:5120
	ds_read_b128 v[56:59], v145 offset:6144
	ds_read_b128 v[60:63], v145 offset:7168
	s_add_u32 s38, s34, 0x180
	s_addc_u32 s39, s35, 0
	s_add_u32 s56, s30, 0x80080
	s_addc_u32 s57, s31, 0
	s_add_i32 m0, s2, 0xc000
	s_nop 0
	global_load_lds_dwordx4 v139, s[56:57]
	s_nop 0
	s_add_i32 m0, s2, 0xe000
	s_nop 0
	global_load_lds_dwordx4 v141, s[56:57]
	s_waitcnt vmcnt(8)
	s_waitcnt lgkmcnt(0)
	s_barrier
	v_mfma_f32_16x16x32_bf16 v[64:67], v[0:3], v[32:35], 0
	v_mfma_f32_16x16x32_bf16 v[68:71], v[8:11], v[32:35], 0
	v_mfma_f32_16x16x32_bf16 v[72:75], v[0:3], v[40:43], 0
	v_mfma_f32_16x16x32_bf16 v[76:79], v[8:11], v[40:43], 0
	v_mfma_f32_16x16x32_bf16 v[80:83], v[0:3], v[48:51], 0
	v_mfma_f32_16x16x32_bf16 v[84:87], v[8:11], v[48:51], 0
	v_mfma_f32_16x16x32_bf16 v[88:91], v[0:3], v[56:59], 0
	v_mfma_f32_16x16x32_bf16 v[92:95], v[8:11], v[56:59], 0
	v_mfma_f32_16x16x32_bf16 v[64:67], v[4:7], v[36:39], v[64:67]
	v_mfma_f32_16x16x32_bf16 v[68:71], v[12:15], v[36:39], v[68:71]
	v_mfma_f32_16x16x32_bf16 v[72:75], v[4:7], v[44:47], v[72:75]
	v_mfma_f32_16x16x32_bf16 v[76:79], v[12:15], v[44:47], v[76:79]
	v_mfma_f32_16x16x32_bf16 v[80:83], v[4:7], v[52:55], v[80:83]
	v_mfma_f32_16x16x32_bf16 v[84:87], v[12:15], v[52:55], v[84:87]
	v_mfma_f32_16x16x32_bf16 v[88:91], v[4:7], v[60:63], v[88:91]
	v_mfma_f32_16x16x32_bf16 v[96:99], v[12:15], v[60:63], v[92:95]
	v_mfma_f32_16x16x32_bf16 v[92:95], v[16:19], v[32:35], 0
	v_mfma_f32_16x16x32_bf16 v[32:35], v[24:27], v[32:35], 0
	v_mfma_f32_16x16x32_bf16 v[104:107], v[20:23], v[36:39], v[92:95]
	v_mfma_f32_16x16x32_bf16 v[32:35], v[28:31], v[36:39], v[32:35]
	v_mfma_f32_16x16x32_bf16 v[36:39], v[16:19], v[40:43], 0
	v_mfma_f32_16x16x32_bf16 v[40:43], v[24:27], v[40:43], 0
	v_mfma_f32_16x16x32_bf16 v[36:39], v[20:23], v[44:47], v[36:39]
	v_mfma_f32_16x16x32_bf16 v[40:43], v[28:31], v[44:47], v[40:43]
	v_mfma_f32_16x16x32_bf16 v[44:47], v[16:19], v[48:51], 0
	v_mfma_f32_16x16x32_bf16 v[48:51], v[24:27], v[48:51], 0
	v_mfma_f32_16x16x32_bf16 v[44:47], v[20:23], v[52:55], v[44:47]
	v_mfma_f32_16x16x32_bf16 v[48:51], v[28:31], v[52:55], v[48:51]
	v_mfma_f32_16x16x32_bf16 v[52:55], v[16:19], v[56:59], 0
	v_mfma_f32_16x16x32_bf16 v[56:59], v[24:27], v[56:59], 0
	v_mfma_f32_16x16x32_bf16 v[52:55], v[20:23], v[60:63], v[52:55]
	v_mfma_f32_16x16x32_bf16 v[60:63], v[28:31], v[60:63], v[56:59]
	s_barrier
	s_nop 3
	ds_read_b128 v[56:59], v145 offset:16384
	ds_read_b128 v[92:95], v145 offset:17408
	ds_read_b128 v[100:103], v145 offset:18432
	ds_read_b128 v[108:111], v145 offset:19456
	ds_read_b128 v[112:115], v145 offset:20480
	ds_read_b128 v[116:119], v145 offset:21504
	ds_read_b128 v[120:123], v145 offset:22528
	ds_read_b128 v[124:127], v145 offset:23552
	s_add_i32 m0, s2, 0x10000
	s_nop 0
	global_load_lds_dwordx4 v140, s[54:55]
	s_nop 0
	s_add_i32 m0, s2, 0x12000
	s_nop 0
	global_load_lds_dwordx4 v142, s[54:55]
	s_add_u32 s54, s34, 0x80100
	s_addc_u32 s55, s35, 0
	s_add_i32 m0, s2, 0x14000
	s_nop 0
	global_load_lds_dwordx4 v140, s[54:55]
	s_nop 0
	s_add_i32 m0, s2, 0x16000
	s_nop 0
	global_load_lds_dwordx4 v142, s[54:55]
	s_nop 0
	s_add_i32 m0, s2, 0
	s_nop 0
	global_load_lds_dwordx4 v139, s[40:41]
	s_nop 0
	s_add_i32 m0, s2, 0x2000
	s_nop 0
	global_load_lds_dwordx4 v141, s[40:41]
	s_waitcnt vmcnt(8)
	s_waitcnt lgkmcnt(0)
	s_barrier
	v_mfma_f32_16x16x32_bf16 v[132:135], v[0:3], v[56:59], 0
	v_mfma_f32_16x16x32_bf16 v[152:155], v[0:3], v[100:103], 0
	v_mfma_f32_16x16x32_bf16 v[160:163], v[0:3], v[112:115], 0
	v_mfma_f32_16x16x32_bf16 v[0:3], v[0:3], v[120:123], 0
	v_mfma_f32_16x16x32_bf16 v[132:135], v[4:7], v[92:95], v[132:135]
	v_mfma_f32_16x16x32_bf16 v[152:155], v[4:7], v[108:111], v[152:155]
	v_mfma_f32_16x16x32_bf16 v[160:163], v[4:7], v[116:119], v[160:163]
	v_mfma_f32_16x16x32_bf16 v[0:3], v[4:7], v[124:127], v[0:3]
	v_mfma_f32_16x16x32_bf16 v[4:7], v[8:11], v[120:123], 0
	v_mfma_f32_16x16x32_bf16 v[148:151], v[8:11], v[56:59], 0
	v_mfma_f32_16x16x32_bf16 v[156:159], v[8:11], v[100:103], 0
	v_mfma_f32_16x16x32_bf16 v[164:167], v[8:11], v[112:115], 0
	v_mfma_f32_16x16x32_bf16 v[4:7], v[12:15], v[124:127], v[4:7]
	v_mfma_f32_16x16x32_bf16 v[148:151], v[12:15], v[92:95], v[148:151]
	v_mfma_f32_16x16x32_bf16 v[156:159], v[12:15], v[108:111], v[156:159]
	v_mfma_f32_16x16x32_bf16 v[164:167], v[12:15], v[116:119], v[164:167]
	v_mfma_f32_16x16x32_bf16 v[12:15], v[24:27], v[56:59], 0
	v_mfma_f32_16x16x32_bf16 v[168:171], v[28:31], v[92:95], v[12:15]
	v_mfma_f32_16x16x32_bf16 v[12:15], v[16:19], v[100:103], 0
	v_mfma_f32_16x16x32_bf16 v[172:175], v[20:23], v[108:111], v[12:15]
	v_mfma_f32_16x16x32_bf16 v[12:15], v[24:27], v[100:103], 0
	v_mfma_f32_16x16x32_bf16 v[176:179], v[28:31], v[108:111], v[12:15]
	v_mfma_f32_16x16x32_bf16 v[12:15], v[16:19], v[112:115], 0
	v_mfma_f32_16x16x32_bf16 v[180:183], v[20:23], v[116:119], v[12:15]
	v_mfma_f32_16x16x32_bf16 v[12:15], v[24:27], v[112:115], 0
	v_mfma_f32_16x16x32_bf16 v[8:11], v[16:19], v[56:59], 0
	v_mfma_f32_16x16x32_bf16 v[184:187], v[28:31], v[116:119], v[12:15]
	v_mfma_f32_16x16x32_bf16 v[12:15], v[16:19], v[120:123], 0
	v_mfma_f32_16x16x32_bf16 v[8:11], v[20:23], v[92:95], v[8:11]
	v_mfma_f32_16x16x32_bf16 v[188:191], v[20:23], v[124:127], v[12:15]
	v_mfma_f32_16x16x32_bf16 v[12:15], v[24:27], v[120:123], 0
	v_mfma_f32_16x16x32_bf16 v[192:195], v[28:31], v[124:127], v[12:15]
	s_barrier
	s_nop 4
	ds_read_b128 v[12:15], v146
	ds_read_b128 v[16:19], v146 offset:1024
	ds_read_b128 v[24:27], v146 offset:2048
	ds_read_b128 v[196:199], v146 offset:3072
	ds_read_b128 v[200:203], v147
	ds_read_b128 v[204:207], v147 offset:1024
	ds_read_b128 v[208:211], v147 offset:2048
	ds_read_b128 v[212:215], v147 offset:3072
	ds_read_b128 v[20:23], v145 offset:32768
	ds_read_b128 v[28:31], v145 offset:33792
	ds_read_b128 v[216:219], v145 offset:34816
	ds_read_b128 v[220:223], v145 offset:35840
	ds_read_b128 v[224:227], v145 offset:36864
	ds_read_b128 v[228:231], v145 offset:37888
	ds_read_b128 v[232:235], v145 offset:38912
	ds_read_b128 v[236:239], v145 offset:39936
	s_add_u32 s40, s30, 0x80100
	s_addc_u32 s41, s31, 0
	s_add_i32 m0, s2, 0x4000
	s_nop 0
	global_load_lds_dwordx4 v139, s[40:41]
	s_nop 0
	s_add_i32 m0, s2, 0x6000
	s_nop 0
	global_load_lds_dwordx4 v141, s[40:41]
	s_waitcnt vmcnt(8)
	s_waitcnt lgkmcnt(0)
	s_barrier
	v_mfma_f32_16x16x32_bf16 v[56:59], v[12:15], v[20:23], v[64:67]
	v_mfma_f32_16x16x32_bf16 v[116:119], v[16:19], v[28:31], v[56:59]
	v_mfma_f32_16x16x32_bf16 v[56:59], v[24:27], v[20:23], v[68:71]
	v_mfma_f32_16x16x32_bf16 v[112:115], v[196:199], v[28:31], v[56:59]
	v_mfma_f32_16x16x32_bf16 v[56:59], v[12:15], v[216:219], v[72:75]
	v_mfma_f32_16x16x32_bf16 v[108:111], v[16:19], v[220:223], v[56:59]
	v_mfma_f32_16x16x32_bf16 v[56:59], v[24:27], v[216:219], v[76:79]
	v_mfma_f32_16x16x32_bf16 v[100:103], v[196:199], v[220:223], v[56:59]
	v_mfma_f32_16x16x32_bf16 v[56:59], v[12:15], v[224:227], v[80:83]
	v_mfma_f32_16x16x32_bf16 v[92:95], v[16:19], v[228:231], v[56:59]
	v_mfma_f32_16x16x32_bf16 v[56:59], v[24:27], v[224:227], v[84:87]
	v_mfma_f32_16x16x32_bf16 v[84:87], v[196:199], v[228:231], v[56:59]
	v_mfma_f32_16x16x32_bf16 v[56:59], v[12:15], v[232:235], v[88:91]
	v_mfma_f32_16x16x32_bf16 v[72:75], v[16:19], v[236:239], v[56:59]
	v_mfma_f32_16x16x32_bf16 v[56:59], v[24:27], v[232:235], v[96:99]
	v_mfma_f32_16x16x32_bf16 v[56:59], v[196:199], v[236:239], v[56:59]
	v_mfma_f32_16x16x32_bf16 v[64:67], v[200:203], v[20:23], v[104:107]
	v_mfma_f32_16x16x32_bf16 v[20:23], v[208:211], v[20:23], v[32:35]
	v_mfma_f32_16x16x32_bf16 v[120:123], v[212:215], v[28:31], v[20:23]
	v_mfma_f32_16x16x32_bf16 v[20:23], v[200:203], v[216:219], v[36:39]
	v_mfma_f32_16x16x32_bf16 v[104:107], v[204:207], v[220:223], v[20:23]
	v_mfma_f32_16x16x32_bf16 v[20:23], v[208:211], v[216:219], v[40:43]
	v_mfma_f32_16x16x32_bf16 v[96:99], v[212:215], v[220:223], v[20:23]
	v_mfma_f32_16x16x32_bf16 v[20:23], v[200:203], v[224:227], v[44:47]
	v_mfma_f32_16x16x32_bf16 v[88:91], v[204:207], v[228:231], v[20:23]
	v_mfma_f32_16x16x32_bf16 v[20:23], v[208:211], v[224:227], v[48:51]
	v_mfma_f32_16x16x32_bf16 v[80:83], v[212:215], v[228:231], v[20:23]
	v_mfma_f32_16x16x32_bf16 v[20:23], v[200:203], v[232:235], v[52:55]
	v_mfma_f32_16x16x32_bf16 v[124:127], v[204:207], v[28:31], v[64:67]
	v_mfma_f32_16x16x32_bf16 v[64:67], v[204:207], v[236:239], v[20:23]
	v_mfma_f32_16x16x32_bf16 v[20:23], v[208:211], v[232:235], v[60:63]
	v_mfma_f32_16x16x32_bf16 v[48:51], v[212:215], v[236:239], v[20:23]
	s_barrier
	ds_read_b128 v[32:35], v145 offset:49152
	ds_read_b128 v[40:43], v145 offset:50176
	ds_read_b128 v[216:219], v145 offset:51200
	ds_read_b128 v[220:223], v145 offset:52224
	ds_read_b128 v[224:227], v145 offset:53248
	ds_read_b128 v[228:231], v145 offset:54272
	ds_read_b128 v[232:235], v145 offset:55296
	ds_read_b128 v[236:239], v145 offset:56320
	s_add_i32 m0, s2, 0x18000
	s_nop 0
	global_load_lds_dwordx4 v140, s[38:39]
	s_nop 0
	s_add_i32 m0, s2, 0x1a000
	s_nop 0
	global_load_lds_dwordx4 v142, s[38:39]
	s_add_u32 s38, s34, 0x80180
	s_addc_u32 s39, s35, 0
	s_add_i32 m0, s2, 0x1c000
	s_nop 0
	global_load_lds_dwordx4 v140, s[38:39]
	s_nop 0
	s_add_i32 m0, s2, 0x1e000
	s_nop 0
	global_load_lds_dwordx4 v142, s[38:39]
	s_nop 0
	s_add_i32 m0, s2, 0x8000
	s_nop 0
	global_load_lds_dwordx4 v139, s[36:37]
	s_nop 0
	s_add_i32 m0, s2, 0xa000
	s_nop 0
	global_load_lds_dwordx4 v141, s[36:37]
	s_waitcnt vmcnt(8)
	s_waitcnt lgkmcnt(0)
	s_barrier
	v_mfma_f32_16x16x32_bf16 v[20:23], v[12:15], v[32:35], v[132:135]
	v_mfma_f32_16x16x32_bf16 v[76:79], v[16:19], v[40:43], v[20:23]
	v_mfma_f32_16x16x32_bf16 v[20:23], v[24:27], v[32:35], v[148:151]
	v_mfma_f32_16x16x32_bf16 v[60:63], v[196:199], v[40:43], v[20:23]
	v_mfma_f32_16x16x32_bf16 v[20:23], v[12:15], v[216:219], v[152:155]
	v_mfma_f32_16x16x32_bf16 v[44:47], v[16:19], v[220:223], v[20:23]
	v_mfma_f32_16x16x32_bf16 v[20:23], v[24:27], v[216:219], v[156:159]
	v_mfma_f32_16x16x32_bf16 v[36:39], v[196:199], v[220:223], v[20:23]
	v_mfma_f32_16x16x32_bf16 v[20:23], v[12:15], v[224:227], v[160:163]
	v_mfma_f32_16x16x32_bf16 v[0:3], v[12:15], v[232:235], v[0:3]
	v_mfma_f32_16x16x32_bf16 v[28:31], v[16:19], v[228:231], v[20:23]
	v_mfma_f32_16x16x32_bf16 v[20:23], v[24:27], v[224:227], v[164:167]
	v_mfma_f32_16x16x32_bf16 v[12:15], v[16:19], v[236:239], v[0:3]
	v_mfma_f32_16x16x32_bf16 v[0:3], v[24:27], v[232:235], v[4:7]
	v_mfma_f32_16x16x32_bf16 v[20:23], v[196:199], v[228:231], v[20:23]
	v_mfma_f32_16x16x32_bf16 v[4:7], v[196:199], v[236:239], v[0:3]
	v_mfma_f32_16x16x32_bf16 v[0:3], v[200:203], v[32:35], v[8:11]
	v_mfma_f32_16x16x32_bf16 v[68:71], v[204:207], v[40:43], v[0:3]
	v_mfma_f32_16x16x32_bf16 v[0:3], v[208:211], v[32:35], v[168:171]
	v_mfma_f32_16x16x32_bf16 v[52:55], v[212:215], v[40:43], v[0:3]
	v_mfma_f32_16x16x32_bf16 v[0:3], v[200:203], v[216:219], v[172:175]
	v_mfma_f32_16x16x32_bf16 v[40:43], v[204:207], v[220:223], v[0:3]
	v_mfma_f32_16x16x32_bf16 v[0:3], v[208:211], v[216:219], v[176:179]
	v_mfma_f32_16x16x32_bf16 v[32:35], v[212:215], v[220:223], v[0:3]
	v_mfma_f32_16x16x32_bf16 v[0:3], v[200:203], v[224:227], v[180:183]
	v_mfma_f32_16x16x32_bf16 v[24:27], v[204:207], v[228:231], v[0:3]
	v_mfma_f32_16x16x32_bf16 v[0:3], v[208:211], v[224:227], v[184:187]
	v_mfma_f32_16x16x32_bf16 v[16:19], v[212:215], v[228:231], v[0:3]
	v_mfma_f32_16x16x32_bf16 v[0:3], v[200:203], v[232:235], v[188:191]
	v_mfma_f32_16x16x32_bf16 v[8:11], v[204:207], v[236:239], v[0:3]
	v_mfma_f32_16x16x32_bf16 v[0:3], v[208:211], v[232:235], v[192:195]
	v_mfma_f32_16x16x32_bf16 v[0:3], v[212:215], v[236:239], v[0:3]
	s_barrier
	s_add_u32 s53, s30, 0x200
	s_addc_u32 s54, s31, 0
	s_add_u32 s55, s34, 0x200
	s_addc_u32 s56, s35, 0
	s_add_u32 s30, s30, 0x80180
	s_addc_u32 s31, s31, 0
	s_mov_b32 s57, 0
.LBB0_1109:
	ds_read_b128 v[132:135], v143
	ds_read_b128 v[148:151], v143 offset:1024
	ds_read_b128 v[152:155], v143 offset:2048
	ds_read_b128 v[156:159], v143 offset:3072
	ds_read_b128 v[160:163], v144
	ds_read_b128 v[164:167], v144 offset:1024
	ds_read_b128 v[168:171], v144 offset:2048
	ds_read_b128 v[172:175], v144 offset:3072
	s_cmp_eq_u32 s57, 28
	s_cselect_b32 s40, s51, s53
	s_cselect_b32 s41, s23, s54
	s_cselect_b32 s36, s52, s55
	s_cselect_b32 s37, s21, s56
	s_add_u32 s34, s40, 0x80
	s_addc_u32 s35, s41, 0
	ds_read_b128 v[176:179], v145
	ds_read_b128 v[180:183], v145 offset:1024
	ds_read_b128 v[184:187], v145 offset:2048
	ds_read_b128 v[188:191], v145 offset:3072
	ds_read_b128 v[192:195], v145 offset:4096
	ds_read_b128 v[196:199], v145 offset:5120
	ds_read_b128 v[200:203], v145 offset:6144
	ds_read_b128 v[204:207], v145 offset:7168
	s_add_u32 s38, s36, 0x80
	s_addc_u32 s39, s37, 0
	s_add_i32 m0, s2, 0xc000
	s_nop 0
	global_load_lds_dwordx4 v139, s[30:31]
	s_nop 0
	s_add_i32 m0, s2, 0xe000
	s_nop 0
	global_load_lds_dwordx4 v141, s[30:31]
	s_waitcnt vmcnt(8)
	s_waitcnt lgkmcnt(0)
	s_barrier
	v_mfma_f32_16x16x32_bf16 v[116:119], v[132:135], v[176:179], v[116:119]
	v_mfma_f32_16x16x32_bf16 v[112:115], v[152:155], v[176:179], v[112:115]
	v_mfma_f32_16x16x32_bf16 v[108:111], v[132:135], v[184:187], v[108:111]
	v_mfma_f32_16x16x32_bf16 v[100:103], v[152:155], v[184:187], v[100:103]
	v_mfma_f32_16x16x32_bf16 v[92:95], v[132:135], v[192:195], v[92:95]
	v_mfma_f32_16x16x32_bf16 v[84:87], v[152:155], v[192:195], v[84:87]
	v_mfma_f32_16x16x32_bf16 v[72:75], v[132:135], v[200:203], v[72:75]
	v_mfma_f32_16x16x32_bf16 v[56:59], v[152:155], v[200:203], v[56:59]
	v_mfma_f32_16x16x32_bf16 v[116:119], v[148:151], v[180:183], v[116:119]
	v_mfma_f32_16x16x32_bf16 v[112:115], v[156:159], v[180:183], v[112:115]
	v_mfma_f32_16x16x32_bf16 v[108:111], v[148:151], v[188:191], v[108:111]
	v_mfma_f32_16x16x32_bf16 v[100:103], v[156:159], v[188:191], v[100:103]
	v_mfma_f32_16x16x32_bf16 v[92:95], v[148:151], v[196:199], v[92:95]
	v_mfma_f32_16x16x32_bf16 v[84:87], v[156:159], v[196:199], v[84:87]
	v_mfma_f32_16x16x32_bf16 v[72:75], v[148:151], v[204:207], v[72:75]
	v_mfma_f32_16x16x32_bf16 v[56:59], v[156:159], v[204:207], v[56:59]
	v_mfma_f32_16x16x32_bf16 v[124:127], v[160:163], v[176:179], v[124:127]
	v_mfma_f32_16x16x32_bf16 v[120:123], v[168:171], v[176:179], v[120:123]
	v_mfma_f32_16x16x32_bf16 v[104:107], v[160:163], v[184:187], v[104:107]
	v_mfma_f32_16x16x32_bf16 v[96:99], v[168:171], v[184:187], v[96:99]
	v_mfma_f32_16x16x32_bf16 v[88:91], v[160:163], v[192:195], v[88:91]
	v_mfma_f32_16x16x32_bf16 v[80:83], v[168:171], v[192:195], v[80:83]
	v_mfma_f32_16x16x32_bf16 v[64:67], v[160:163], v[200:203], v[64:67]
	v_mfma_f32_16x16x32_bf16 v[48:51], v[168:171], v[200:203], v[48:51]
	v_mfma_f32_16x16x32_bf16 v[124:127], v[164:167], v[180:183], v[124:127]
	v_mfma_f32_16x16x32_bf16 v[120:123], v[172:175], v[180:183], v[120:123]
	v_mfma_f32_16x16x32_bf16 v[104:107], v[164:167], v[188:191], v[104:107]
	v_mfma_f32_16x16x32_bf16 v[96:99], v[172:175], v[188:191], v[96:99]
	v_mfma_f32_16x16x32_bf16 v[88:91], v[164:167], v[196:199], v[88:91]
	v_mfma_f32_16x16x32_bf16 v[80:83], v[172:175], v[196:199], v[80:83]
	v_mfma_f32_16x16x32_bf16 v[64:67], v[164:167], v[204:207], v[64:67]
	v_mfma_f32_16x16x32_bf16 v[48:51], v[172:175], v[204:207], v[48:51]
	s_barrier
	ds_read_b128 v[176:179], v145 offset:16384
	ds_read_b128 v[180:183], v145 offset:17408
	ds_read_b128 v[184:187], v145 offset:18432
	ds_read_b128 v[188:191], v145 offset:19456
	ds_read_b128 v[192:195], v145 offset:20480
	ds_read_b128 v[196:199], v145 offset:21504
	ds_read_b128 v[200:203], v145 offset:22528
	ds_read_b128 v[204:207], v145 offset:23552
	s_add_i32 m0, s2, 0x10000
	s_nop 0
	global_load_lds_dwordx4 v140, s[36:37]
	s_nop 0
	s_add_i32 m0, s2, 0x12000
	s_nop 0
	global_load_lds_dwordx4 v142, s[36:37]
	s_add_u32 s58, s36, 0x80000
	s_addc_u32 s59, s37, 0
	s_add_i32 m0, s2, 0x14000
	s_nop 0
	global_load_lds_dwordx4 v140, s[58:59]
	s_nop 0
	s_add_i32 m0, s2, 0x16000
	s_nop 0
	global_load_lds_dwordx4 v142, s[58:59]
	s_nop 0
	s_add_i32 m0, s2, 0
	s_nop 0
	global_load_lds_dwordx4 v139, s[40:41]
	s_nop 0
	s_add_i32 m0, s2, 0x2000
	s_nop 0
	global_load_lds_dwordx4 v141, s[40:41]
	s_waitcnt vmcnt(8)
	s_waitcnt lgkmcnt(0)
	s_barrier
	v_mfma_f32_16x16x32_bf16 v[76:79], v[132:135], v[176:179], v[76:79]
	v_mfma_f32_16x16x32_bf16 v[60:63], v[152:155], v[176:179], v[60:63]
	v_mfma_f32_16x16x32_bf16 v[44:47], v[132:135], v[184:187], v[44:47]
	v_mfma_f32_16x16x32_bf16 v[36:39], v[152:155], v[184:187], v[36:39]
	v_mfma_f32_16x16x32_bf16 v[28:31], v[132:135], v[192:195], v[28:31]
	v_mfma_f32_16x16x32_bf16 v[20:23], v[152:155], v[192:195], v[20:23]
	v_mfma_f32_16x16x32_bf16 v[12:15], v[132:135], v[200:203], v[12:15]
	v_mfma_f32_16x16x32_bf16 v[4:7], v[152:155], v[200:203], v[4:7]
	v_mfma_f32_16x16x32_bf16 v[76:79], v[148:151], v[180:183], v[76:79]
	v_mfma_f32_16x16x32_bf16 v[60:63], v[156:159], v[180:183], v[60:63]
	v_mfma_f32_16x16x32_bf16 v[44:47], v[148:151], v[188:191], v[44:47]
	v_mfma_f32_16x16x32_bf16 v[36:39], v[156:159], v[188:191], v[36:39]
	v_mfma_f32_16x16x32_bf16 v[28:31], v[148:151], v[196:199], v[28:31]
	v_mfma_f32_16x16x32_bf16 v[20:23], v[156:159], v[196:199], v[20:23]
	v_mfma_f32_16x16x32_bf16 v[12:15], v[148:151], v[204:207], v[12:15]
	v_mfma_f32_16x16x32_bf16 v[4:7], v[156:159], v[204:207], v[4:7]
	v_mfma_f32_16x16x32_bf16 v[68:71], v[160:163], v[176:179], v[68:71]
	v_mfma_f32_16x16x32_bf16 v[52:55], v[168:171], v[176:179], v[52:55]
	v_mfma_f32_16x16x32_bf16 v[40:43], v[160:163], v[184:187], v[40:43]
	v_mfma_f32_16x16x32_bf16 v[32:35], v[168:171], v[184:187], v[32:35]
	v_mfma_f32_16x16x32_bf16 v[24:27], v[160:163], v[192:195], v[24:27]
	v_mfma_f32_16x16x32_bf16 v[16:19], v[168:171], v[192:195], v[16:19]
	v_mfma_f32_16x16x32_bf16 v[8:11], v[160:163], v[200:203], v[8:11]
	v_mfma_f32_16x16x32_bf16 v[0:3], v[168:171], v[200:203], v[0:3]
	v_mfma_f32_16x16x32_bf16 v[68:71], v[164:167], v[180:183], v[68:71]
	v_mfma_f32_16x16x32_bf16 v[52:55], v[172:175], v[180:183], v[52:55]
	v_mfma_f32_16x16x32_bf16 v[40:43], v[164:167], v[188:191], v[40:43]
	v_mfma_f32_16x16x32_bf16 v[32:35], v[172:175], v[188:191], v[32:35]
	v_mfma_f32_16x16x32_bf16 v[24:27], v[164:167], v[196:199], v[24:27]
	v_mfma_f32_16x16x32_bf16 v[16:19], v[172:175], v[196:199], v[16:19]
	v_mfma_f32_16x16x32_bf16 v[8:11], v[164:167], v[204:207], v[8:11]
	v_mfma_f32_16x16x32_bf16 v[0:3], v[172:175], v[204:207], v[0:3]
	s_barrier
	ds_read_b128 v[132:135], v146
	ds_read_b128 v[148:151], v146 offset:1024
	ds_read_b128 v[152:155], v146 offset:2048
	ds_read_b128 v[156:159], v146 offset:3072
	ds_read_b128 v[160:163], v147
	ds_read_b128 v[164:167], v147 offset:1024
	ds_read_b128 v[168:171], v147 offset:2048
	ds_read_b128 v[172:175], v147 offset:3072
	ds_read_b128 v[176:179], v145 offset:32768
	ds_read_b128 v[180:183], v145 offset:33792
	ds_read_b128 v[184:187], v145 offset:34816
	ds_read_b128 v[188:191], v145 offset:35840
	ds_read_b128 v[192:195], v145 offset:36864
	ds_read_b128 v[196:199], v145 offset:37888
	ds_read_b128 v[200:203], v145 offset:38912
	ds_read_b128 v[204:207], v145 offset:39936
	s_add_u32 s40, s40, 0x80000
	s_addc_u32 s41, s41, 0
	s_add_i32 m0, s2, 0x4000
	s_nop 0
	global_load_lds_dwordx4 v139, s[40:41]
	s_nop 0
	s_add_i32 m0, s2, 0x6000
	s_nop 0
	global_load_lds_dwordx4 v141, s[40:41]
	s_waitcnt vmcnt(8)
	s_waitcnt lgkmcnt(0)
	s_barrier
	v_mfma_f32_16x16x32_bf16 v[116:119], v[132:135], v[176:179], v[116:119]
	v_mfma_f32_16x16x32_bf16 v[112:115], v[152:155], v[176:179], v[112:115]
	v_mfma_f32_16x16x32_bf16 v[108:111], v[132:135], v[184:187], v[108:111]
	v_mfma_f32_16x16x32_bf16 v[100:103], v[152:155], v[184:187], v[100:103]
	v_mfma_f32_16x16x32_bf16 v[92:95], v[132:135], v[192:195], v[92:95]
	v_mfma_f32_16x16x32_bf16 v[84:87], v[152:155], v[192:195], v[84:87]
	v_mfma_f32_16x16x32_bf16 v[72:75], v[132:135], v[200:203], v[72:75]
	v_mfma_f32_16x16x32_bf16 v[56:59], v[152:155], v[200:203], v[56:59]
	v_mfma_f32_16x16x32_bf16 v[116:119], v[148:151], v[180:183], v[116:119]
	v_mfma_f32_16x16x32_bf16 v[112:115], v[156:159], v[180:183], v[112:115]
	v_mfma_f32_16x16x32_bf16 v[108:111], v[148:151], v[188:191], v[108:111]
	v_mfma_f32_16x16x32_bf16 v[100:103], v[156:159], v[188:191], v[100:103]
	v_mfma_f32_16x16x32_bf16 v[92:95], v[148:151], v[196:199], v[92:95]
	v_mfma_f32_16x16x32_bf16 v[84:87], v[156:159], v[196:199], v[84:87]
	v_mfma_f32_16x16x32_bf16 v[72:75], v[148:151], v[204:207], v[72:75]
	v_mfma_f32_16x16x32_bf16 v[56:59], v[156:159], v[204:207], v[56:59]
	v_mfma_f32_16x16x32_bf16 v[124:127], v[160:163], v[176:179], v[124:127]
	v_mfma_f32_16x16x32_bf16 v[120:123], v[168:171], v[176:179], v[120:123]
	v_mfma_f32_16x16x32_bf16 v[104:107], v[160:163], v[184:187], v[104:107]
	v_mfma_f32_16x16x32_bf16 v[96:99], v[168:171], v[184:187], v[96:99]
	v_mfma_f32_16x16x32_bf16 v[88:91], v[160:163], v[192:195], v[88:91]
	v_mfma_f32_16x16x32_bf16 v[80:83], v[168:171], v[192:195], v[80:83]
	v_mfma_f32_16x16x32_bf16 v[64:67], v[160:163], v[200:203], v[64:67]
	v_mfma_f32_16x16x32_bf16 v[48:51], v[168:171], v[200:203], v[48:51]
	v_mfma_f32_16x16x32_bf16 v[124:127], v[164:167], v[180:183], v[124:127]
	v_mfma_f32_16x16x32_bf16 v[120:123], v[172:175], v[180:183], v[120:123]
	v_mfma_f32_16x16x32_bf16 v[104:107], v[164:167], v[188:191], v[104:107]
	v_mfma_f32_16x16x32_bf16 v[96:99], v[172:175], v[188:191], v[96:99]
	v_mfma_f32_16x16x32_bf16 v[88:91], v[164:167], v[196:199], v[88:91]
	v_mfma_f32_16x16x32_bf16 v[80:83], v[172:175], v[196:199], v[80:83]
	v_mfma_f32_16x16x32_bf16 v[64:67], v[164:167], v[204:207], v[64:67]
	v_mfma_f32_16x16x32_bf16 v[48:51], v[172:175], v[204:207], v[48:51]
	s_barrier
	ds_read_b128 v[176:179], v145 offset:49152
	ds_read_b128 v[180:183], v145 offset:50176
	ds_read_b128 v[184:187], v145 offset:51200
	ds_read_b128 v[188:191], v145 offset:52224
	ds_read_b128 v[192:195], v145 offset:53248
	ds_read_b128 v[196:199], v145 offset:54272
	ds_read_b128 v[200:203], v145 offset:55296
	ds_read_b128 v[204:207], v145 offset:56320
	s_add_i32 m0, s2, 0x18000
	s_nop 0
	global_load_lds_dwordx4 v140, s[38:39]
	s_nop 0
	s_add_i32 m0, s2, 0x1a000
	s_nop 0
	global_load_lds_dwordx4 v142, s[38:39]
	s_add_u32 s36, s36, 0x80080
	s_addc_u32 s37, s37, 0
	s_add_i32 m0, s2, 0x1c000
	s_nop 0
	global_load_lds_dwordx4 v140, s[36:37]
	s_nop 0
	s_add_i32 m0, s2, 0x1e000
	s_nop 0
	global_load_lds_dwordx4 v142, s[36:37]
	s_nop 0
	s_add_i32 m0, s2, 0x8000
	s_nop 0
	global_load_lds_dwordx4 v139, s[34:35]
	s_nop 0
	s_add_i32 m0, s2, 0xa000
	s_nop 0
	global_load_lds_dwordx4 v141, s[34:35]
	s_waitcnt vmcnt(8)
	s_waitcnt lgkmcnt(0)
	s_barrier
	v_mfma_f32_16x16x32_bf16 v[76:79], v[132:135], v[176:179], v[76:79]
	v_mfma_f32_16x16x32_bf16 v[60:63], v[152:155], v[176:179], v[60:63]
	v_mfma_f32_16x16x32_bf16 v[44:47], v[132:135], v[184:187], v[44:47]
	v_mfma_f32_16x16x32_bf16 v[36:39], v[152:155], v[184:187], v[36:39]
	v_mfma_f32_16x16x32_bf16 v[28:31], v[132:135], v[192:195], v[28:31]
	v_mfma_f32_16x16x32_bf16 v[20:23], v[152:155], v[192:195], v[20:23]
	v_mfma_f32_16x16x32_bf16 v[12:15], v[132:135], v[200:203], v[12:15]
	v_mfma_f32_16x16x32_bf16 v[4:7], v[152:155], v[200:203], v[4:7]
	v_mfma_f32_16x16x32_bf16 v[76:79], v[148:151], v[180:183], v[76:79]
	v_mfma_f32_16x16x32_bf16 v[60:63], v[156:159], v[180:183], v[60:63]
	v_mfma_f32_16x16x32_bf16 v[44:47], v[148:151], v[188:191], v[44:47]
	v_mfma_f32_16x16x32_bf16 v[36:39], v[156:159], v[188:191], v[36:39]
	v_mfma_f32_16x16x32_bf16 v[28:31], v[148:151], v[196:199], v[28:31]
	v_mfma_f32_16x16x32_bf16 v[20:23], v[156:159], v[196:199], v[20:23]
	v_mfma_f32_16x16x32_bf16 v[12:15], v[148:151], v[204:207], v[12:15]
	v_mfma_f32_16x16x32_bf16 v[4:7], v[156:159], v[204:207], v[4:7]
	v_mfma_f32_16x16x32_bf16 v[68:71], v[160:163], v[176:179], v[68:71]
	v_mfma_f32_16x16x32_bf16 v[52:55], v[168:171], v[176:179], v[52:55]
	v_mfma_f32_16x16x32_bf16 v[40:43], v[160:163], v[184:187], v[40:43]
	v_mfma_f32_16x16x32_bf16 v[32:35], v[168:171], v[184:187], v[32:35]
	v_mfma_f32_16x16x32_bf16 v[24:27], v[160:163], v[192:195], v[24:27]
	v_mfma_f32_16x16x32_bf16 v[16:19], v[168:171], v[192:195], v[16:19]
	v_mfma_f32_16x16x32_bf16 v[8:11], v[160:163], v[200:203], v[8:11]
	v_mfma_f32_16x16x32_bf16 v[0:3], v[168:171], v[200:203], v[0:3]
	v_mfma_f32_16x16x32_bf16 v[68:71], v[164:167], v[180:183], v[68:71]
	v_mfma_f32_16x16x32_bf16 v[52:55], v[172:175], v[180:183], v[52:55]
	v_mfma_f32_16x16x32_bf16 v[40:43], v[164:167], v[188:191], v[40:43]
	v_mfma_f32_16x16x32_bf16 v[32:35], v[172:175], v[188:191], v[32:35]
	v_mfma_f32_16x16x32_bf16 v[24:27], v[164:167], v[196:199], v[24:27]
	v_mfma_f32_16x16x32_bf16 v[16:19], v[172:175], v[196:199], v[16:19]
	v_mfma_f32_16x16x32_bf16 v[8:11], v[164:167], v[204:207], v[8:11]
	v_mfma_f32_16x16x32_bf16 v[0:3], v[172:175], v[204:207], v[0:3]
	s_barrier
	s_add_i32 s57, s57, 2
	s_add_u32 s53, s53, 0x100
	s_addc_u32 s54, s54, 0
	s_add_u32 s55, s55, 0x100
	s_addc_u32 s56, s56, 0
	s_add_u32 s30, s30, 0x100
	s_addc_u32 s31, s31, 0
	s_cmp_gt_u32 s57, 29
	s_cbranch_scc0 .LBB0_1109
	s_and_b64 vcc, exec, s[10:11]
	s_cbranch_vccz .LBB0_1112
	s_barrier

.LBB0_1410:
	ds_read_b128 v[0:3], v138
	ds_read_b128 v[4:7], v138 offset:1024
	ds_read_b128 v[8:11], v138 offset:2048
	ds_read_b128 v[12:15], v138 offset:3072
	ds_read_b128 v[16:19], v139
	ds_read_b128 v[20:23], v139 offset:1024
	ds_read_b128 v[24:27], v139 offset:2048
	ds_read_b128 v[28:31], v139 offset:3072
	s_lshl_b64 s[20:21], s[16:17], 19
	s_add_u32 s20, s39, s20
	s_addc_u32 s21, s40, s21
	s_and_b64 s[6:7], exec, s[6:7]
	s_cselect_b32 s2, s21, s29
	s_cselect_b32 s15, s20, s28
	s_add_u32 s6, s28, 0x100
	s_addc_u32 s7, s29, 0
	s_add_u32 s36, s26, 0x100
	s_addc_u32 s37, s27, 0
	s_add_u32 s30, s28, 0x180
	s_addc_u32 s31, s29, 0
	ds_read_b128 v[32:35], v140
	ds_read_b128 v[36:39], v140 offset:1024
	ds_read_b128 v[40:43], v140 offset:2048
	ds_read_b128 v[44:47], v140 offset:3072
	ds_read_b128 v[48:51], v140 offset:4096
	ds_read_b128 v[52:55], v140 offset:5120
	ds_read_b128 v[56:59], v140 offset:6144
	ds_read_b128 v[60:63], v140 offset:7168
	s_add_u32 s34, s26, 0x180
	s_addc_u32 s35, s27, 0
	s_add_u32 s54, s28, 0x40080
	s_addc_u32 s55, s29, 0
	s_add_i32 m0, s47, 0xc000
	s_nop 0
	global_load_lds_dwordx4 v134, s[54:55]
	s_nop 0
	s_add_i32 m0, s47, 0xe000
	s_nop 0
	global_load_lds_dwordx4 v136, s[54:55]
	s_waitcnt vmcnt(8)
	s_waitcnt lgkmcnt(0)
	s_barrier
	v_mfma_f32_16x16x128_f8f6f4 v[64:67], v[0:7], v[32:39], 0
	v_mfma_f32_16x16x128_f8f6f4 v[68:71], v[8:15], v[32:39], 0
	v_mfma_f32_16x16x128_f8f6f4 v[72:75], v[0:7], v[40:47], 0
	v_mfma_f32_16x16x128_f8f6f4 v[76:79], v[8:15], v[40:47], 0
	v_mfma_f32_16x16x128_f8f6f4 v[80:83], v[0:7], v[48:55], 0
	v_mfma_f32_16x16x128_f8f6f4 v[88:91], v[8:15], v[48:55], 0
	v_mfma_f32_16x16x128_f8f6f4 v[92:95], v[0:7], v[56:63], 0
	v_mfma_f32_16x16x128_f8f6f4 v[104:107], v[8:15], v[56:63], 0
	v_mfma_f32_16x16x128_f8f6f4 v[108:111], v[16:23], v[32:39], 0
	v_mfma_f32_16x16x128_f8f6f4 v[124:127], v[24:31], v[32:39], 0
	v_mfma_f32_16x16x128_f8f6f4 v[162:165], v[16:23], v[40:47], 0
	v_mfma_f32_16x16x128_f8f6f4 v[166:169], v[24:31], v[40:47], 0
	v_mfma_f32_16x16x128_f8f6f4 v[170:173], v[16:23], v[48:55], 0
	v_mfma_f32_16x16x128_f8f6f4 v[174:177], v[24:31], v[48:55], 0
	v_mfma_f32_16x16x128_f8f6f4 v[178:181], v[16:23], v[56:63], 0
	v_mfma_f32_16x16x128_f8f6f4 v[182:185], v[24:31], v[56:63], 0
	s_barrier
	ds_read_b128 v[32:35], v140 offset:16384
	ds_read_b128 v[36:39], v140 offset:17408
	ds_read_b128 v[40:43], v140 offset:18432
	ds_read_b128 v[44:47], v140 offset:19456
	ds_read_b128 v[48:51], v140 offset:20480
	ds_read_b128 v[52:55], v140 offset:21504
	ds_read_b128 v[56:59], v140 offset:22528
	ds_read_b128 v[60:63], v140 offset:23552
	s_add_i32 m0, s47, 0x10000
	s_nop 0
	global_load_lds_dwordx4 v135, s[36:37]
	s_nop 0
	s_add_i32 m0, s47, 0x12000
	s_nop 0
	global_load_lds_dwordx4 v137, s[36:37]
	s_add_u32 s36, s26, 0x40100
	s_addc_u32 s37, s27, 0
	s_add_i32 m0, s47, 0x14000
	s_nop 0
	global_load_lds_dwordx4 v135, s[36:37]
	s_nop 0
	s_add_i32 m0, s47, 0x16000
	s_nop 0
	global_load_lds_dwordx4 v137, s[36:37]
	s_nop 0
	s_add_i32 m0, s47, 0
	s_nop 0
	global_load_lds_dwordx4 v134, s[6:7]
	s_nop 0
	s_add_i32 m0, s47, 0x2000
	s_nop 0
	global_load_lds_dwordx4 v136, s[6:7]
	s_waitcnt vmcnt(8)
	s_waitcnt lgkmcnt(0)
	s_barrier
	v_mfma_f32_16x16x128_f8f6f4 v[186:189], v[0:7], v[32:39], 0
	v_mfma_f32_16x16x128_f8f6f4 v[190:193], v[8:15], v[32:39], 0
	v_mfma_f32_16x16x128_f8f6f4 v[194:197], v[0:7], v[40:47], 0
	v_mfma_f32_16x16x128_f8f6f4 v[198:201], v[8:15], v[40:47], 0
	v_mfma_f32_16x16x128_f8f6f4 v[202:205], v[0:7], v[48:55], 0
	v_mfma_f32_16x16x128_f8f6f4 v[206:209], v[8:15], v[48:55], 0
	v_mfma_f32_16x16x128_f8f6f4 v[210:213], v[0:7], v[56:63], 0
	v_mfma_f32_16x16x128_f8f6f4 v[214:217], v[8:15], v[56:63], 0
	v_mfma_f32_16x16x128_f8f6f4 v[218:221], v[16:23], v[32:39], 0
	v_mfma_f32_16x16x128_f8f6f4 v[222:225], v[24:31], v[32:39], 0
	v_mfma_f32_16x16x128_f8f6f4 v[226:229], v[16:23], v[40:47], 0
	v_mfma_f32_16x16x128_f8f6f4 v[230:233], v[24:31], v[40:47], 0
	v_mfma_f32_16x16x128_f8f6f4 v[234:237], v[16:23], v[48:55], 0
	v_mfma_f32_16x16x128_f8f6f4 v[238:241], v[24:31], v[48:55], 0
	v_mfma_f32_16x16x128_f8f6f4 v[242:245], v[16:23], v[56:63], 0
	v_mfma_f32_16x16x128_f8f6f4 v[246:249], v[24:31], v[56:63], 0
	s_barrier
	ds_read_b128 v[0:3], v141
	ds_read_b128 v[4:7], v141 offset:1024
	ds_read_b128 v[8:11], v141 offset:2048
	ds_read_b128 v[12:15], v141 offset:3072
	ds_read_b128 v[146:149], v142
	ds_read_b128 v[150:153], v142 offset:1024
	ds_read_b128 v[154:157], v142 offset:2048
	ds_read_b128 v[158:161], v142 offset:3072
	ds_read_b128 v[16:19], v140 offset:32768
	ds_read_b128 v[20:23], v140 offset:33792
	ds_read_b128 v[24:27], v140 offset:34816
	ds_read_b128 v[28:31], v140 offset:35840
	ds_read_b128 v[32:35], v140 offset:36864
	ds_read_b128 v[36:39], v140 offset:37888
	ds_read_b128 v[40:43], v140 offset:38912
	ds_read_b128 v[44:47], v140 offset:39936
	s_add_u32 s28, s28, 0x40100
	s_addc_u32 s29, s29, 0
	s_add_i32 m0, s47, 0x4000
	s_nop 0
	global_load_lds_dwordx4 v134, s[28:29]
	s_nop 0
	s_add_i32 m0, s47, 0x6000
	s_nop 0
	global_load_lds_dwordx4 v136, s[28:29]
	s_waitcnt vmcnt(8)
	s_waitcnt lgkmcnt(0)
	s_barrier
	v_mfma_f32_16x16x128_f8f6f4 v[112:115], v[0:7], v[16:23], v[64:67]
	v_mfma_f32_16x16x128_f8f6f4 v[116:119], v[8:15], v[16:23], v[68:71]
	v_mfma_f32_16x16x128_f8f6f4 v[100:103], v[0:7], v[24:31], v[72:75]
	v_mfma_f32_16x16x128_f8f6f4 v[96:99], v[8:15], v[24:31], v[76:79]
	v_mfma_f32_16x16x128_f8f6f4 v[84:87], v[0:7], v[32:39], v[80:83]
	v_mfma_f32_16x16x128_f8f6f4 v[80:83], v[8:15], v[32:39], v[88:91]
	v_mfma_f32_16x16x128_f8f6f4 v[60:63], v[0:7], v[40:47], v[92:95]
	v_mfma_f32_16x16x128_f8f6f4 v[56:59], v[8:15], v[40:47], v[104:107]
	v_mfma_f32_16x16x128_f8f6f4 v[120:123], v[146:153], v[16:23], v[108:111]
	v_mfma_f32_16x16x128_f8f6f4 v[124:127], v[154:161], v[16:23], v[124:127]
	v_mfma_f32_16x16x128_f8f6f4 v[108:111], v[146:153], v[24:31], v[162:165]
	v_mfma_f32_16x16x128_f8f6f4 v[104:107], v[154:161], v[24:31], v[166:169]
	v_mfma_f32_16x16x128_f8f6f4 v[92:95], v[146:153], v[32:39], v[170:173]
	v_mfma_f32_16x16x128_f8f6f4 v[88:91], v[154:161], v[32:39], v[174:177]
	v_mfma_f32_16x16x128_f8f6f4 v[76:79], v[146:153], v[40:47], v[178:181]
	v_mfma_f32_16x16x128_f8f6f4 v[72:75], v[154:161], v[40:47], v[182:185]
	s_barrier
	ds_read_b128 v[24:27], v140 offset:49152
	ds_read_b128 v[28:31], v140 offset:50176
	ds_read_b128 v[162:165], v140 offset:51200
	ds_read_b128 v[166:169], v140 offset:52224
	ds_read_b128 v[170:173], v140 offset:53248
	ds_read_b128 v[174:177], v140 offset:54272
	ds_read_b128 v[178:181], v140 offset:55296
	ds_read_b128 v[182:185], v140 offset:56320
	s_add_i32 m0, s47, 0x18000
	s_nop 0
	global_load_lds_dwordx4 v135, s[34:35]
	s_nop 0
	s_add_i32 m0, s47, 0x1a000
	s_nop 0
	global_load_lds_dwordx4 v137, s[34:35]
	s_add_u32 s28, s26, 0x40180
	s_addc_u32 s29, s27, 0
	s_add_i32 m0, s47, 0x1c000
	s_nop 0
	global_load_lds_dwordx4 v135, s[28:29]
	s_nop 0
	s_add_i32 m0, s47, 0x1e000
	s_nop 0
	global_load_lds_dwordx4 v137, s[28:29]
	s_nop 0
	s_add_i32 m0, s47, 0x8000
	s_nop 0
	global_load_lds_dwordx4 v134, s[30:31]
	s_nop 0
	s_add_i32 m0, s47, 0xa000
	s_nop 0
	global_load_lds_dwordx4 v136, s[30:31]
	s_waitcnt vmcnt(8)
	s_waitcnt lgkmcnt(0)
	s_barrier
	v_mfma_f32_16x16x128_f8f6f4 v[52:55], v[0:7], v[24:31], v[186:189]
	v_mfma_f32_16x16x128_f8f6f4 v[48:51], v[8:15], v[24:31], v[190:193]
	v_mfma_f32_16x16x128_f8f6f4 v[36:39], v[0:7], v[162:169], v[194:197]
	v_mfma_f32_16x16x128_f8f6f4 v[32:35], v[8:15], v[162:169], v[198:201]
	v_mfma_f32_16x16x128_f8f6f4 v[20:23], v[0:7], v[170:177], v[202:205]
	v_mfma_f32_16x16x128_f8f6f4 v[16:19], v[8:15], v[170:177], v[206:209]
	v_mfma_f32_16x16x128_f8f6f4 v[4:7], v[0:7], v[178:185], v[210:213]
	v_mfma_f32_16x16x128_f8f6f4 v[0:3], v[8:15], v[178:185], v[214:217]
	v_mfma_f32_16x16x128_f8f6f4 v[68:71], v[146:153], v[24:31], v[218:221]
	v_mfma_f32_16x16x128_f8f6f4 v[64:67], v[154:161], v[24:31], v[222:225]
	v_mfma_f32_16x16x128_f8f6f4 v[44:47], v[146:153], v[162:169], v[226:229]
	v_mfma_f32_16x16x128_f8f6f4 v[40:43], v[154:161], v[162:169], v[230:233]
	v_mfma_f32_16x16x128_f8f6f4 v[28:31], v[146:153], v[170:177], v[234:237]
	v_mfma_f32_16x16x128_f8f6f4 v[24:27], v[154:161], v[170:177], v[238:241]
	v_mfma_f32_16x16x128_f8f6f4 v[12:15], v[146:153], v[178:185], v[242:245]
	v_mfma_f32_16x16x128_f8f6f4 v[8:11], v[154:161], v[178:185], v[246:249]
	s_barrier
	s_add_u32 s17, s26, 0x200
	s_addc_u32 s54, s27, 0
	s_mov_b32 s55, 0
.LBB0_1411:
	ds_read_b128 v[146:149], v138
	ds_read_b128 v[150:153], v138 offset:1024
	ds_read_b128 v[154:157], v138 offset:2048
	ds_read_b128 v[158:161], v138 offset:3072
	ds_read_b128 v[162:165], v139
	ds_read_b128 v[166:169], v139 offset:1024
	ds_read_b128 v[170:173], v139 offset:2048
	ds_read_b128 v[174:177], v139 offset:3072
	s_add_u32 s26, s6, 0x100
	s_addc_u32 s27, s7, 0
	s_cmp_eq_u32 s55, 12
	s_cselect_b32 s36, s15, s26
	s_cselect_b32 s37, s2, s27
	s_cselect_b32 s30, s18, s17
	s_cselect_b32 s31, s19, s54
	s_add_u32 s28, s36, 0x80
	s_addc_u32 s29, s37, 0
	ds_read_b128 v[178:181], v140
	ds_read_b128 v[182:185], v140 offset:1024
	ds_read_b128 v[186:189], v140 offset:2048
	ds_read_b128 v[190:193], v140 offset:3072
	ds_read_b128 v[194:197], v140 offset:4096
	ds_read_b128 v[198:201], v140 offset:5120
	ds_read_b128 v[202:205], v140 offset:6144
	ds_read_b128 v[206:209], v140 offset:7168
	s_add_u32 s34, s30, 0x80
	s_addc_u32 s35, s31, 0
	s_add_u32 s6, s6, 0x40080
	s_addc_u32 s7, s7, 0
	s_add_i32 m0, s47, 0xc000
	s_nop 0
	global_load_lds_dwordx4 v134, s[6:7]
	s_nop 0
	s_add_i32 m0, s47, 0xe000
	s_nop 0
	global_load_lds_dwordx4 v136, s[6:7]
	s_waitcnt vmcnt(8)
	s_waitcnt lgkmcnt(0)
	s_barrier
	v_mfma_f32_16x16x128_f8f6f4 v[112:115], v[146:153], v[178:185], v[112:115]
	v_mfma_f32_16x16x128_f8f6f4 v[116:119], v[154:161], v[178:185], v[116:119]
	v_mfma_f32_16x16x128_f8f6f4 v[100:103], v[146:153], v[186:193], v[100:103]
	v_mfma_f32_16x16x128_f8f6f4 v[96:99], v[154:161], v[186:193], v[96:99]
	v_mfma_f32_16x16x128_f8f6f4 v[210:213], v[146:153], v[194:201], v[84:87]
	v_mfma_f32_16x16x128_f8f6f4 v[214:217], v[154:161], v[194:201], v[80:83]
	v_mfma_f32_16x16x128_f8f6f4 v[218:221], v[146:153], v[202:209], v[60:63]
	v_mfma_f32_16x16x128_f8f6f4 v[222:225], v[154:161], v[202:209], v[56:59]
	v_mfma_f32_16x16x128_f8f6f4 v[120:123], v[162:169], v[178:185], v[120:123]
	v_mfma_f32_16x16x128_f8f6f4 v[124:127], v[170:177], v[178:185], v[124:127]
	v_mfma_f32_16x16x128_f8f6f4 v[108:111], v[162:169], v[186:193], v[108:111]
	v_mfma_f32_16x16x128_f8f6f4 v[104:107], v[170:177], v[186:193], v[104:107]
	v_mfma_f32_16x16x128_f8f6f4 v[178:181], v[162:169], v[194:201], v[92:95]
	v_mfma_f32_16x16x128_f8f6f4 v[182:185], v[170:177], v[194:201], v[88:91]
	v_mfma_f32_16x16x128_f8f6f4 v[186:189], v[162:169], v[202:209], v[76:79]
	v_mfma_f32_16x16x128_f8f6f4 v[190:193], v[170:177], v[202:209], v[72:75]
	s_barrier
	ds_read_b128 v[56:59], v140 offset:16384
	ds_read_b128 v[60:63], v140 offset:17408
	s_nop 2
	ds_read_b128 v[72:75], v140 offset:18432
	ds_read_b128 v[76:79], v140 offset:19456
	ds_read_b128 v[80:83], v140 offset:20480
	ds_read_b128 v[84:87], v140 offset:21504
	ds_read_b128 v[88:91], v140 offset:22528
	ds_read_b128 v[92:95], v140 offset:23552
	s_add_i32 m0, s47, 0x10000
	s_nop 0
	global_load_lds_dwordx4 v135, s[30:31]
	s_nop 0
	s_add_i32 m0, s47, 0x12000
	s_nop 0
	global_load_lds_dwordx4 v137, s[30:31]
	s_add_u32 s6, s30, 0x40000
	s_addc_u32 s7, s31, 0
	s_add_i32 m0, s47, 0x14000
	s_nop 0
	global_load_lds_dwordx4 v135, s[6:7]
	s_nop 0
	s_add_i32 m0, s47, 0x16000
	s_nop 0
	global_load_lds_dwordx4 v137, s[6:7]
	s_nop 0
	s_add_i32 m0, s47, 0
	s_nop 0
	global_load_lds_dwordx4 v134, s[36:37]
	s_nop 0
	s_add_i32 m0, s47, 0x2000
	s_nop 0
	global_load_lds_dwordx4 v136, s[36:37]
	s_waitcnt vmcnt(8)
	s_waitcnt lgkmcnt(0)
	s_barrier
	v_mfma_f32_16x16x128_f8f6f4 v[52:55], v[146:153], v[56:63], v[52:55]
	v_mfma_f32_16x16x128_f8f6f4 v[48:51], v[154:161], v[56:63], v[48:51]
	v_mfma_f32_16x16x128_f8f6f4 v[194:197], v[146:153], v[72:79], v[36:39]
	v_mfma_f32_16x16x128_f8f6f4 v[198:201], v[154:161], v[72:79], v[32:35]
	v_mfma_f32_16x16x128_f8f6f4 v[202:205], v[146:153], v[80:87], v[20:23]
	v_mfma_f32_16x16x128_f8f6f4 v[206:209], v[154:161], v[80:87], v[16:19]
	v_mfma_f32_16x16x128_f8f6f4 v[226:229], v[146:153], v[88:95], v[4:7]
	v_mfma_f32_16x16x128_f8f6f4 v[230:233], v[154:161], v[88:95], v[0:3]
	v_mfma_f32_16x16x128_f8f6f4 v[68:71], v[162:169], v[56:63], v[68:71]
	v_mfma_f32_16x16x128_f8f6f4 v[64:67], v[170:177], v[56:63], v[64:67]
	v_mfma_f32_16x16x128_f8f6f4 v[234:237], v[162:169], v[72:79], v[44:47]
	v_mfma_f32_16x16x128_f8f6f4 v[238:241], v[170:177], v[72:79], v[40:43]
	v_mfma_f32_16x16x128_f8f6f4 v[242:245], v[162:169], v[80:87], v[28:31]
	v_mfma_f32_16x16x128_f8f6f4 v[246:249], v[170:177], v[80:87], v[24:27]
	v_mfma_f32_16x16x128_f8f6f4 v[250:253], v[162:169], v[88:95], v[12:15]
	v_mfma_f32_16x16x128_f8f6f4 v[130:133], v[170:177], v[88:95], v[8:11]
	s_barrier
	ds_read_b128 v[0:3], v141
	ds_read_b128 v[4:7], v141 offset:1024
	s_nop 2
	ds_read_b128 v[8:11], v141 offset:2048
	ds_read_b128 v[12:15], v141 offset:3072
	ds_read_b128 v[146:149], v142
	ds_read_b128 v[150:153], v142 offset:1024
	ds_read_b128 v[154:157], v142 offset:2048
	ds_read_b128 v[158:161], v142 offset:3072
	ds_read_b128 v[16:19], v140 offset:32768
	ds_read_b128 v[20:23], v140 offset:33792
	ds_read_b128 v[24:27], v140 offset:34816
	ds_read_b128 v[28:31], v140 offset:35840
	ds_read_b128 v[32:35], v140 offset:36864
	ds_read_b128 v[36:39], v140 offset:37888
	ds_read_b128 v[40:43], v140 offset:38912
	ds_read_b128 v[44:47], v140 offset:39936
	s_add_u32 s6, s36, 0x40000
	s_addc_u32 s7, s37, 0
	s_add_i32 m0, s47, 0x4000
	s_nop 0
	global_load_lds_dwordx4 v134, s[6:7]
	s_nop 0
	s_add_i32 m0, s47, 0x6000
	s_nop 0
	global_load_lds_dwordx4 v136, s[6:7]
	s_waitcnt vmcnt(8)
	s_waitcnt lgkmcnt(0)
	s_barrier
	v_mfma_f32_16x16x128_f8f6f4 v[112:115], v[0:7], v[16:23], v[112:115]
	v_mfma_f32_16x16x128_f8f6f4 v[116:119], v[8:15], v[16:23], v[116:119]
	v_mfma_f32_16x16x128_f8f6f4 v[100:103], v[0:7], v[24:31], v[100:103]
	v_mfma_f32_16x16x128_f8f6f4 v[96:99], v[8:15], v[24:31], v[96:99]
	v_mfma_f32_16x16x128_f8f6f4 v[84:87], v[0:7], v[32:39], v[210:213]
	v_mfma_f32_16x16x128_f8f6f4 v[80:83], v[8:15], v[32:39], v[214:217]
	v_mfma_f32_16x16x128_f8f6f4 v[60:63], v[0:7], v[40:47], v[218:221]
	v_mfma_f32_16x16x128_f8f6f4 v[56:59], v[8:15], v[40:47], v[222:225]
	v_mfma_f32_16x16x128_f8f6f4 v[120:123], v[146:153], v[16:23], v[120:123]
	v_mfma_f32_16x16x128_f8f6f4 v[124:127], v[154:161], v[16:23], v[124:127]
	v_mfma_f32_16x16x128_f8f6f4 v[108:111], v[146:153], v[24:31], v[108:111]
	v_mfma_f32_16x16x128_f8f6f4 v[104:107], v[154:161], v[24:31], v[104:107]
	v_mfma_f32_16x16x128_f8f6f4 v[92:95], v[146:153], v[32:39], v[178:181]
	v_mfma_f32_16x16x128_f8f6f4 v[88:91], v[154:161], v[32:39], v[182:185]
	v_mfma_f32_16x16x128_f8f6f4 v[76:79], v[146:153], v[40:47], v[186:189]
	v_mfma_f32_16x16x128_f8f6f4 v[72:75], v[154:161], v[40:47], v[190:193]
	s_barrier
	ds_read_b128 v[24:27], v140 offset:49152
	ds_read_b128 v[28:31], v140 offset:50176
	ds_read_b128 v[162:165], v140 offset:51200
	ds_read_b128 v[166:169], v140 offset:52224
	ds_read_b128 v[170:173], v140 offset:53248
	ds_read_b128 v[174:177], v140 offset:54272
	ds_read_b128 v[178:181], v140 offset:55296
	ds_read_b128 v[182:185], v140 offset:56320
	s_add_i32 m0, s47, 0x18000
	s_nop 0
	global_load_lds_dwordx4 v135, s[34:35]
	s_nop 0
	s_add_i32 m0, s47, 0x1a000
	s_nop 0
	global_load_lds_dwordx4 v137, s[34:35]
	s_add_u32 s6, s30, 0x40080
	s_addc_u32 s7, s31, 0
	s_add_i32 m0, s47, 0x1c000
	s_nop 0
	global_load_lds_dwordx4 v135, s[6:7]
	s_nop 0
	s_add_i32 m0, s47, 0x1e000
	s_nop 0
	global_load_lds_dwordx4 v137, s[6:7]
	s_nop 0
	s_add_i32 m0, s47, 0x8000
	s_nop 0
	global_load_lds_dwordx4 v134, s[28:29]
	s_nop 0
	s_add_i32 m0, s47, 0xa000
	s_nop 0
	global_load_lds_dwordx4 v136, s[28:29]
	s_waitcnt vmcnt(8)
	s_waitcnt lgkmcnt(0)
	s_barrier
	v_mfma_f32_16x16x128_f8f6f4 v[52:55], v[0:7], v[24:31], v[52:55]
	v_mfma_f32_16x16x128_f8f6f4 v[48:51], v[8:15], v[24:31], v[48:51]
	v_mfma_f32_16x16x128_f8f6f4 v[36:39], v[0:7], v[162:169], v[194:197]
	v_mfma_f32_16x16x128_f8f6f4 v[32:35], v[8:15], v[162:169], v[198:201]
	v_mfma_f32_16x16x128_f8f6f4 v[20:23], v[0:7], v[170:177], v[202:205]
	v_mfma_f32_16x16x128_f8f6f4 v[16:19], v[8:15], v[170:177], v[206:209]
	v_mfma_f32_16x16x128_f8f6f4 v[4:7], v[0:7], v[178:185], v[226:229]
	v_mfma_f32_16x16x128_f8f6f4 v[0:3], v[8:15], v[178:185], v[230:233]
	v_mfma_f32_16x16x128_f8f6f4 v[68:71], v[146:153], v[24:31], v[68:71]
	v_mfma_f32_16x16x128_f8f6f4 v[64:67], v[154:161], v[24:31], v[64:67]
	v_mfma_f32_16x16x128_f8f6f4 v[44:47], v[146:153], v[162:169], v[234:237]
	v_mfma_f32_16x16x128_f8f6f4 v[40:43], v[154:161], v[162:169], v[238:241]
	v_mfma_f32_16x16x128_f8f6f4 v[28:31], v[146:153], v[170:177], v[242:245]
	v_mfma_f32_16x16x128_f8f6f4 v[24:27], v[154:161], v[170:177], v[246:249]
	v_mfma_f32_16x16x128_f8f6f4 v[12:15], v[146:153], v[178:185], v[250:253]
	v_mfma_f32_16x16x128_f8f6f4 v[8:11], v[154:161], v[178:185], v[130:133]
	s_barrier
	s_add_i32 s55, s55, 2
	s_add_u32 s17, s17, 0x100
	s_addc_u32 s54, s54, 0
	s_cmp_gt_u32 s55, 13
	s_mov_b64 s[6:7], s[26:27]
	s_cbranch_scc0 .LBB0_1411
	s_and_b64 vcc, exec, s[12:13]
	s_cbranch_vccz .LBB0_1414
	s_barrier

.LBB0_1487:
	ds_read_b128 v[0:3], v153
	ds_read_b128 v[4:7], v153 offset:1024
	ds_read_b128 v[8:11], v153 offset:2048
	ds_read_b128 v[12:15], v153 offset:3072
	ds_read_b128 v[16:19], v154
	ds_read_b128 v[20:23], v154 offset:1024
	ds_read_b128 v[24:27], v154 offset:2048
	ds_read_b128 v[28:31], v154 offset:3072
	s_add_u32 s26, s28, 0x100
	s_addc_u32 s27, s29, 0
	s_add_u32 s36, s24, 0x100
	s_addc_u32 s37, s25, 0
	s_add_u32 s30, s28, 0x180
	s_addc_u32 s31, s29, 0
	ds_read_b128 v[32:35], v155
	ds_read_b128 v[36:39], v155 offset:1024
	ds_read_b128 v[40:43], v155 offset:2048
	ds_read_b128 v[44:47], v155 offset:3072
	ds_read_b128 v[48:51], v155 offset:4096
	ds_read_b128 v[52:55], v155 offset:5120
	ds_read_b128 v[56:59], v155 offset:6144
	ds_read_b128 v[60:63], v155 offset:7168
	s_add_u32 s34, s24, 0x180
	s_addc_u32 s35, s25, 0
	s_add_u32 s52, s28, 0xe0080
	s_addc_u32 s53, s29, 0
	s_add_i32 m0, s44, 0xc000
	s_nop 0
	global_load_lds_dwordx4 v149, s[52:53]
	s_nop 0
	s_add_i32 m0, s44, 0xe000
	s_nop 0
	global_load_lds_dwordx4 v151, s[52:53]
	s_waitcnt vmcnt(8)
	s_waitcnt lgkmcnt(0)
	s_barrier
	v_mfma_f32_16x16x128_f8f6f4 v[64:67], v[0:7], v[32:39], 0
	v_mfma_f32_16x16x128_f8f6f4 v[68:71], v[8:15], v[32:39], 0
	v_mfma_f32_16x16x128_f8f6f4 v[72:75], v[0:7], v[40:47], 0
	v_mfma_f32_16x16x128_f8f6f4 v[76:79], v[8:15], v[40:47], 0
	v_mfma_f32_16x16x128_f8f6f4 v[80:83], v[0:7], v[48:55], 0
	v_mfma_f32_16x16x128_f8f6f4 v[88:91], v[8:15], v[48:55], 0
	v_mfma_f32_16x16x128_f8f6f4 v[92:95], v[0:7], v[56:63], 0
	v_mfma_f32_16x16x128_f8f6f4 v[104:107], v[8:15], v[56:63], 0
	v_mfma_f32_16x16x128_f8f6f4 v[108:111], v[16:23], v[32:39], 0
	v_mfma_f32_16x16x128_f8f6f4 v[124:127], v[24:31], v[32:39], 0
	v_mfma_f32_16x16x128_f8f6f4 v[158:161], v[16:23], v[40:47], 0
	v_mfma_f32_16x16x128_f8f6f4 v[162:165], v[24:31], v[40:47], 0
	v_mfma_f32_16x16x128_f8f6f4 v[166:169], v[16:23], v[48:55], 0
	v_mfma_f32_16x16x128_f8f6f4 v[170:173], v[24:31], v[48:55], 0
	v_mfma_f32_16x16x128_f8f6f4 v[174:177], v[16:23], v[56:63], 0
	v_mfma_f32_16x16x128_f8f6f4 v[178:181], v[24:31], v[56:63], 0
	s_barrier
	ds_read_b128 v[32:35], v155 offset:16384
	ds_read_b128 v[36:39], v155 offset:17408
	ds_read_b128 v[40:43], v155 offset:18432
	ds_read_b128 v[44:47], v155 offset:19456
	ds_read_b128 v[48:51], v155 offset:20480
	ds_read_b128 v[52:55], v155 offset:21504
	ds_read_b128 v[56:59], v155 offset:22528
	ds_read_b128 v[60:63], v155 offset:23552
	s_add_i32 m0, s44, 0x10000
	s_nop 0
	global_load_lds_dwordx4 v150, s[36:37]
	s_nop 0
	s_add_i32 m0, s44, 0x12000
	s_nop 0
	global_load_lds_dwordx4 v152, s[36:37]
	s_add_u32 s36, s24, 0xe0100
	s_addc_u32 s37, s25, 0
	s_add_i32 m0, s44, 0x14000
	s_nop 0
	global_load_lds_dwordx4 v150, s[36:37]
	s_nop 0
	s_add_i32 m0, s44, 0x16000
	s_nop 0
	global_load_lds_dwordx4 v152, s[36:37]
	s_nop 0
	s_add_i32 m0, s44, 0
	s_nop 0
	global_load_lds_dwordx4 v149, s[26:27]
	s_nop 0
	s_add_i32 m0, s44, 0x2000
	s_nop 0
	global_load_lds_dwordx4 v151, s[26:27]
	s_waitcnt vmcnt(8)
	s_waitcnt lgkmcnt(0)
	s_barrier
	v_mfma_f32_16x16x128_f8f6f4 v[190:193], v[0:7], v[32:39], 0
	v_mfma_f32_16x16x128_f8f6f4 v[194:197], v[8:15], v[32:39], 0
	v_mfma_f32_16x16x128_f8f6f4 v[198:201], v[0:7], v[40:47], 0
	v_mfma_f32_16x16x128_f8f6f4 v[202:205], v[8:15], v[40:47], 0
	v_mfma_f32_16x16x128_f8f6f4 v[206:209], v[0:7], v[48:55], 0
	v_mfma_f32_16x16x128_f8f6f4 v[210:213], v[8:15], v[48:55], 0
	v_mfma_f32_16x16x128_f8f6f4 v[214:217], v[0:7], v[56:63], 0
	v_mfma_f32_16x16x128_f8f6f4 v[218:221], v[8:15], v[56:63], 0
	v_mfma_f32_16x16x128_f8f6f4 v[222:225], v[16:23], v[32:39], 0
	v_mfma_f32_16x16x128_f8f6f4 v[226:229], v[24:31], v[32:39], 0
	v_mfma_f32_16x16x128_f8f6f4 v[230:233], v[16:23], v[40:47], 0
	v_mfma_f32_16x16x128_f8f6f4 v[234:237], v[24:31], v[40:47], 0
	v_mfma_f32_16x16x128_f8f6f4 v[238:241], v[16:23], v[48:55], 0
	v_mfma_f32_16x16x128_f8f6f4 v[242:245], v[24:31], v[48:55], 0
	v_mfma_f32_16x16x128_f8f6f4 v[246:249], v[16:23], v[56:63], 0
	v_mfma_f32_16x16x128_f8f6f4 v[250:253], v[24:31], v[56:63], 0
	s_barrier
	ds_read_b128 v[0:3], v156
	ds_read_b128 v[4:7], v156 offset:1024
	ds_read_b128 v[16:19], v156 offset:2048
	ds_read_b128 v[20:23], v156 offset:3072
	ds_read_b128 v[132:135], v157
	ds_read_b128 v[136:139], v157 offset:1024
	ds_read_b128 v[140:143], v157 offset:2048
	ds_read_b128 v[144:147], v157 offset:3072
	ds_read_b128 v[8:11], v155 offset:32768
	ds_read_b128 v[12:15], v155 offset:33792
	ds_read_b128 v[24:27], v155 offset:34816
	ds_read_b128 v[28:31], v155 offset:35840
	ds_read_b128 v[32:35], v155 offset:36864
	ds_read_b128 v[36:39], v155 offset:37888
	ds_read_b128 v[40:43], v155 offset:38912
	ds_read_b128 v[44:47], v155 offset:39936
	s_add_u32 s28, s28, 0xe0100
	s_addc_u32 s29, s29, 0
	s_add_i32 m0, s44, 0x4000
	s_nop 0
	global_load_lds_dwordx4 v149, s[28:29]
	s_nop 0
	s_add_i32 m0, s44, 0x6000
	s_nop 0
	global_load_lds_dwordx4 v151, s[28:29]
	s_waitcnt vmcnt(8)
	s_waitcnt lgkmcnt(0)
	s_barrier
	v_mfma_f32_16x16x128_f8f6f4 v[112:115], v[0:7], v[8:15], v[64:67]
	v_mfma_f32_16x16x128_f8f6f4 v[116:119], v[16:23], v[8:15], v[68:71]
	v_mfma_f32_16x16x128_f8f6f4 v[100:103], v[0:7], v[24:31], v[72:75]
	v_mfma_f32_16x16x128_f8f6f4 v[96:99], v[16:23], v[24:31], v[76:79]
	v_mfma_f32_16x16x128_f8f6f4 v[84:87], v[0:7], v[32:39], v[80:83]
	v_mfma_f32_16x16x128_f8f6f4 v[80:83], v[16:23], v[32:39], v[88:91]
	v_mfma_f32_16x16x128_f8f6f4 v[60:63], v[0:7], v[40:47], v[92:95]
	v_mfma_f32_16x16x128_f8f6f4 v[52:55], v[16:23], v[40:47], v[104:107]
	v_mfma_f32_16x16x128_f8f6f4 v[120:123], v[132:139], v[8:15], v[108:111]
	v_mfma_f32_16x16x128_f8f6f4 v[124:127], v[140:147], v[8:15], v[124:127]
	v_mfma_f32_16x16x128_f8f6f4 v[108:111], v[132:139], v[24:31], v[158:161]
	v_mfma_f32_16x16x128_f8f6f4 v[104:107], v[140:147], v[24:31], v[162:165]
	v_mfma_f32_16x16x128_f8f6f4 v[92:95], v[132:139], v[32:39], v[166:169]
	v_mfma_f32_16x16x128_f8f6f4 v[88:91], v[140:147], v[32:39], v[170:173]
	v_mfma_f32_16x16x128_f8f6f4 v[56:59], v[132:139], v[40:47], v[174:177]
	v_mfma_f32_16x16x128_f8f6f4 v[48:51], v[140:147], v[40:47], v[178:181]
	s_barrier
	ds_read_b128 v[158:161], v155 offset:49152
	ds_read_b128 v[162:165], v155 offset:50176
	ds_read_b128 v[166:169], v155 offset:51200
	ds_read_b128 v[170:173], v155 offset:52224
	ds_read_b128 v[174:177], v155 offset:53248
	ds_read_b128 v[178:181], v155 offset:54272
	ds_read_b128 v[182:185], v155 offset:55296
	ds_read_b128 v[186:189], v155 offset:56320
	s_add_i32 m0, s44, 0x18000
	s_nop 0
	global_load_lds_dwordx4 v150, s[34:35]
	s_nop 0
	s_add_i32 m0, s44, 0x1a000
	s_nop 0
	global_load_lds_dwordx4 v152, s[34:35]
	s_add_u32 s28, s24, 0xe0180
	s_addc_u32 s29, s25, 0
	s_add_i32 m0, s44, 0x1c000
	s_nop 0
	global_load_lds_dwordx4 v150, s[28:29]
	s_nop 0
	s_add_i32 m0, s44, 0x1e000
	s_nop 0
	global_load_lds_dwordx4 v152, s[28:29]
	s_nop 0
	s_add_i32 m0, s44, 0x8000
	s_nop 0
	global_load_lds_dwordx4 v149, s[30:31]
	s_nop 0
	s_add_i32 m0, s44, 0xa000
	s_nop 0
	global_load_lds_dwordx4 v151, s[30:31]
	s_waitcnt vmcnt(8)
	s_waitcnt lgkmcnt(0)
	s_barrier
	v_mfma_f32_16x16x128_f8f6f4 v[68:71], v[0:7], v[158:165], v[190:193]
	v_mfma_f32_16x16x128_f8f6f4 v[64:67], v[16:23], v[158:165], v[194:197]
	v_mfma_f32_16x16x128_f8f6f4 v[44:47], v[0:7], v[166:173], v[198:201]
	v_mfma_f32_16x16x128_f8f6f4 v[36:39], v[16:23], v[166:173], v[202:205]
	v_mfma_f32_16x16x128_f8f6f4 v[28:31], v[0:7], v[174:181], v[206:209]
	v_mfma_f32_16x16x128_f8f6f4 v[24:27], v[16:23], v[174:181], v[210:213]
	v_mfma_f32_16x16x128_f8f6f4 v[12:15], v[0:7], v[182:189], v[214:217]
	v_mfma_f32_16x16x128_f8f6f4 v[8:11], v[16:23], v[182:189], v[218:221]
	v_mfma_f32_16x16x128_f8f6f4 v[76:79], v[132:139], v[158:165], v[222:225]
	v_mfma_f32_16x16x128_f8f6f4 v[72:75], v[140:147], v[158:165], v[226:229]
	v_mfma_f32_16x16x128_f8f6f4 v[40:43], v[132:139], v[166:173], v[230:233]
	v_mfma_f32_16x16x128_f8f6f4 v[32:35], v[140:147], v[166:173], v[234:237]
	v_mfma_f32_16x16x128_f8f6f4 v[20:23], v[132:139], v[174:181], v[238:241]
	v_mfma_f32_16x16x128_f8f6f4 v[16:19], v[140:147], v[174:181], v[242:245]
	v_mfma_f32_16x16x128_f8f6f4 v[4:7], v[132:139], v[182:189], v[246:249]
	v_mfma_f32_16x16x128_f8f6f4 v[0:3], v[140:147], v[182:189], v[250:253]
	s_barrier
	s_add_u32 s23, s24, 0x200
	s_addc_u32 s51, s25, 0
	s_mov_b32 s52, 0
.LBB0_1488:
	ds_read_b128 v[132:135], v153
	ds_read_b128 v[136:139], v153 offset:1024
	ds_read_b128 v[140:143], v153 offset:2048
	ds_read_b128 v[144:147], v153 offset:3072
	ds_read_b128 v[158:161], v154
	ds_read_b128 v[162:165], v154 offset:1024
	ds_read_b128 v[166:169], v154 offset:2048
	ds_read_b128 v[170:173], v154 offset:3072
	s_add_u32 s24, s26, 0x100
	s_addc_u32 s25, s27, 0
	s_cmp_eq_u32 s52, 52
	s_cselect_b32 s36, s6, s24
	s_cselect_b32 s37, s7, s25
	s_cselect_b32 s30, s20, s23
	s_cselect_b32 s31, s21, s51
	s_add_u32 s28, s36, 0x80
	s_addc_u32 s29, s37, 0
	ds_read_b128 v[174:177], v155
	ds_read_b128 v[178:181], v155 offset:1024
	ds_read_b128 v[182:185], v155 offset:2048
	ds_read_b128 v[186:189], v155 offset:3072
	ds_read_b128 v[190:193], v155 offset:4096
	ds_read_b128 v[194:197], v155 offset:5120
	ds_read_b128 v[198:201], v155 offset:6144
	ds_read_b128 v[202:205], v155 offset:7168
	s_add_u32 s34, s30, 0x80
	s_addc_u32 s35, s31, 0
	s_add_u32 s26, s26, 0xe0080
	s_addc_u32 s27, s27, 0
	s_add_i32 m0, s44, 0xc000
	s_nop 0
	global_load_lds_dwordx4 v149, s[26:27]
	s_nop 0
	s_add_i32 m0, s44, 0xe000
	s_nop 0
	global_load_lds_dwordx4 v151, s[26:27]
	s_waitcnt vmcnt(8)
	s_waitcnt lgkmcnt(0)
	s_barrier
	v_mfma_f32_16x16x128_f8f6f4 v[112:115], v[132:139], v[174:181], v[112:115]
	v_mfma_f32_16x16x128_f8f6f4 v[116:119], v[140:147], v[174:181], v[116:119]
	v_mfma_f32_16x16x128_f8f6f4 v[100:103], v[132:139], v[182:189], v[100:103]
	v_mfma_f32_16x16x128_f8f6f4 v[96:99], v[140:147], v[182:189], v[96:99]
	v_mfma_f32_16x16x128_f8f6f4 v[206:209], v[132:139], v[190:197], v[84:87]
	v_mfma_f32_16x16x128_f8f6f4 v[210:213], v[140:147], v[190:197], v[80:83]
	v_mfma_f32_16x16x128_f8f6f4 v[214:217], v[132:139], v[198:205], v[60:63]
	v_mfma_f32_16x16x128_f8f6f4 v[218:221], v[140:147], v[198:205], v[52:55]
	v_mfma_f32_16x16x128_f8f6f4 v[120:123], v[158:165], v[174:181], v[120:123]
	v_mfma_f32_16x16x128_f8f6f4 v[124:127], v[166:173], v[174:181], v[124:127]
	v_mfma_f32_16x16x128_f8f6f4 v[108:111], v[158:165], v[182:189], v[108:111]
	v_mfma_f32_16x16x128_f8f6f4 v[104:107], v[166:173], v[182:189], v[104:107]
	v_mfma_f32_16x16x128_f8f6f4 v[174:177], v[158:165], v[190:197], v[92:95]
	v_mfma_f32_16x16x128_f8f6f4 v[178:181], v[166:173], v[190:197], v[88:91]
	v_mfma_f32_16x16x128_f8f6f4 v[182:185], v[158:165], v[198:205], v[56:59]
	v_mfma_f32_16x16x128_f8f6f4 v[186:189], v[166:173], v[198:205], v[48:51]
	s_barrier
	s_nop 4
	ds_read_b128 v[48:51], v155 offset:16384
	ds_read_b128 v[52:55], v155 offset:17408
	ds_read_b128 v[56:59], v155 offset:18432
	ds_read_b128 v[60:63], v155 offset:19456
	ds_read_b128 v[80:83], v155 offset:20480
	ds_read_b128 v[84:87], v155 offset:21504
	ds_read_b128 v[88:91], v155 offset:22528
	ds_read_b128 v[92:95], v155 offset:23552
	s_add_i32 m0, s44, 0x10000
	s_nop 0
	global_load_lds_dwordx4 v150, s[30:31]
	s_nop 0
	s_add_i32 m0, s44, 0x12000
	s_nop 0
	global_load_lds_dwordx4 v152, s[30:31]
	s_add_u32 s26, s30, 0xe0000
	s_addc_u32 s27, s31, 0
	s_add_i32 m0, s44, 0x14000
	s_nop 0
	global_load_lds_dwordx4 v150, s[26:27]
	s_nop 0
	s_add_i32 m0, s44, 0x16000
	s_nop 0
	global_load_lds_dwordx4 v152, s[26:27]
	s_nop 0
	s_add_i32 m0, s44, 0
	s_nop 0
	global_load_lds_dwordx4 v149, s[36:37]
	s_nop 0
	s_add_i32 m0, s44, 0x2000
	s_nop 0
	global_load_lds_dwordx4 v151, s[36:37]
	s_waitcnt vmcnt(8)
	s_waitcnt lgkmcnt(0)
	s_barrier
	v_mfma_f32_16x16x128_f8f6f4 v[68:71], v[132:139], v[48:55], v[68:71]
	v_mfma_f32_16x16x128_f8f6f4 v[64:67], v[140:147], v[48:55], v[64:67]
	v_mfma_f32_16x16x128_f8f6f4 v[190:193], v[132:139], v[56:63], v[44:47]
	v_mfma_f32_16x16x128_f8f6f4 v[194:197], v[140:147], v[56:63], v[36:39]
	v_mfma_f32_16x16x128_f8f6f4 v[198:201], v[132:139], v[80:87], v[28:31]
	v_mfma_f32_16x16x128_f8f6f4 v[202:205], v[140:147], v[80:87], v[24:27]
	v_mfma_f32_16x16x128_f8f6f4 v[222:225], v[132:139], v[88:95], v[12:15]
	v_mfma_f32_16x16x128_f8f6f4 v[226:229], v[140:147], v[88:95], v[8:11]
	v_mfma_f32_16x16x128_f8f6f4 v[76:79], v[158:165], v[48:55], v[76:79]
	v_mfma_f32_16x16x128_f8f6f4 v[72:75], v[166:173], v[48:55], v[72:75]
	v_mfma_f32_16x16x128_f8f6f4 v[230:233], v[158:165], v[56:63], v[40:43]
	v_mfma_f32_16x16x128_f8f6f4 v[234:237], v[166:173], v[56:63], v[32:35]
	v_mfma_f32_16x16x128_f8f6f4 v[238:241], v[158:165], v[80:87], v[20:23]
	v_mfma_f32_16x16x128_f8f6f4 v[242:245], v[166:173], v[80:87], v[16:19]
	v_mfma_f32_16x16x128_f8f6f4 v[246:249], v[158:165], v[88:95], v[4:7]
	v_mfma_f32_16x16x128_f8f6f4 v[250:253], v[166:173], v[88:95], v[0:3]
	s_barrier
	s_nop 4
	ds_read_b128 v[0:3], v156
	ds_read_b128 v[4:7], v156 offset:1024
	ds_read_b128 v[16:19], v156 offset:2048
	ds_read_b128 v[20:23], v156 offset:3072
	ds_read_b128 v[132:135], v157
	ds_read_b128 v[136:139], v157 offset:1024
	ds_read_b128 v[140:143], v157 offset:2048
	ds_read_b128 v[144:147], v157 offset:3072
	ds_read_b128 v[8:11], v155 offset:32768
	ds_read_b128 v[12:15], v155 offset:33792
	ds_read_b128 v[24:27], v155 offset:34816
	ds_read_b128 v[28:31], v155 offset:35840
	ds_read_b128 v[32:35], v155 offset:36864
	ds_read_b128 v[36:39], v155 offset:37888
	ds_read_b128 v[40:43], v155 offset:38912
	ds_read_b128 v[44:47], v155 offset:39936
	s_add_u32 s26, s36, 0xe0000
	s_addc_u32 s27, s37, 0
	s_add_i32 m0, s44, 0x4000
	s_nop 0
	global_load_lds_dwordx4 v149, s[26:27]
	s_nop 0
	s_add_i32 m0, s44, 0x6000
	s_nop 0
	global_load_lds_dwordx4 v151, s[26:27]
	s_waitcnt vmcnt(8)
	s_waitcnt lgkmcnt(0)
	s_barrier
	v_mfma_f32_16x16x128_f8f6f4 v[112:115], v[0:7], v[8:15], v[112:115]
	v_mfma_f32_16x16x128_f8f6f4 v[116:119], v[16:23], v[8:15], v[116:119]
	v_mfma_f32_16x16x128_f8f6f4 v[100:103], v[0:7], v[24:31], v[100:103]
	v_mfma_f32_16x16x128_f8f6f4 v[96:99], v[16:23], v[24:31], v[96:99]
	v_mfma_f32_16x16x128_f8f6f4 v[84:87], v[0:7], v[32:39], v[206:209]
	v_mfma_f32_16x16x128_f8f6f4 v[80:83], v[16:23], v[32:39], v[210:213]
	v_mfma_f32_16x16x128_f8f6f4 v[60:63], v[0:7], v[40:47], v[214:217]
	v_mfma_f32_16x16x128_f8f6f4 v[52:55], v[16:23], v[40:47], v[218:221]
	v_mfma_f32_16x16x128_f8f6f4 v[120:123], v[132:139], v[8:15], v[120:123]
	v_mfma_f32_16x16x128_f8f6f4 v[124:127], v[140:147], v[8:15], v[124:127]
	v_mfma_f32_16x16x128_f8f6f4 v[108:111], v[132:139], v[24:31], v[108:111]
	v_mfma_f32_16x16x128_f8f6f4 v[104:107], v[140:147], v[24:31], v[104:107]
	v_mfma_f32_16x16x128_f8f6f4 v[92:95], v[132:139], v[32:39], v[174:177]
	v_mfma_f32_16x16x128_f8f6f4 v[88:91], v[140:147], v[32:39], v[178:181]
	v_mfma_f32_16x16x128_f8f6f4 v[56:59], v[132:139], v[40:47], v[182:185]
	v_mfma_f32_16x16x128_f8f6f4 v[48:51], v[140:147], v[40:47], v[186:189]
	s_barrier
	ds_read_b128 v[158:161], v155 offset:49152
	ds_read_b128 v[162:165], v155 offset:50176
	ds_read_b128 v[166:169], v155 offset:51200
	ds_read_b128 v[170:173], v155 offset:52224
	ds_read_b128 v[174:177], v155 offset:53248
	ds_read_b128 v[178:181], v155 offset:54272
	ds_read_b128 v[182:185], v155 offset:55296
	ds_read_b128 v[186:189], v155 offset:56320
	s_add_i32 m0, s44, 0x18000
	s_nop 0
	global_load_lds_dwordx4 v150, s[34:35]
	s_nop 0
	s_add_i32 m0, s44, 0x1a000
	s_nop 0
	global_load_lds_dwordx4 v152, s[34:35]
	s_add_u32 s26, s30, 0xe0080
	s_addc_u32 s27, s31, 0
	s_add_i32 m0, s44, 0x1c000
	s_nop 0
	global_load_lds_dwordx4 v150, s[26:27]
	s_nop 0
	s_add_i32 m0, s44, 0x1e000
	s_nop 0
	global_load_lds_dwordx4 v152, s[26:27]
	s_nop 0
	s_add_i32 m0, s44, 0x8000
	s_nop 0
	global_load_lds_dwordx4 v149, s[28:29]
	s_nop 0
	s_add_i32 m0, s44, 0xa000
	s_nop 0
	global_load_lds_dwordx4 v151, s[28:29]
	s_waitcnt vmcnt(8)
	s_waitcnt lgkmcnt(0)
	s_barrier
	v_mfma_f32_16x16x128_f8f6f4 v[68:71], v[0:7], v[158:165], v[68:71]
	v_mfma_f32_16x16x128_f8f6f4 v[64:67], v[16:23], v[158:165], v[64:67]
	v_mfma_f32_16x16x128_f8f6f4 v[44:47], v[0:7], v[166:173], v[190:193]
	v_mfma_f32_16x16x128_f8f6f4 v[36:39], v[16:23], v[166:173], v[194:197]
	v_mfma_f32_16x16x128_f8f6f4 v[28:31], v[0:7], v[174:181], v[198:201]
	v_mfma_f32_16x16x128_f8f6f4 v[24:27], v[16:23], v[174:181], v[202:205]
	v_mfma_f32_16x16x128_f8f6f4 v[12:15], v[0:7], v[182:189], v[222:225]
	v_mfma_f32_16x16x128_f8f6f4 v[8:11], v[16:23], v[182:189], v[226:229]
	v_mfma_f32_16x16x128_f8f6f4 v[76:79], v[132:139], v[158:165], v[76:79]
	v_mfma_f32_16x16x128_f8f6f4 v[72:75], v[140:147], v[158:165], v[72:75]
	v_mfma_f32_16x16x128_f8f6f4 v[40:43], v[132:139], v[166:173], v[230:233]
	v_mfma_f32_16x16x128_f8f6f4 v[32:35], v[140:147], v[166:173], v[234:237]
	v_mfma_f32_16x16x128_f8f6f4 v[20:23], v[132:139], v[174:181], v[238:241]
	v_mfma_f32_16x16x128_f8f6f4 v[16:19], v[140:147], v[174:181], v[242:245]
	v_mfma_f32_16x16x128_f8f6f4 v[4:7], v[132:139], v[182:189], v[246:249]
	v_mfma_f32_16x16x128_f8f6f4 v[0:3], v[140:147], v[182:189], v[250:253]
	s_barrier
	s_add_i32 s52, s52, 2
	s_add_u32 s23, s23, 0x100
	s_addc_u32 s51, s51, 0
	s_cmp_gt_u32 s52, 53
	s_mov_b64 s[26:27], s[24:25]
	s_cbranch_scc0 .LBB0_1488
	s_and_b64 vcc, exec, s[16:17]
	s_cbranch_vccz .LBB0_1491
	s_barrier
